# plus: batched row loads in P0 w_in conversion items and remaining P3 conversion variants; batched ss loads in EpiVT epilogues
# speedup vs baseline: 1.0185x; 1.0036x over previous
; #define GAS __attribute__((address_space(1)))
;     ...
;     for (int i = 0; i < 16; ++i) { const int kk = 4 * i + kq;
;         f32x4 v = __builtin_nontemporal_load((const GAS f32x4*)(W + (size_t)(k0 + kk) * ldw + n0 + 4 * c4));
;         v = v * (gk ? gk[k0 + kk] * scale : scale);
.LBB0_21:
	s_mov_b32 s100, 0x30000
	s_mov_b32 s101, 0
	s_andn2_b64 vcc, exec, s[6:7]
	s_cbranch_vccnz .Lconv_nogain_p0f8
	v_lshl_add_u64 v[196:197], s[14:15], 0, v[34:35]
	global_load_dword v164, v[196:197], off
	global_load_dword v166, v[196:197], off offset:16
	global_load_dword v168, v[196:197], off offset:32
	global_load_dword v170, v[196:197], off offset:48
	global_load_dword v172, v[196:197], off offset:64
	global_load_dword v174, v[196:197], off offset:80
	global_load_dword v176, v[196:197], off offset:96
	global_load_dword v178, v[196:197], off offset:112
	global_load_dword v180, v[196:197], off offset:128
	global_load_dword v182, v[196:197], off offset:144
	global_load_dword v184, v[196:197], off offset:160
	global_load_dword v186, v[196:197], off offset:176
	global_load_dword v188, v[196:197], off offset:192
	global_load_dword v190, v[196:197], off offset:208
	global_load_dword v192, v[196:197], off offset:224
	global_load_dword v194, v[196:197], off offset:240
	s_branch .Lconv_gdone_p0f8

; #define GAS __attribute__((address_space(1)))
; #define LAS __attribute__((address_space(3)))
;     ...
;     for (int i = 0; i < 16; ++i) { const int kk = 4 * i + kq;
;         f32x4 v = __builtin_nontemporal_load((const GAS f32x4*)(W + (size_t)(k0 + kk) * ldw + n0 + 4 * c4));
;         v = v * (gk ? gk[k0 + kk] * scale : scale);
;         LAS float* d = scr + kk * 65 + 4 * c4; d[0] = v[0]; d[1] = v[1]; d[2] = v[2]; d[3] = v[3]; }
.Lconv_gdone_p0f8:
	global_load_dwordx4 v[100:103], v[32:33], off nt
	v_lshl_add_u64 v[32:33], v[32:33], 0, s[100:101]
	global_load_dwordx4 v[104:107], v[32:33], off nt
	v_lshl_add_u64 v[32:33], v[32:33], 0, s[100:101]
	global_load_dwordx4 v[108:111], v[32:33], off nt
	v_lshl_add_u64 v[32:33], v[32:33], 0, s[100:101]
	global_load_dwordx4 v[112:115], v[32:33], off nt
	v_lshl_add_u64 v[32:33], v[32:33], 0, s[100:101]
	global_load_dwordx4 v[116:119], v[32:33], off nt
	v_lshl_add_u64 v[32:33], v[32:33], 0, s[100:101]
	global_load_dwordx4 v[120:123], v[32:33], off nt
	v_lshl_add_u64 v[32:33], v[32:33], 0, s[100:101]
	global_load_dwordx4 v[124:127], v[32:33], off nt
	v_lshl_add_u64 v[32:33], v[32:33], 0, s[100:101]
	global_load_dwordx4 v[128:131], v[32:33], off nt
	v_lshl_add_u64 v[32:33], v[32:33], 0, s[100:101]
	global_load_dwordx4 v[132:135], v[32:33], off nt
	v_lshl_add_u64 v[32:33], v[32:33], 0, s[100:101]
	global_load_dwordx4 v[136:139], v[32:33], off nt
	v_lshl_add_u64 v[32:33], v[32:33], 0, s[100:101]
	global_load_dwordx4 v[140:143], v[32:33], off nt
	v_lshl_add_u64 v[32:33], v[32:33], 0, s[100:101]
	global_load_dwordx4 v[144:147], v[32:33], off nt
	v_lshl_add_u64 v[32:33], v[32:33], 0, s[100:101]
	global_load_dwordx4 v[148:151], v[32:33], off nt
	v_lshl_add_u64 v[32:33], v[32:33], 0, s[100:101]
	global_load_dwordx4 v[152:155], v[32:33], off nt
	v_lshl_add_u64 v[32:33], v[32:33], 0, s[100:101]
	global_load_dwordx4 v[156:159], v[32:33], off nt
	v_lshl_add_u64 v[32:33], v[32:33], 0, s[100:101]
	global_load_dwordx4 v[160:163], v[32:33], off nt
	s_waitcnt vmcnt(15)
	v_mul_f32_e32 v164, 0x42800000, v164
	v_pk_mul_f32 v[100:101], v[100:101], v[164:165] op_sel_hi:[1,0]
	v_pk_mul_f32 v[102:103], v[102:103], v[164:165] op_sel_hi:[1,0]
	ds_write2_b32 v54, v100, v101 offset1:1
	ds_write2_b32 v54, v102, v103 offset0:2 offset1:3
	s_waitcnt vmcnt(14)
	v_mul_f32_e32 v166, 0x42800000, v166
	v_pk_mul_f32 v[104:105], v[104:105], v[166:167] op_sel_hi:[1,0]
	v_pk_mul_f32 v[106:107], v[106:107], v[166:167] op_sel_hi:[1,0]
	v_add_u32_e32 v196, 0x410, v54
	ds_write2_b32 v196, v104, v105 offset1:1
	ds_write2_b32 v196, v106, v107 offset0:2 offset1:3
	s_waitcnt vmcnt(13)
	v_mul_f32_e32 v168, 0x42800000, v168
	v_pk_mul_f32 v[108:109], v[108:109], v[168:169] op_sel_hi:[1,0]
	v_pk_mul_f32 v[110:111], v[110:111], v[168:169] op_sel_hi:[1,0]
	v_add_u32_e32 v196, 0x820, v54
	ds_write2_b32 v196, v108, v109 offset1:1
	ds_write2_b32 v196, v110, v111 offset0:2 offset1:3
	s_waitcnt vmcnt(12)
	v_mul_f32_e32 v170, 0x42800000, v170
	v_pk_mul_f32 v[112:113], v[112:113], v[170:171] op_sel_hi:[1,0]
	v_pk_mul_f32 v[114:115], v[114:115], v[170:171] op_sel_hi:[1,0]
	v_add_u32_e32 v196, 0xc30, v54
	ds_write2_b32 v196, v112, v113 offset1:1
	ds_write2_b32 v196, v114, v115 offset0:2 offset1:3
	s_waitcnt vmcnt(11)
	v_mul_f32_e32 v172, 0x42800000, v172
	v_pk_mul_f32 v[116:117], v[116:117], v[172:173] op_sel_hi:[1,0]
	v_pk_mul_f32 v[118:119], v[118:119], v[172:173] op_sel_hi:[1,0]
	v_add_u32_e32 v196, 0x1040, v54
	ds_write2_b32 v196, v116, v117 offset1:1
	ds_write2_b32 v196, v118, v119 offset0:2 offset1:3
	s_waitcnt vmcnt(10)
	v_mul_f32_e32 v174, 0x42800000, v174
	v_pk_mul_f32 v[120:121], v[120:121], v[174:175] op_sel_hi:[1,0]
	v_pk_mul_f32 v[122:123], v[122:123], v[174:175] op_sel_hi:[1,0]
	v_add_u32_e32 v196, 0x1450, v54
	ds_write2_b32 v196, v120, v121 offset1:1
	ds_write2_b32 v196, v122, v123 offset0:2 offset1:3
	s_waitcnt vmcnt(9)
	v_mul_f32_e32 v176, 0x42800000, v176
	v_pk_mul_f32 v[124:125], v[124:125], v[176:177] op_sel_hi:[1,0]
	v_pk_mul_f32 v[126:127], v[126:127], v[176:177] op_sel_hi:[1,0]
	v_add_u32_e32 v196, 0x1860, v54
	ds_write2_b32 v196, v124, v125 offset1:1
	ds_write2_b32 v196, v126, v127 offset0:2 offset1:3
	s_waitcnt vmcnt(8)
	v_mul_f32_e32 v178, 0x42800000, v178
	v_pk_mul_f32 v[128:129], v[128:129], v[178:179] op_sel_hi:[1,0]
	v_pk_mul_f32 v[130:131], v[130:131], v[178:179] op_sel_hi:[1,0]
	v_add_u32_e32 v196, 0x1c70, v54
	ds_write2_b32 v196, v128, v129 offset1:1
	ds_write2_b32 v196, v130, v131 offset0:2 offset1:3
	s_waitcnt vmcnt(7)
	v_mul_f32_e32 v180, 0x42800000, v180
	v_pk_mul_f32 v[132:133], v[132:133], v[180:181] op_sel_hi:[1,0]
	v_pk_mul_f32 v[134:135], v[134:135], v[180:181] op_sel_hi:[1,0]
	v_add_u32_e32 v196, 0x2080, v54
	ds_write2_b32 v196, v132, v133 offset1:1
	ds_write2_b32 v196, v134, v135 offset0:2 offset1:3
	s_waitcnt vmcnt(6)
	v_mul_f32_e32 v182, 0x42800000, v182
	v_pk_mul_f32 v[136:137], v[136:137], v[182:183] op_sel_hi:[1,0]
	v_pk_mul_f32 v[138:139], v[138:139], v[182:183] op_sel_hi:[1,0]
	v_add_u32_e32 v196, 0x2490, v54
	ds_write2_b32 v196, v136, v137 offset1:1
	ds_write2_b32 v196, v138, v139 offset0:2 offset1:3
	s_waitcnt vmcnt(5)
	v_mul_f32_e32 v184, 0x42800000, v184
	v_pk_mul_f32 v[140:141], v[140:141], v[184:185] op_sel_hi:[1,0]
	v_pk_mul_f32 v[142:143], v[142:143], v[184:185] op_sel_hi:[1,0]
	v_add_u32_e32 v196, 0x28a0, v54
	ds_write2_b32 v196, v140, v141 offset1:1
	ds_write2_b32 v196, v142, v143 offset0:2 offset1:3
	s_waitcnt vmcnt(4)
	v_mul_f32_e32 v186, 0x42800000, v186
	v_pk_mul_f32 v[144:145], v[144:145], v[186:187] op_sel_hi:[1,0]
	v_pk_mul_f32 v[146:147], v[146:147], v[186:187] op_sel_hi:[1,0]
	v_add_u32_e32 v196, 0x2cb0, v54
	ds_write2_b32 v196, v144, v145 offset1:1
	ds_write2_b32 v196, v146, v147 offset0:2 offset1:3
	s_waitcnt vmcnt(3)
	v_mul_f32_e32 v188, 0x42800000, v188
	v_pk_mul_f32 v[148:149], v[148:149], v[188:189] op_sel_hi:[1,0]
	v_pk_mul_f32 v[150:151], v[150:151], v[188:189] op_sel_hi:[1,0]
	v_add_u32_e32 v196, 0x30c0, v54
	ds_write2_b32 v196, v148, v149 offset1:1
	ds_write2_b32 v196, v150, v151 offset0:2 offset1:3
	s_waitcnt vmcnt(2)
	v_mul_f32_e32 v190, 0x42800000, v190
	v_pk_mul_f32 v[152:153], v[152:153], v[190:191] op_sel_hi:[1,0]
	v_pk_mul_f32 v[154:155], v[154:155], v[190:191] op_sel_hi:[1,0]
	v_add_u32_e32 v196, 0x34d0, v54
	ds_write2_b32 v196, v152, v153 offset1:1
	ds_write2_b32 v196, v154, v155 offset0:2 offset1:3
	s_waitcnt vmcnt(1)
	v_mul_f32_e32 v192, 0x42800000, v192
	v_pk_mul_f32 v[156:157], v[156:157], v[192:193] op_sel_hi:[1,0]
	v_pk_mul_f32 v[158:159], v[158:159], v[192:193] op_sel_hi:[1,0]
	v_add_u32_e32 v196, 0x38e0, v54
	ds_write2_b32 v196, v156, v157 offset1:1
	ds_write2_b32 v196, v158, v159 offset0:2 offset1:3
	s_waitcnt vmcnt(0)
	v_mul_f32_e32 v194, 0x42800000, v194
	v_pk_mul_f32 v[160:161], v[160:161], v[194:195] op_sel_hi:[1,0]
	v_pk_mul_f32 v[162:163], v[162:163], v[194:195] op_sel_hi:[1,0]
	v_add_u32_e32 v196, 0x3cf0, v54
	ds_write2_b32 v196, v160, v161 offset1:1
	ds_write2_b32 v196, v162, v163 offset0:2 offset1:3

; #define GAS __attribute__((address_space(1)))
;     const int nblk = N / 64, kb = item / nblk, nb = item - kb * nblk, k0 = 64 * kb, n0 = 64 * nb; if (ldw == 0) ldw = N;
;     const int c4 = lane & 15, kq = lane >> 4;
; #pragma unroll 4
;     for (int i = 0; i < 16; ++i) { const int kk = 4 * i + kq;
;         f32x4 v = __builtin_nontemporal_load((const GAS f32x4*)(W + (size_t)(k0 + kk) * ldw + n0 + 4 * c4));
;         if (gk) v = v * gk[k0 + kk];
.LBB0_33:
	v_mad_i64_i32 v[198:199], s[0:1], v12, s17, v[24:25]
	s_lshl_b32 s100, s17, 2
	s_mov_b32 s101, 0
	s_andn2_b64 vcc, exec, s[6:7]
	s_cbranch_vccnz .Lconv_nogain_p0bf
	v_mov_b32_e32 v196, v12
	v_ashrrev_i32_e32 v197, 31, v12
	v_lshl_add_u64 v[196:197], v[196:197], 2, s[56:57]
	global_load_dword v164, v[196:197], off
	global_load_dword v166, v[196:197], off offset:16
	global_load_dword v168, v[196:197], off offset:32
	global_load_dword v170, v[196:197], off offset:48
	global_load_dword v172, v[196:197], off offset:64
	global_load_dword v174, v[196:197], off offset:80
	global_load_dword v176, v[196:197], off offset:96
	global_load_dword v178, v[196:197], off offset:112
	global_load_dword v180, v[196:197], off offset:128
	global_load_dword v182, v[196:197], off offset:144
	global_load_dword v184, v[196:197], off offset:160
	global_load_dword v186, v[196:197], off offset:176
	global_load_dword v188, v[196:197], off offset:192
	global_load_dword v190, v[196:197], off offset:208
	global_load_dword v192, v[196:197], off offset:224
	global_load_dword v194, v[196:197], off offset:240
	s_branch .Lconv_gdone_p0bf

; #define GAS __attribute__((address_space(1)))
; #define LAS __attribute__((address_space(3)))
;     ...
;     for (int i = 0; i < 16; ++i) { const int kk = 4 * i + kq;
;         f32x4 v = __builtin_nontemporal_load((const GAS f32x4*)(W + (size_t)(k0 + kk) * ldw + n0 + 4 * c4));
;         if (gk) v = v * gk[k0 + kk];
;         LAS float* d = scr + kk * 65 + 4 * c4; d[0] = v[0]; d[1] = v[1]; d[2] = v[2]; d[3] = v[3]; }
.Lconv_gdone_p0bf:
	global_load_dwordx4 v[100:103], v[198:199], off nt
	v_lshl_add_u64 v[198:199], v[198:199], 0, s[100:101]
	global_load_dwordx4 v[104:107], v[198:199], off nt
	v_lshl_add_u64 v[198:199], v[198:199], 0, s[100:101]
	global_load_dwordx4 v[108:111], v[198:199], off nt
	v_lshl_add_u64 v[198:199], v[198:199], 0, s[100:101]
	global_load_dwordx4 v[112:115], v[198:199], off nt
	v_lshl_add_u64 v[198:199], v[198:199], 0, s[100:101]
	global_load_dwordx4 v[116:119], v[198:199], off nt
	v_lshl_add_u64 v[198:199], v[198:199], 0, s[100:101]
	global_load_dwordx4 v[120:123], v[198:199], off nt
	v_lshl_add_u64 v[198:199], v[198:199], 0, s[100:101]
	global_load_dwordx4 v[124:127], v[198:199], off nt
	v_lshl_add_u64 v[198:199], v[198:199], 0, s[100:101]
	global_load_dwordx4 v[128:131], v[198:199], off nt
	v_lshl_add_u64 v[198:199], v[198:199], 0, s[100:101]
	global_load_dwordx4 v[132:135], v[198:199], off nt
	v_lshl_add_u64 v[198:199], v[198:199], 0, s[100:101]
	global_load_dwordx4 v[136:139], v[198:199], off nt
	v_lshl_add_u64 v[198:199], v[198:199], 0, s[100:101]
	global_load_dwordx4 v[140:143], v[198:199], off nt
	v_lshl_add_u64 v[198:199], v[198:199], 0, s[100:101]
	global_load_dwordx4 v[144:147], v[198:199], off nt
	v_lshl_add_u64 v[198:199], v[198:199], 0, s[100:101]
	global_load_dwordx4 v[148:151], v[198:199], off nt
	v_lshl_add_u64 v[198:199], v[198:199], 0, s[100:101]
	global_load_dwordx4 v[152:155], v[198:199], off nt
	v_lshl_add_u64 v[198:199], v[198:199], 0, s[100:101]
	global_load_dwordx4 v[156:159], v[198:199], off nt
	v_lshl_add_u64 v[198:199], v[198:199], 0, s[100:101]
	global_load_dwordx4 v[160:163], v[198:199], off nt
	s_waitcnt vmcnt(15)
	v_pk_mul_f32 v[100:101], v[100:101], v[164:165] op_sel_hi:[1,0]
	v_pk_mul_f32 v[102:103], v[102:103], v[164:165] op_sel_hi:[1,0]
	ds_write2_b32 v30, v100, v101 offset1:1
	ds_write2_b32 v30, v102, v103 offset0:2 offset1:3
	s_waitcnt vmcnt(14)
	v_pk_mul_f32 v[104:105], v[104:105], v[166:167] op_sel_hi:[1,0]
	v_pk_mul_f32 v[106:107], v[106:107], v[166:167] op_sel_hi:[1,0]
	v_add_u32_e32 v196, 0x410, v30
	ds_write2_b32 v196, v104, v105 offset1:1
	ds_write2_b32 v196, v106, v107 offset0:2 offset1:3
	s_waitcnt vmcnt(13)
	v_pk_mul_f32 v[108:109], v[108:109], v[168:169] op_sel_hi:[1,0]
	v_pk_mul_f32 v[110:111], v[110:111], v[168:169] op_sel_hi:[1,0]
	v_add_u32_e32 v196, 0x820, v30
	ds_write2_b32 v196, v108, v109 offset1:1
	ds_write2_b32 v196, v110, v111 offset0:2 offset1:3
	s_waitcnt vmcnt(12)
	v_pk_mul_f32 v[112:113], v[112:113], v[170:171] op_sel_hi:[1,0]
	v_pk_mul_f32 v[114:115], v[114:115], v[170:171] op_sel_hi:[1,0]
	v_add_u32_e32 v196, 0xc30, v30
	ds_write2_b32 v196, v112, v113 offset1:1
	ds_write2_b32 v196, v114, v115 offset0:2 offset1:3
	s_waitcnt vmcnt(11)
	v_pk_mul_f32 v[116:117], v[116:117], v[172:173] op_sel_hi:[1,0]
	v_pk_mul_f32 v[118:119], v[118:119], v[172:173] op_sel_hi:[1,0]
	v_add_u32_e32 v196, 0x1040, v30
	ds_write2_b32 v196, v116, v117 offset1:1
	ds_write2_b32 v196, v118, v119 offset0:2 offset1:3
	s_waitcnt vmcnt(10)
	v_pk_mul_f32 v[120:121], v[120:121], v[174:175] op_sel_hi:[1,0]
	v_pk_mul_f32 v[122:123], v[122:123], v[174:175] op_sel_hi:[1,0]
	v_add_u32_e32 v196, 0x1450, v30
	ds_write2_b32 v196, v120, v121 offset1:1
	ds_write2_b32 v196, v122, v123 offset0:2 offset1:3
	s_waitcnt vmcnt(9)
	v_pk_mul_f32 v[124:125], v[124:125], v[176:177] op_sel_hi:[1,0]
	v_pk_mul_f32 v[126:127], v[126:127], v[176:177] op_sel_hi:[1,0]
	v_add_u32_e32 v196, 0x1860, v30
	ds_write2_b32 v196, v124, v125 offset1:1
	ds_write2_b32 v196, v126, v127 offset0:2 offset1:3
	s_waitcnt vmcnt(8)
	v_pk_mul_f32 v[128:129], v[128:129], v[178:179] op_sel_hi:[1,0]
	v_pk_mul_f32 v[130:131], v[130:131], v[178:179] op_sel_hi:[1,0]
	v_add_u32_e32 v196, 0x1c70, v30
	ds_write2_b32 v196, v128, v129 offset1:1
	ds_write2_b32 v196, v130, v131 offset0:2 offset1:3
	s_waitcnt vmcnt(7)
	v_pk_mul_f32 v[132:133], v[132:133], v[180:181] op_sel_hi:[1,0]
	v_pk_mul_f32 v[134:135], v[134:135], v[180:181] op_sel_hi:[1,0]
	v_add_u32_e32 v196, 0x2080, v30
	ds_write2_b32 v196, v132, v133 offset1:1
	ds_write2_b32 v196, v134, v135 offset0:2 offset1:3
	s_waitcnt vmcnt(6)
	v_pk_mul_f32 v[136:137], v[136:137], v[182:183] op_sel_hi:[1,0]
	v_pk_mul_f32 v[138:139], v[138:139], v[182:183] op_sel_hi:[1,0]
	v_add_u32_e32 v196, 0x2490, v30
	ds_write2_b32 v196, v136, v137 offset1:1
	ds_write2_b32 v196, v138, v139 offset0:2 offset1:3
	s_waitcnt vmcnt(5)
	v_pk_mul_f32 v[140:141], v[140:141], v[184:185] op_sel_hi:[1,0]
	v_pk_mul_f32 v[142:143], v[142:143], v[184:185] op_sel_hi:[1,0]
	v_add_u32_e32 v196, 0x28a0, v30
	ds_write2_b32 v196, v140, v141 offset1:1
	ds_write2_b32 v196, v142, v143 offset0:2 offset1:3
	s_waitcnt vmcnt(4)
	v_pk_mul_f32 v[144:145], v[144:145], v[186:187] op_sel_hi:[1,0]
	v_pk_mul_f32 v[146:147], v[146:147], v[186:187] op_sel_hi:[1,0]
	v_add_u32_e32 v196, 0x2cb0, v30
	ds_write2_b32 v196, v144, v145 offset1:1
	ds_write2_b32 v196, v146, v147 offset0:2 offset1:3
	s_waitcnt vmcnt(3)
	v_pk_mul_f32 v[148:149], v[148:149], v[188:189] op_sel_hi:[1,0]
	v_pk_mul_f32 v[150:151], v[150:151], v[188:189] op_sel_hi:[1,0]
	v_add_u32_e32 v196, 0x30c0, v30
	ds_write2_b32 v196, v148, v149 offset1:1
	ds_write2_b32 v196, v150, v151 offset0:2 offset1:3
	s_waitcnt vmcnt(2)
	v_pk_mul_f32 v[152:153], v[152:153], v[190:191] op_sel_hi:[1,0]
	v_pk_mul_f32 v[154:155], v[154:155], v[190:191] op_sel_hi:[1,0]
	v_add_u32_e32 v196, 0x34d0, v30
	ds_write2_b32 v196, v152, v153 offset1:1
	ds_write2_b32 v196, v154, v155 offset0:2 offset1:3
	s_waitcnt vmcnt(1)
	v_pk_mul_f32 v[156:157], v[156:157], v[192:193] op_sel_hi:[1,0]
	v_pk_mul_f32 v[158:159], v[158:159], v[192:193] op_sel_hi:[1,0]
	v_add_u32_e32 v196, 0x38e0, v30
	ds_write2_b32 v196, v156, v157 offset1:1
	ds_write2_b32 v196, v158, v159 offset0:2 offset1:3
	s_waitcnt vmcnt(0)
	v_pk_mul_f32 v[160:161], v[160:161], v[194:195] op_sel_hi:[1,0]
	v_pk_mul_f32 v[162:163], v[162:163], v[194:195] op_sel_hi:[1,0]
	v_add_u32_e32 v196, 0x3cf0, v30
	ds_write2_b32 v196, v160, v161 offset1:1
	ds_write2_b32 v196, v162, v163 offset0:2 offset1:3
	s_branch .LBB0_16

; #define PG8_STAGE(bufoff, gbase, voff) do { _Pragma("unroll") for (int _i = 0; _i < 2; ++_i) \
;         __builtin_amdgcn_global_load_lds((const unsigned*)((const char*)(gbase) + (voff)[_i]), (PG8_LAS unsigned*)(lds + (bufoff) + ldsw + _i * 8192), 16, 0, 0); } while (0)
; #define PG8_LDA(dst, b, h) do { _Pragma("unroll") for (int m = 0; m < 4; ++m) _Pragma("unroll") for (int k = 0; k < 2; ++k) dst[m][k] = *(const PG8_LAS bf16x8*)(lds + PG8_SA(b, h) + aoff + m * 2048 + k * 1024); } while (0)
; #define PG8_LDB(dst, b, h) do { _Pragma("unroll") for (int n = 0; n < 2; ++n) _Pragma("unroll") for (int k = 0; k < 2; ++k) dst[n][k] = *(const PG8_LAS bf16x8*)(lds + PG8_SB(b, h) + boff + n * 2048 + k * 1024); } while (0)
; #define PG8_MMA(ai, bj, At, Bt) do { __builtin_amdgcn_s_setprio(1); _Pragma("unroll") for (int m = 0; m < 4; ++m) _Pragma("unroll") for (int n = 0; n < 2; ++n) _Pragma("unroll") for (int k = 0; k < 2; ++k) \
;         acc[ai][bj][m][n] = __builtin_amdgcn_mfma_f32_16x16x32_bf16(Bt[n][k], At[m][k], acc[ai][bj][m][n], 0, 0, 0); __builtin_amdgcn_s_setprio(0); } while (0)
; #define PG8_WAIT_V(n) asm volatile("s_waitcnt vmcnt(" #n ")" ::: "memory")
; #define PG8_WAIT_L(n) asm volatile("s_waitcnt lgkmcnt(" #n ")" ::: "memory")
; #define PG8_BAR __builtin_amdgcn_s_barrier()
; #define PG8_SCHED __builtin_amdgcn_sched_barrier(0)
; #define PG8_BAR __builtin_amdgcn_s_barrier()
; template <class Epi, class Sched, bool ALIGN_EPI = false, bool SP2 = false, bool ABLK = false, bool BBLK = false>
; __device__ __forceinline__ void gemm_phase_f8(PG8_LAS unsigned char* lds, const Gemm g, const Sched& S, const Epi& E) {
;     ...
;             PG8_LDB(B0, 0, 0); PG8_LDB(B1, 0, 1); PG8_SCHED; PG8_LDA(At, 0, 0); PG8_STAGE(PG8_SA(1, 1), a1 + hstep, voffA);
;             PG8_WAIT_V(8); PG8_WAIT_L(0); PG8_BAR; PG8_MMA(0, 0, At, B0); PG8_MMA(0, 1, At, B1); PG8_BAR; PG8_SCHED;
;             PG8_LDA(At, 0, 1); PG8_STAGE(PG8_SB(0, 0), b2, voffB); PG8_STAGE(PG8_SB(0, 1), b2 + hstep, voffB); PG8_STAGE(PG8_SA(0, 0), a2, voffA);
;             PG8_WAIT_V(8); PG8_WAIT_L(0); PG8_BAR; PG8_MMA(1, 0, At, B0); PG8_MMA(1, 1, At, B1); PG8_BAR; PG8_SCHED;
;             PG8_LDB(B0, 1, 0); PG8_LDB(B1, 1, 1); PG8_SCHED; PG8_LDA(At, 1, 0); PG8_STAGE(PG8_SA(0, 1), a2 + hstep, voffA);
;             PG8_WAIT_V(8); PG8_WAIT_L(0); PG8_BAR; PG8_MMA(0, 0, At, B0); PG8_MMA(0, 1, At, B1); PG8_BAR; PG8_SCHED;
.LBB0_893:
	ds_read_b128 v[18:21], v189
	ds_read_b128 v[22:25], v189 offset:1024
	ds_read_b128 v[26:29], v189 offset:2048
	ds_read_b128 v[30:33], v189 offset:3072
	ds_read_b128 v[2:5], v190
	ds_read_b128 v[6:9], v190 offset:1024
	ds_read_b128 v[10:13], v190 offset:2048
	ds_read_b128 v[14:17], v190 offset:3072
	s_add_u32 s30, s28, 0xfff80080
	s_addc_u32 s31, s29, -1
	s_cmp_eq_u32 s57, 28
	s_cselect_b32 s35, s17, s31
	s_cselect_b32 s34, s52, s30
	s_cselect_b32 s31, s15, s55
	s_cselect_b32 s30, s53, s54
	v_lshl_add_u64 v[210:211], s[28:29], 0, v[172:173]
	s_add_i32 m0, s41, 0xc000
	ds_read_b128 v[180:183], v191
	ds_read_b128 v[184:187], v191 offset:1024
	ds_read_b128 v[194:197], v191 offset:2048
	ds_read_b128 v[198:201], v191 offset:3072
	ds_read_b128 v[202:205], v191 offset:4096
	ds_read_b128 v[206:209], v191 offset:5120
	ds_read_b128 v[218:221], v191 offset:6144
	ds_read_b128 v[222:225], v191 offset:7168
	global_load_lds_dwordx4 v[210:211], off
	v_lshl_add_u64 v[210:211], s[28:29], 0, v[174:175]
	s_add_i32 m0, s41, 0xe000
	s_nop 0
	global_load_lds_dwordx4 v[210:211], off
	s_waitcnt vmcnt(8)
	s_waitcnt lgkmcnt(0)
	s_barrier
	s_setprio 1
	s_waitcnt lgkmcnt(0)
	v_mfma_f32_16x16x128_f8f6f4 v[158:161], v[18:25], v[180:187], v[158:161]
	v_mfma_f32_16x16x128_f8f6f4 v[142:145], v[26:33], v[180:187], v[142:145]
	v_mfma_f32_16x16x128_f8f6f4 v[154:157], v[18:25], v[194:201], v[154:157]
	v_mfma_f32_16x16x128_f8f6f4 v[138:141], v[26:33], v[194:201], v[138:141]
	v_mfma_f32_16x16x128_f8f6f4 v[150:153], v[18:25], v[202:209], v[150:153]
	v_mfma_f32_16x16x128_f8f6f4 v[134:137], v[26:33], v[202:209], v[134:137]
	v_mfma_f32_16x16x128_f8f6f4 v[146:149], v[18:25], v[218:225], v[146:149]
	v_mfma_f32_16x16x128_f8f6f4 v[130:133], v[26:33], v[218:225], v[130:133]
	s_setprio 0
	s_setprio 1
	v_mfma_f32_16x16x128_f8f6f4 v[126:129], v[2:9], v[180:187], v[126:129]
	v_mfma_f32_16x16x128_f8f6f4 v[110:113], v[10:17], v[180:187], v[110:113]
	v_mfma_f32_16x16x128_f8f6f4 v[122:125], v[2:9], v[194:201], v[122:125]
	v_mfma_f32_16x16x128_f8f6f4 v[106:109], v[10:17], v[194:201], v[106:109]
	v_mfma_f32_16x16x128_f8f6f4 v[118:121], v[2:9], v[202:209], v[118:121]
	v_mfma_f32_16x16x128_f8f6f4 v[102:105], v[10:17], v[202:209], v[102:105]
	v_mfma_f32_16x16x128_f8f6f4 v[114:117], v[2:9], v[218:225], v[114:117]
	v_mfma_f32_16x16x128_f8f6f4 v[98:101], v[10:17], v[218:225], v[98:101]
	s_setprio 0
	s_barrier
	s_add_i32 s58, s48, s40
	v_lshl_add_u64 v[180:181], s[30:31], 0, v[166:167]
	s_mov_b32 m0, s58
	ds_read_b128 v[194:197], v191 offset:16384
	ds_read_b128 v[198:201], v191 offset:17408
	ds_read_b128 v[202:205], v191 offset:18432
	ds_read_b128 v[206:209], v191 offset:19456
	ds_read_b128 v[218:221], v191 offset:20480
	ds_read_b128 v[222:225], v191 offset:21504
	ds_read_b128 v[226:229], v191 offset:22528
	ds_read_b128 v[230:233], v191 offset:23552
	global_load_lds_dwordx4 v[180:181], off
	s_add_i32 m0, s58, 0x2000
	s_add_u32 s58, s30, 0x80000
	v_lshl_add_u64 v[182:183], s[30:31], 0, v[162:163]
	s_addc_u32 s59, s31, 0
	s_add_i32 s60, s49, s40
	global_load_lds_dwordx4 v[182:183], off
	v_lshl_add_u64 v[184:185], s[58:59], 0, v[166:167]
	s_mov_b32 m0, s60
	v_lshl_add_u64 v[186:187], s[34:35], 0, v[164:165]
	global_load_lds_dwordx4 v[184:185], off
	v_lshl_add_u64 v[184:185], s[58:59], 0, v[162:163]
	s_add_i32 m0, s60, 0x2000
	s_nop 0
	global_load_lds_dwordx4 v[184:185], off
	v_lshl_add_u64 v[184:185], s[34:35], 0, v[168:169]
	s_mov_b32 m0, s41
	s_nop 0
	global_load_lds_dwordx4 v[184:185], off
	s_mov_b32 m0, s42
	s_nop 0
	global_load_lds_dwordx4 v[186:187], off
	s_waitcnt vmcnt(8)
	s_waitcnt lgkmcnt(0)
	s_barrier
	s_setprio 1
	s_waitcnt lgkmcnt(0)
	v_mfma_f32_16x16x128_f8f6f4 v[94:97], v[18:25], v[194:201], v[94:97]
	v_mfma_f32_16x16x128_f8f6f4 v[78:81], v[26:33], v[194:201], v[78:81]
	v_mfma_f32_16x16x128_f8f6f4 v[90:93], v[18:25], v[202:209], v[90:93]
	v_mfma_f32_16x16x128_f8f6f4 v[74:77], v[26:33], v[202:209], v[74:77]
	v_mfma_f32_16x16x128_f8f6f4 v[86:89], v[18:25], v[218:225], v[86:89]
	v_mfma_f32_16x16x128_f8f6f4 v[70:73], v[26:33], v[218:225], v[70:73]
	v_mfma_f32_16x16x128_f8f6f4 v[82:85], v[18:25], v[226:233], v[82:85]
	v_mfma_f32_16x16x128_f8f6f4 v[66:69], v[26:33], v[226:233], v[66:69]
	s_setprio 0
	s_setprio 1
	v_mfma_f32_16x16x128_f8f6f4 v[62:65], v[2:9], v[194:201], v[62:65]
	v_mfma_f32_16x16x128_f8f6f4 v[46:49], v[10:17], v[194:201], v[46:49]
	v_mfma_f32_16x16x128_f8f6f4 v[58:61], v[2:9], v[202:209], v[58:61]
	v_mfma_f32_16x16x128_f8f6f4 v[42:45], v[10:17], v[202:209], v[42:45]
	v_mfma_f32_16x16x128_f8f6f4 v[54:57], v[2:9], v[218:225], v[54:57]
	v_mfma_f32_16x16x128_f8f6f4 v[38:41], v[10:17], v[218:225], v[38:41]
	v_mfma_f32_16x16x128_f8f6f4 v[50:53], v[2:9], v[226:233], v[50:53]
	v_mfma_f32_16x16x128_f8f6f4 v[34:37], v[10:17], v[226:233], v[34:37]
	s_setprio 0
	s_barrier
	s_add_i32 s58, 0, 0x18000
	s_add_i32 s59, 0, 0x1c000
	v_add_u32_e32 v14, s58, v188
	v_add_u32_e32 v30, s59, v188
	ds_read_b128 v[2:5], v14
	ds_read_b128 v[6:9], v14 offset:1024
	ds_read_b128 v[10:13], v14 offset:2048
	ds_read_b128 v[14:17], v14 offset:3072
	ds_read_b128 v[18:21], v30
	ds_read_b128 v[22:25], v30 offset:1024
	ds_read_b128 v[26:29], v30 offset:2048
	ds_read_b128 v[30:33], v30 offset:3072
	s_add_u32 s34, s34, 0x80000
	s_addc_u32 s35, s35, 0
	s_mov_b32 m0, s43
	v_lshl_add_u64 v[210:211], s[34:35], 0, v[168:169]
	ds_read_b128 v[194:197], v191 offset:32768
	ds_read_b128 v[198:201], v191 offset:33792
	ds_read_b128 v[202:205], v191 offset:34816
	ds_read_b128 v[206:209], v191 offset:35840
	ds_read_b128 v[218:221], v191 offset:36864
	ds_read_b128 v[222:225], v191 offset:37888
	ds_read_b128 v[226:229], v191 offset:38912
	ds_read_b128 v[230:233], v191 offset:39936
	global_load_lds_dwordx4 v[210:211], off
	v_lshl_add_u64 v[210:211], s[34:35], 0, v[164:165]
	s_mov_b32 m0, s44
	s_nop 0
	global_load_lds_dwordx4 v[210:211], off
	s_waitcnt vmcnt(8)
	s_waitcnt lgkmcnt(0)
	s_barrier
; #define PG8_STAGE(bufoff, gbase, voff) do { _Pragma("unroll") for (int _i = 0; _i < 2; ++_i) \
;         __builtin_amdgcn_global_load_lds((const unsigned*)((const char*)(gbase) + (voff)[_i]), (PG8_LAS unsigned*)(lds + (bufoff) + ldsw + _i * 8192), 16, 0, 0); } while (0)
; #define PG8_LDA(dst, b, h) do { _Pragma("unroll") for (int m = 0; m < 4; ++m) _Pragma("unroll") for (int k = 0; k < 2; ++k) dst[m][k] = *(const PG8_LAS bf16x8*)(lds + PG8_SA(b, h) + aoff + m * 2048 + k * 1024); } while (0)
; #define PG8_MMA(ai, bj, At, Bt) do { __builtin_amdgcn_s_setprio(1); _Pragma("unroll") for (int m = 0; m < 4; ++m) _Pragma("unroll") for (int n = 0; n < 2; ++n) _Pragma("unroll") for (int k = 0; k < 2; ++k) \
;         acc[ai][bj][m][n] = __builtin_amdgcn_mfma_f32_16x16x32_bf16(Bt[n][k], At[m][k], acc[ai][bj][m][n], 0, 0, 0); __builtin_amdgcn_s_setprio(0); } while (0)
; #define PG8_WAIT_V(n) asm volatile("s_waitcnt vmcnt(" #n ")" ::: "memory")
; #define PG8_WAIT_L(n) asm volatile("s_waitcnt lgkmcnt(" #n ")" ::: "memory")
; #define PG8_BAR __builtin_amdgcn_s_barrier()
; #define PG8_SCHED __builtin_amdgcn_sched_barrier(0)
; #define PG8_STAGE(bufoff, gbase, voff) do { _Pragma("unroll") for (int _i = 0; _i < 2; ++_i) \
;         __builtin_amdgcn_global_load_lds((const unsigned*)((const char*)(gbase) + (voff)[_i]), (PG8_LAS unsigned*)(lds + (bufoff) + ldsw + _i * 8192), 16, 0, 0); } while (0)
;     __device__ __forceinline__ void operator()(const f32x4 (&acc)[2][2][4][2], const Unit& u, int wr, int wc, int fr, int fq) const {
;     ...
;         for (int ai = 0; ai < 2; ++ai) { float rs4[4];
; #pragma unroll
;             for (int m = 0; m < 4; ++m) rs4[m] = rsqrtf(ss[u.pm * 256 + ai * HALF + wr * 64 + m * 16 + fr] * (1.0f / 4096.0f) + RMS_EPS) * (sc * 16.f);
; template <class Epi, class Sched, bool ALIGN_EPI = false, bool SP2 = false, bool ABLK = false, bool BBLK = false>
; __device__ __forceinline__ void gemm_phase_f8(PG8_LAS unsigned char* lds, const Gemm g, const Sched& S, const Epi& E) {
;     ...
;             PG8_WAIT_V(8); PG8_WAIT_L(0); PG8_BAR; PG8_MMA(0, 0, At, B0); PG8_MMA(0, 1, At, B1); PG8_BAR; PG8_SCHED;
;             PG8_LDA(At, 1, 1); PG8_STAGE(PG8_SB(1, 0), b3, voffB); PG8_STAGE(PG8_SB(1, 1), b3 + hstep, voffB); PG8_STAGE(PG8_SA(1, 0), a3, voffA);
;             PG8_WAIT_V(8); PG8_WAIT_L(0); PG8_BAR; PG8_MMA(1, 0, At, B0); PG8_MMA(1, 1, At, B1); PG8_BAR; PG8_SCHED;
	s_setprio 1
	s_waitcnt lgkmcnt(0)
	v_mfma_f32_16x16x128_f8f6f4 v[158:161], v[2:9], v[194:201], v[158:161]
	v_mfma_f32_16x16x128_f8f6f4 v[142:145], v[10:17], v[194:201], v[142:145]
	v_mfma_f32_16x16x128_f8f6f4 v[154:157], v[2:9], v[202:209], v[154:157]
	v_mfma_f32_16x16x128_f8f6f4 v[138:141], v[10:17], v[202:209], v[138:141]
	v_mfma_f32_16x16x128_f8f6f4 v[150:153], v[2:9], v[218:225], v[150:153]
	v_mfma_f32_16x16x128_f8f6f4 v[134:137], v[10:17], v[218:225], v[134:137]
	v_mfma_f32_16x16x128_f8f6f4 v[146:149], v[2:9], v[226:233], v[146:149]
	v_mfma_f32_16x16x128_f8f6f4 v[130:133], v[10:17], v[226:233], v[130:133]
	s_setprio 0
	s_setprio 1
	v_mfma_f32_16x16x128_f8f6f4 v[126:129], v[18:25], v[194:201], v[126:129]
	v_mfma_f32_16x16x128_f8f6f4 v[110:113], v[26:33], v[194:201], v[110:113]
	v_mfma_f32_16x16x128_f8f6f4 v[122:125], v[18:25], v[202:209], v[122:125]
	v_mfma_f32_16x16x128_f8f6f4 v[106:109], v[26:33], v[202:209], v[106:109]
	v_mfma_f32_16x16x128_f8f6f4 v[118:121], v[18:25], v[218:225], v[118:121]
	v_mfma_f32_16x16x128_f8f6f4 v[102:105], v[26:33], v[218:225], v[102:105]
	v_mfma_f32_16x16x128_f8f6f4 v[114:117], v[18:25], v[226:233], v[114:117]
	v_mfma_f32_16x16x128_f8f6f4 v[98:101], v[26:33], v[226:233], v[98:101]
	s_setprio 0
	s_barrier
	s_add_i32 s34, s58, s40
	v_lshl_add_u64 v[180:181], v[180:181], 0, s[8:9]
	s_mov_b32 m0, s34
	ds_read_b128 v[194:197], v191 offset:49152
	ds_read_b128 v[198:201], v191 offset:50176
	ds_read_b128 v[202:205], v191 offset:51200
	ds_read_b128 v[206:209], v191 offset:52224
	ds_read_b128 v[218:221], v191 offset:53248
	ds_read_b128 v[222:225], v191 offset:54272
	ds_read_b128 v[226:229], v191 offset:55296
	ds_read_b128 v[230:233], v191 offset:56320
	global_load_lds_dwordx4 v[180:181], off
	s_add_i32 m0, s34, 0x2000
	s_add_u32 s30, s30, 0x80800
	v_lshl_add_u64 v[180:181], v[182:183], 0, s[8:9]
	s_addc_u32 s31, s31, 0
	s_add_i32 s34, s59, s40
	global_load_lds_dwordx4 v[180:181], off
	v_lshl_add_u64 v[180:181], s[30:31], 0, v[166:167]
	s_mov_b32 m0, s34
	s_nop 0
	global_load_lds_dwordx4 v[180:181], off
	v_lshl_add_u64 v[180:181], s[30:31], 0, v[162:163]
	s_add_i32 m0, s34, 0x2000
	s_nop 0
	global_load_lds_dwordx4 v[180:181], off
	v_lshl_add_u64 v[180:181], v[184:185], 0, s[10:11]
	s_mov_b32 m0, s45
	s_nop 0
	global_load_lds_dwordx4 v[180:181], off
	v_lshl_add_u64 v[180:181], v[186:187], 0, s[10:11]
	s_mov_b32 m0, s46
	s_nop 0
	global_load_lds_dwordx4 v[180:181], off
	s_waitcnt vmcnt(8)
	s_waitcnt lgkmcnt(0)
	s_barrier
	s_setprio 1
	s_waitcnt lgkmcnt(0)
	v_mfma_f32_16x16x128_f8f6f4 v[94:97], v[2:9], v[194:201], v[94:97]
	v_mfma_f32_16x16x128_f8f6f4 v[78:81], v[10:17], v[194:201], v[78:81]
	v_mfma_f32_16x16x128_f8f6f4 v[90:93], v[2:9], v[202:209], v[90:93]
	v_mfma_f32_16x16x128_f8f6f4 v[74:77], v[10:17], v[202:209], v[74:77]
	v_mfma_f32_16x16x128_f8f6f4 v[86:89], v[2:9], v[218:225], v[86:89]
	v_mfma_f32_16x16x128_f8f6f4 v[70:73], v[10:17], v[218:225], v[70:73]
	v_mfma_f32_16x16x128_f8f6f4 v[82:85], v[2:9], v[226:233], v[82:85]
	v_mfma_f32_16x16x128_f8f6f4 v[66:69], v[10:17], v[226:233], v[66:69]
	s_setprio 0
	s_setprio 1
	v_mfma_f32_16x16x128_f8f6f4 v[62:65], v[18:25], v[194:201], v[62:65]
	v_mfma_f32_16x16x128_f8f6f4 v[46:49], v[26:33], v[194:201], v[46:49]
	v_mfma_f32_16x16x128_f8f6f4 v[58:61], v[18:25], v[202:209], v[58:61]
	v_mfma_f32_16x16x128_f8f6f4 v[42:45], v[26:33], v[202:209], v[42:45]
	v_mfma_f32_16x16x128_f8f6f4 v[54:57], v[18:25], v[218:225], v[54:57]
	v_mfma_f32_16x16x128_f8f6f4 v[38:41], v[26:33], v[218:225], v[38:41]
	v_mfma_f32_16x16x128_f8f6f4 v[50:53], v[18:25], v[226:233], v[50:53]
	v_mfma_f32_16x16x128_f8f6f4 v[34:37], v[26:33], v[226:233], v[34:37]
	s_setprio 0
	s_barrier
	s_add_i32 s57, s57, 2
	s_add_u32 s54, s54, 0x1000
	s_addc_u32 s55, s55, 0
	s_add_u32 s28, s28, 0x100
	s_addc_u32 s29, s29, 0
	s_cmp_gt_u32 s57, 29
	s_cbranch_scc0 .LBB0_893
	v_lshl_add_u32 v242, s26, 8, v1
	v_ashrrev_i32_e32 v243, 31, v242
	v_lshl_add_u64 v[244:245], v[242:243], 2, s[20:21]
	global_load_dword v234, v[244:245], off
	global_load_dword v235, v[244:245], off offset:64
	global_load_dword v236, v[244:245], off offset:128
	global_load_dword v237, v[244:245], off offset:192
	global_load_dword v238, v[244:245], off offset:512
	global_load_dword v239, v[244:245], off offset:576
	global_load_dword v240, v[244:245], off offset:640
	global_load_dword v241, v[244:245], off offset:704
	s_and_b64 vcc, exec, s[12:13]
	s_cbranch_vccz .LBB0_896
	s_barrier
;     __device__ __forceinline__ void operator()(const f32x4 (&acc)[2][2][4][2], const Unit& u, int wr, int wc, int fr, int fq) const {
;     ...
;         for (int ai = 0; ai < 2; ++ai) { float rs4[4];
; #pragma unroll
;             for (int m = 0; m < 4; ++m) rs4[m] = rsqrtf(ss[u.pm * 256 + ai * HALF + wr * 64 + m * 16 + fr] * (1.0f / 4096.0f) + RMS_EPS) * (sc * 16.f);
;             const int T = (u.pm & 15) * 4 + ai * 2 + wr;
; #pragma unroll
;             for (int bj = 0; bj < 2; ++bj) { const int head = u.pn * 2 + bj;
;                 unsigned char* base = VT + (((size_t)b * 16 + head) * 64 + T) * 8192 + (wc * 32 + 8 * fq) * 64 + 32 * (fr >> 3) + 4 * (fr & 7);
; #pragma unroll
;                 for (int n = 0; n < 2; ++n)
; #pragma unroll
;                     for (int jj = 0; jj < 4; ++jj)
;                         *(unsigned*)(base + (4 * n + jj) * 64) = pk4_fp8(acc[ai][bj][0][n][jj] * rs4[0], acc[ai][bj][1][n][jj] * rs4[1], acc[ai][bj][2][n][jj] * rs4[2], acc[ai][bj][3][n][jj] * rs4[3]); } }
.LBB0_896:
	v_lshl_add_u32 v6, s26, 8, v1
	v_ashrrev_i32_e32 v7, 31, v6
	s_nop 15
	s_nop 15
	v_lshl_add_u64 v[2:3], v[6:7], 2, s[20:21]
	v_mov_b32_e32 v15, 0
	s_lshl_b32 s15, s26, 2
	s_lshl_b32 s28, s27, 1
	s_ashr_i32 s30, s26, 4
	s_and_b32 s15, s15, 60
	s_ashr_i32 s29, s28, 31
	s_add_i32 s26, s15, s39
	s_ashr_i32 s31, s30, 31
	s_lshl_b64 s[34:35], s[28:29], 19
	s_ashr_i32 s27, s26, 31
	s_lshl_b64 s[30:31], s[30:31], 23
	s_lshl_b64 s[26:27], s[26:27], 13
	v_mov_b32_e32 v17, 0
	s_or_b32 s28, s28, 1
	s_ashr_i32 s29, s28, 31
	s_lshl_b64 s[28:29], s[28:29], 19
	s_waitcnt vmcnt(0)
	v_fmamk_f32 v4, v234, 0x39800000, v192
	v_cmp_gt_f32_e32 vcc, s50, v4
	v_mul_f32_e32 v5, 0x4b800000, v4
	s_nop 0
	v_cndmask_b32_e32 v4, v4, v5, vcc
	v_rsq_f32_e32 v4, v4
	s_nop 0
	v_mul_f32_e32 v5, 0x45800000, v4
	v_cndmask_b32_e32 v4, v4, v5, vcc
	v_mul_f32_e32 v7, 0x3e800000, v4
	v_mul_f32_e32 v8, v158, v7
	v_med3_f32 v8, v8, s51, v193
	v_fmamk_f32 v4, v235, 0x39800000, v192
	v_cmp_gt_f32_e32 vcc, s50, v4
	v_mul_f32_e32 v5, 0x4b800000, v4
	s_nop 0
	v_cndmask_b32_e32 v4, v4, v5, vcc
	v_rsq_f32_e32 v4, v4
	s_nop 0
	v_mul_f32_e32 v5, 0x45800000, v4
	v_cndmask_b32_e32 v4, v4, v5, vcc
	v_mul_f32_e32 v10, 0x3e800000, v4
	v_mul_f32_e32 v9, v154, v10
	v_med3_f32 v9, v9, s51, v193
	v_cvt_pk_fp8_f32 v15, v8, v9
	v_mul_f32_e32 v8, v159, v7
	v_mul_f32_e32 v9, v155, v10
	v_med3_f32 v8, v8, s51, v193
	v_med3_f32 v9, v9, s51, v193
	v_fmamk_f32 v4, v236, 0x39800000, v192
	v_cmp_gt_f32_e32 vcc, s50, v4
	v_mul_f32_e32 v5, 0x4b800000, v4
	v_fmamk_f32 v2, v237, 0x39800000, v192
	v_cndmask_b32_e32 v4, v4, v5, vcc
	v_rsq_f32_e32 v4, v4
	v_mul_f32_e32 v3, 0x4b800000, v2
	v_mul_f32_e32 v5, 0x45800000, v4
	v_cndmask_b32_e32 v4, v4, v5, vcc
	v_cmp_gt_f32_e32 vcc, s50, v2
	v_mul_f32_e32 v11, 0x3e800000, v4
	v_mul_f32_e32 v13, v150, v11
	v_cndmask_b32_e32 v2, v2, v3, vcc
	v_rsq_f32_e32 v2, v2
	v_med3_f32 v13, v13, s51, v193
	v_mul_f32_e32 v3, 0x45800000, v2
	v_cndmask_b32_e32 v2, v2, v3, vcc
	v_mul_f32_e32 v12, 0x3e800000, v2
	v_mul_f32_e32 v14, v146, v12
	v_med3_f32 v14, v14, s51, v193
	v_cvt_pk_fp8_f32 v15, v13, v14 op_sel:[0,0,1]
	v_lshl_add_u64 v[2:3], v[170:171], 0, s[34:35]
	v_lshl_add_u64 v[4:5], v[2:3], 0, s[30:31]
	v_lshl_add_u64 v[2:3], v[4:5], 0, s[26:27]
	global_store_dword v[2:3], v15, off
	v_mov_b32_e32 v15, 0
	v_cvt_pk_fp8_f32 v15, v8, v9
	v_mul_f32_e32 v13, v151, v11
	v_mul_f32_e32 v14, v147, v12
	v_med3_f32 v13, v13, s51, v193
	v_med3_f32 v14, v14, s51, v193
	v_cvt_pk_fp8_f32 v15, v13, v14 op_sel:[0,0,1]
	v_mul_f32_e32 v8, v160, v7
	v_mul_f32_e32 v9, v156, v10
	v_med3_f32 v8, v8, s51, v193
	global_store_dword v[2:3], v15, off offset:64
	v_med3_f32 v9, v9, s51, v193
	v_mov_b32_e32 v15, 0
	v_cvt_pk_fp8_f32 v15, v8, v9
	v_mul_f32_e32 v13, v152, v11
	v_mul_f32_e32 v14, v148, v12
	v_med3_f32 v13, v13, s51, v193
	v_med3_f32 v14, v14, s51, v193
	v_cvt_pk_fp8_f32 v15, v13, v14 op_sel:[0,0,1]
	v_mul_f32_e32 v8, v161, v7
	v_mul_f32_e32 v9, v157, v10
	v_med3_f32 v8, v8, s51, v193
	global_store_dword v[2:3], v15, off offset:128
	v_med3_f32 v9, v9, s51, v193
	v_mov_b32_e32 v15, 0
	v_cvt_pk_fp8_f32 v15, v8, v9
	v_mul_f32_e32 v13, v153, v11
	v_mul_f32_e32 v14, v149, v12
	v_med3_f32 v13, v13, s51, v193
	v_med3_f32 v14, v14, s51, v193
	v_cvt_pk_fp8_f32 v15, v13, v14 op_sel:[0,0,1]
	v_mul_f32_e32 v8, v142, v7
	v_mul_f32_e32 v9, v138, v10
	v_med3_f32 v8, v8, s51, v193
	global_store_dword v[2:3], v15, off offset:192
	v_med3_f32 v9, v9, s51, v193
	v_mov_b32_e32 v15, 0
	v_cvt_pk_fp8_f32 v15, v8, v9
	v_mul_f32_e32 v13, v134, v11
	v_mul_f32_e32 v14, v130, v12
	v_med3_f32 v13, v13, s51, v193
	v_med3_f32 v14, v14, s51, v193
	v_cvt_pk_fp8_f32 v15, v13, v14 op_sel:[0,0,1]
	v_mul_f32_e32 v8, v143, v7
	v_mul_f32_e32 v9, v139, v10
	v_med3_f32 v8, v8, s51, v193
	global_store_dword v[2:3], v15, off offset:256
	v_med3_f32 v9, v9, s51, v193
	v_mov_b32_e32 v15, 0
	v_cvt_pk_fp8_f32 v15, v8, v9
	v_mul_f32_e32 v13, v135, v11
	v_mul_f32_e32 v14, v131, v12
	v_med3_f32 v13, v13, s51, v193
	v_med3_f32 v14, v14, s51, v193
	v_cvt_pk_fp8_f32 v15, v13, v14 op_sel:[0,0,1]
	v_mul_f32_e32 v8, v144, v7
	v_mul_f32_e32 v9, v140, v10
	v_med3_f32 v8, v8, s51, v193
	global_store_dword v[2:3], v15, off offset:320
	v_med3_f32 v9, v9, s51, v193
	v_mov_b32_e32 v15, 0
	v_cvt_pk_fp8_f32 v15, v8, v9
	v_mul_f32_e32 v13, v136, v11
	v_mul_f32_e32 v14, v132, v12
	v_med3_f32 v13, v13, s51, v193
	v_med3_f32 v14, v14, s51, v193
	v_cvt_pk_fp8_f32 v15, v13, v14 op_sel:[0,0,1]
	v_mul_f32_e32 v8, v145, v7
	v_mul_f32_e32 v9, v141, v10
	v_med3_f32 v8, v8, s51, v193
	global_store_dword v[2:3], v15, off offset:384
	v_med3_f32 v9, v9, s51, v193
	v_mov_b32_e32 v15, 0
	v_cvt_pk_fp8_f32 v15, v8, v9
	v_mul_f32_e32 v13, v137, v11
	v_mul_f32_e32 v14, v133, v12
	v_med3_f32 v13, v13, s51, v193
	v_med3_f32 v14, v14, s51, v193
	v_cvt_pk_fp8_f32 v15, v13, v14 op_sel:[0,0,1]
	v_mul_f32_e32 v13, v126, v7
	v_mul_f32_e32 v14, v122, v10
	v_med3_f32 v13, v13, s51, v193
	v_med3_f32 v14, v14, s51, v193
	v_cvt_pk_fp8_f32 v17, v13, v14
	global_store_dword v[2:3], v15, off offset:448
	v_mul_f32_e32 v15, v118, v11
	v_mul_f32_e32 v16, v114, v12
	v_med3_f32 v15, v15, s51, v193
	v_med3_f32 v16, v16, s51, v193
	v_cvt_pk_fp8_f32 v17, v15, v16 op_sel:[0,0,1]
	v_lshl_add_u64 v[2:3], v[170:171], 0, s[28:29]
	v_lshl_add_u64 v[2:3], v[2:3], 0, s[30:31]
	v_lshl_add_u64 v[8:9], v[2:3], 0, s[26:27]
	v_mul_f32_e32 v13, v127, v7
	v_mul_f32_e32 v14, v123, v10
	global_store_dword v[8:9], v17, off
	v_med3_f32 v13, v13, s51, v193
	v_med3_f32 v14, v14, s51, v193
	v_mov_b32_e32 v17, 0
	v_cvt_pk_fp8_f32 v17, v13, v14
	v_mul_f32_e32 v15, v119, v11
	v_mul_f32_e32 v16, v115, v12
;     __device__ __forceinline__ void operator()(const f32x4 (&acc)[2][2][4][2], const Unit& u, int wr, int wc, int fr, int fq) const {
;     ...
;         for (int ai = 0; ai < 2; ++ai) { float rs4[4];
; #pragma unroll
;             for (int m = 0; m < 4; ++m) rs4[m] = rsqrtf(ss[u.pm * 256 + ai * HALF + wr * 64 + m * 16 + fr] * (1.0f / 4096.0f) + RMS_EPS) * (sc * 16.f);
;             const int T = (u.pm & 15) * 4 + ai * 2 + wr;
; #pragma unroll
;             for (int bj = 0; bj < 2; ++bj) { const int head = u.pn * 2 + bj;
;                 unsigned char* base = VT + (((size_t)b * 16 + head) * 64 + T) * 8192 + (wc * 32 + 8 * fq) * 64 + 32 * (fr >> 3) + 4 * (fr & 7);
; #pragma unroll
;                 for (int n = 0; n < 2; ++n)
; #pragma unroll
;                     for (int jj = 0; jj < 4; ++jj)
;                         *(unsigned*)(base + (4 * n + jj) * 64) = pk4_fp8(acc[ai][bj][0][n][jj] * rs4[0], acc[ai][bj][1][n][jj] * rs4[1], acc[ai][bj][2][n][jj] * rs4[2], acc[ai][bj][3][n][jj] * rs4[3]); } }
	v_med3_f32 v15, v15, s51, v193
	v_med3_f32 v16, v16, s51, v193
	v_cvt_pk_fp8_f32 v17, v15, v16 op_sel:[0,0,1]
	v_mul_f32_e32 v13, v128, v7
	v_mul_f32_e32 v14, v124, v10
	v_med3_f32 v13, v13, s51, v193
	global_store_dword v[8:9], v17, off offset:64
	v_med3_f32 v14, v14, s51, v193
	v_mov_b32_e32 v17, 0
	v_cvt_pk_fp8_f32 v17, v13, v14
	v_mul_f32_e32 v15, v120, v11
	v_mul_f32_e32 v16, v116, v12
	v_med3_f32 v15, v15, s51, v193
	v_med3_f32 v16, v16, s51, v193
	v_cvt_pk_fp8_f32 v17, v15, v16 op_sel:[0,0,1]
	v_mul_f32_e32 v13, v129, v7
	v_mul_f32_e32 v14, v125, v10
	v_med3_f32 v13, v13, s51, v193
	global_store_dword v[8:9], v17, off offset:128
	v_med3_f32 v14, v14, s51, v193
	v_mov_b32_e32 v17, 0
	v_cvt_pk_fp8_f32 v17, v13, v14
	v_mul_f32_e32 v15, v121, v11
	v_mul_f32_e32 v16, v117, v12
	v_med3_f32 v15, v15, s51, v193
	v_med3_f32 v16, v16, s51, v193
	v_cvt_pk_fp8_f32 v17, v15, v16 op_sel:[0,0,1]
	v_mul_f32_e32 v13, v110, v7
	v_mul_f32_e32 v14, v106, v10
	v_med3_f32 v13, v13, s51, v193
	global_store_dword v[8:9], v17, off offset:192
	v_med3_f32 v14, v14, s51, v193
	v_mov_b32_e32 v17, 0
	v_cvt_pk_fp8_f32 v17, v13, v14
	v_mul_f32_e32 v15, v102, v11
	v_mul_f32_e32 v16, v98, v12
	v_med3_f32 v15, v15, s51, v193
	v_med3_f32 v16, v16, s51, v193
	v_cvt_pk_fp8_f32 v17, v15, v16 op_sel:[0,0,1]
	v_mul_f32_e32 v13, v111, v7
	v_mul_f32_e32 v14, v107, v10
	v_med3_f32 v13, v13, s51, v193
	global_store_dword v[8:9], v17, off offset:256
	v_med3_f32 v14, v14, s51, v193
	v_mov_b32_e32 v17, 0
	v_cvt_pk_fp8_f32 v17, v13, v14
	v_mul_f32_e32 v15, v103, v11
	v_mul_f32_e32 v16, v99, v12
	v_med3_f32 v15, v15, s51, v193
	v_med3_f32 v16, v16, s51, v193
	v_cvt_pk_fp8_f32 v17, v15, v16 op_sel:[0,0,1]
	v_mul_f32_e32 v13, v112, v7
	v_mul_f32_e32 v14, v108, v10
	v_med3_f32 v13, v13, s51, v193
	global_store_dword v[8:9], v17, off offset:320
	v_med3_f32 v14, v14, s51, v193
	v_mov_b32_e32 v17, 0
	v_mul_f32_e32 v7, v113, v7
	v_mul_f32_e32 v10, v109, v10
	v_cvt_pk_fp8_f32 v17, v13, v14
	v_med3_f32 v7, v7, s51, v193
	v_med3_f32 v10, v10, s51, v193
	v_mov_b32_e32 v13, 0
	v_cvt_pk_fp8_f32 v13, v7, v10
	v_mul_f32_e32 v15, v104, v11
	v_mul_f32_e32 v16, v100, v12
	v_mul_f32_e32 v11, v105, v11
	v_mul_f32_e32 v12, v101, v12
	v_med3_f32 v15, v15, s51, v193
	v_med3_f32 v16, v16, s51, v193
	v_med3_f32 v11, v11, s51, v193
	v_med3_f32 v12, v12, s51, v193
	v_cvt_pk_fp8_f32 v17, v15, v16 op_sel:[0,0,1]
	v_cvt_pk_fp8_f32 v13, v11, v12 op_sel:[0,0,1]
	v_add_u32_e32 v10, 0xa0, v6
	v_ashrrev_i32_e32 v11, 31, v10
	global_store_dword v[8:9], v17, off offset:384
	global_store_dword v[8:9], v13, off offset:448
	v_add_u32_e32 v8, 0x80, v6
	v_ashrrev_i32_e32 v9, 31, v8
	v_lshl_add_u64 v[8:9], v[8:9], 2, s[20:21]
	v_lshl_add_u64 v[10:11], v[10:11], 2, s[20:21]
	v_mov_b32_e32 v14, 0
	s_add_u32 s26, s26, 0x4000
	s_addc_u32 s27, s27, 0
	v_lshl_add_u64 v[4:5], v[4:5], 0, s[26:27]
	v_lshl_add_u64 v[2:3], v[2:3], 0, s[26:27]
	s_mov_b64 s[26:27], -1
	v_fmamk_f32 v7, v238, 0x39800000, v192
	v_cmp_gt_f32_e32 vcc, s50, v7
	v_mul_f32_e32 v8, 0x4b800000, v7
	s_nop 0
	v_cndmask_b32_e32 v7, v7, v8, vcc
	v_rsq_f32_e32 v7, v7
	s_nop 0
	v_mul_f32_e32 v8, 0x45800000, v7
	v_cndmask_b32_e32 v7, v7, v8, vcc
	v_add_u32_e32 v8, 0x90, v6
	v_ashrrev_i32_e32 v9, 31, v8
	v_lshl_add_u64 v[8:9], v[8:9], 2, s[20:21]
	v_mul_f32_e32 v7, 0x3e800000, v7
	v_fmamk_f32 v8, v239, 0x39800000, v192
	v_cmp_gt_f32_e32 vcc, s50, v8
	v_mul_f32_e32 v9, 0x4b800000, v8
	s_nop 0
	v_cndmask_b32_e32 v8, v8, v9, vcc
	v_rsq_f32_e32 v8, v8
	s_nop 0
	v_mul_f32_e32 v9, 0x45800000, v8
	v_cndmask_b32_e32 v8, v8, v9, vcc
	v_mul_f32_e32 v8, 0x3e800000, v8
	v_fmamk_f32 v9, v240, 0x39800000, v192
	v_cmp_gt_f32_e32 vcc, s50, v9
	v_mul_f32_e32 v10, 0x4b800000, v9
	s_nop 0
	v_cndmask_b32_e32 v9, v9, v10, vcc
	v_rsq_f32_e32 v9, v9
	s_nop 0
	v_mul_f32_e32 v10, 0x45800000, v9
	v_cndmask_b32_e32 v9, v9, v10, vcc
	v_add_u32_e32 v10, 0xb0, v6
	v_ashrrev_i32_e32 v11, 31, v10
	v_lshl_add_u64 v[10:11], v[10:11], 2, s[20:21]
	v_mul_f32_e32 v11, v90, v8
	v_med3_f32 v11, v11, s51, v193
	v_mul_f32_e32 v9, 0x3e800000, v9
	v_mul_f32_e32 v12, v86, v9
	v_med3_f32 v12, v12, s51, v193
	v_fmamk_f32 v6, v241, 0x39800000, v192
	v_cmp_gt_f32_e32 vcc, s50, v6
	v_mul_f32_e32 v10, 0x4b800000, v6
	s_nop 0
	v_cndmask_b32_e32 v6, v6, v10, vcc
	v_rsq_f32_e32 v6, v6
	s_nop 0
	v_mul_f32_e32 v10, 0x45800000, v6
	v_cndmask_b32_e32 v6, v6, v10, vcc
	v_mul_f32_e32 v10, v94, v7
	v_med3_f32 v10, v10, s51, v193
	v_cvt_pk_fp8_f32 v14, v10, v11
	v_mul_f32_e32 v6, 0x3e800000, v6
	v_mul_f32_e32 v13, v82, v6
	v_med3_f32 v13, v13, s51, v193
	v_cvt_pk_fp8_f32 v14, v12, v13 op_sel:[0,0,1]
	v_mul_f32_e32 v10, v95, v7
	v_mul_f32_e32 v11, v91, v8
	v_med3_f32 v10, v10, s51, v193
	global_store_dword v[4:5], v14, off
	v_med3_f32 v11, v11, s51, v193
	v_mov_b32_e32 v14, 0
	v_cvt_pk_fp8_f32 v14, v10, v11
	v_mul_f32_e32 v12, v87, v9
	v_mul_f32_e32 v13, v83, v6
	v_med3_f32 v12, v12, s51, v193
	v_med3_f32 v13, v13, s51, v193
	v_cvt_pk_fp8_f32 v14, v12, v13 op_sel:[0,0,1]
	v_mul_f32_e32 v10, v96, v7
	v_mul_f32_e32 v11, v92, v8
	v_med3_f32 v10, v10, s51, v193
	global_store_dword v[4:5], v14, off offset:64
	v_med3_f32 v11, v11, s51, v193
	v_mov_b32_e32 v14, 0
	v_cvt_pk_fp8_f32 v14, v10, v11
	v_mul_f32_e32 v12, v88, v9
	v_mul_f32_e32 v13, v84, v6
;     __device__ __forceinline__ void operator()(const f32x4 (&acc)[2][2][4][2], const Unit& u, int wr, int wc, int fr, int fq) const {
;     ...
;             for (int bj = 0; bj < 2; ++bj) { const int head = u.pn * 2 + bj;
;                 unsigned char* base = VT + (((size_t)b * 16 + head) * 64 + T) * 8192 + (wc * 32 + 8 * fq) * 64 + 32 * (fr >> 3) + 4 * (fr & 7);
; #pragma unroll
;                 for (int n = 0; n < 2; ++n)
; #pragma unroll
;                     for (int jj = 0; jj < 4; ++jj)
;                         *(unsigned*)(base + (4 * n + jj) * 64) = pk4_fp8(acc[ai][bj][0][n][jj] * rs4[0], acc[ai][bj][1][n][jj] * rs4[1], acc[ai][bj][2][n][jj] * rs4[2], acc[ai][bj][3][n][jj] * rs4[3]); } }
	v_med3_f32 v12, v12, s51, v193
	v_med3_f32 v13, v13, s51, v193
	v_cvt_pk_fp8_f32 v14, v12, v13 op_sel:[0,0,1]
	v_mul_f32_e32 v10, v97, v7
	v_mul_f32_e32 v11, v93, v8
	v_med3_f32 v10, v10, s51, v193
	global_store_dword v[4:5], v14, off offset:128
	v_med3_f32 v11, v11, s51, v193
	v_mov_b32_e32 v14, 0
	v_cvt_pk_fp8_f32 v14, v10, v11
	v_mul_f32_e32 v12, v89, v9
	v_mul_f32_e32 v13, v85, v6
	v_med3_f32 v12, v12, s51, v193
	v_med3_f32 v13, v13, s51, v193
	v_cvt_pk_fp8_f32 v14, v12, v13 op_sel:[0,0,1]
	v_mul_f32_e32 v10, v78, v7
	v_mul_f32_e32 v11, v74, v8
	v_med3_f32 v10, v10, s51, v193
	global_store_dword v[4:5], v14, off offset:192
	v_med3_f32 v11, v11, s51, v193
	v_mov_b32_e32 v14, 0
	v_cvt_pk_fp8_f32 v14, v10, v11
	v_mul_f32_e32 v12, v70, v9
	v_mul_f32_e32 v13, v66, v6
	v_med3_f32 v12, v12, s51, v193
	v_med3_f32 v13, v13, s51, v193
	v_cvt_pk_fp8_f32 v14, v12, v13 op_sel:[0,0,1]
	v_mul_f32_e32 v10, v79, v7
	v_mul_f32_e32 v11, v75, v8
	v_med3_f32 v10, v10, s51, v193
	global_store_dword v[4:5], v14, off offset:256
	v_med3_f32 v11, v11, s51, v193
	v_mov_b32_e32 v14, 0
	v_cvt_pk_fp8_f32 v14, v10, v11
	v_mul_f32_e32 v12, v71, v9
	v_mul_f32_e32 v13, v67, v6
	v_med3_f32 v12, v12, s51, v193
	v_med3_f32 v13, v13, s51, v193
	v_cvt_pk_fp8_f32 v14, v12, v13 op_sel:[0,0,1]
	v_mul_f32_e32 v10, v80, v7
	v_mul_f32_e32 v11, v76, v8
	v_med3_f32 v10, v10, s51, v193
	global_store_dword v[4:5], v14, off offset:320
	v_med3_f32 v11, v11, s51, v193
	v_mov_b32_e32 v14, 0
	v_cvt_pk_fp8_f32 v14, v10, v11
	v_mul_f32_e32 v12, v72, v9
	v_mul_f32_e32 v13, v68, v6
	v_med3_f32 v12, v12, s51, v193
	v_med3_f32 v13, v13, s51, v193
	v_cvt_pk_fp8_f32 v14, v12, v13 op_sel:[0,0,1]
	v_mul_f32_e32 v10, v81, v7
	v_mul_f32_e32 v11, v77, v8
	v_med3_f32 v10, v10, s51, v193
	global_store_dword v[4:5], v14, off offset:384
	v_med3_f32 v11, v11, s51, v193
	v_mov_b32_e32 v14, 0
	v_cvt_pk_fp8_f32 v14, v10, v11
	v_mul_f32_e32 v12, v73, v9
	v_mul_f32_e32 v13, v69, v6
	v_med3_f32 v12, v12, s51, v193
	v_med3_f32 v13, v13, s51, v193
	v_cvt_pk_fp8_f32 v14, v12, v13 op_sel:[0,0,1]
	v_mov_b32_e32 v12, 0
	v_mul_f32_e32 v10, v54, v9
	v_mul_f32_e32 v11, v50, v6
	global_store_dword v[4:5], v14, off offset:448
	v_mul_f32_e32 v4, v62, v7
	v_mul_f32_e32 v5, v58, v8
	v_med3_f32 v4, v4, s51, v193
	v_med3_f32 v5, v5, s51, v193
	v_cvt_pk_fp8_f32 v12, v4, v5
	v_med3_f32 v10, v10, s51, v193
	v_med3_f32 v11, v11, s51, v193
	v_mul_f32_e32 v4, v63, v7
	v_cvt_pk_fp8_f32 v12, v10, v11 op_sel:[0,0,1]
	v_mul_f32_e32 v5, v59, v8
	v_med3_f32 v4, v4, s51, v193
	v_med3_f32 v5, v5, s51, v193
	global_store_dword v[2:3], v12, off
	v_mov_b32_e32 v12, 0
	v_cvt_pk_fp8_f32 v12, v4, v5
	v_mul_f32_e32 v10, v55, v9
	v_mul_f32_e32 v11, v51, v6
	v_med3_f32 v10, v10, s51, v193
	v_med3_f32 v11, v11, s51, v193
	v_cvt_pk_fp8_f32 v12, v10, v11 op_sel:[0,0,1]
	v_mul_f32_e32 v4, v64, v7
	v_mul_f32_e32 v5, v60, v8
	v_med3_f32 v4, v4, s51, v193
	global_store_dword v[2:3], v12, off offset:64
	v_med3_f32 v5, v5, s51, v193
	v_mov_b32_e32 v12, 0
	v_cvt_pk_fp8_f32 v12, v4, v5
	v_mul_f32_e32 v10, v56, v9
	v_mul_f32_e32 v11, v52, v6
	v_med3_f32 v10, v10, s51, v193
	v_med3_f32 v11, v11, s51, v193
	v_cvt_pk_fp8_f32 v12, v10, v11 op_sel:[0,0,1]
	v_mul_f32_e32 v4, v65, v7
	v_mul_f32_e32 v5, v61, v8
	v_med3_f32 v4, v4, s51, v193
	global_store_dword v[2:3], v12, off offset:128
	v_med3_f32 v5, v5, s51, v193
	v_mov_b32_e32 v12, 0
	v_cvt_pk_fp8_f32 v12, v4, v5
	v_mul_f32_e32 v10, v57, v9
	v_mul_f32_e32 v11, v53, v6
	v_med3_f32 v10, v10, s51, v193
	v_med3_f32 v11, v11, s51, v193
	v_cvt_pk_fp8_f32 v12, v10, v11 op_sel:[0,0,1]
	v_mul_f32_e32 v4, v46, v7
	v_mul_f32_e32 v5, v42, v8
	v_med3_f32 v4, v4, s51, v193
	global_store_dword v[2:3], v12, off offset:192
	v_med3_f32 v5, v5, s51, v193
	v_mov_b32_e32 v12, 0
	v_cvt_pk_fp8_f32 v12, v4, v5
	v_mul_f32_e32 v10, v38, v9
	v_mul_f32_e32 v11, v34, v6
	v_med3_f32 v10, v10, s51, v193
	v_med3_f32 v11, v11, s51, v193
	v_cvt_pk_fp8_f32 v12, v10, v11 op_sel:[0,0,1]
	v_mul_f32_e32 v4, v47, v7
	v_mul_f32_e32 v5, v43, v8
	v_med3_f32 v4, v4, s51, v193
	global_store_dword v[2:3], v12, off offset:256
	v_med3_f32 v5, v5, s51, v193
	v_mov_b32_e32 v12, 0
	v_cvt_pk_fp8_f32 v12, v4, v5
	v_mul_f32_e32 v10, v39, v9
	v_mul_f32_e32 v11, v35, v6
	v_med3_f32 v10, v10, s51, v193
	v_med3_f32 v11, v11, s51, v193
	v_cvt_pk_fp8_f32 v12, v10, v11 op_sel:[0,0,1]
	v_mul_f32_e32 v4, v48, v7
	v_mul_f32_e32 v5, v44, v8
	v_med3_f32 v4, v4, s51, v193
	global_store_dword v[2:3], v12, off offset:320
	v_med3_f32 v5, v5, s51, v193
	v_mov_b32_e32 v12, 0
	v_cvt_pk_fp8_f32 v12, v4, v5
	v_mul_f32_e32 v4, v49, v7
	v_mul_f32_e32 v5, v45, v8
	v_med3_f32 v4, v4, s51, v193
	v_med3_f32 v5, v5, s51, v193
	v_mov_b32_e32 v8, 0
	v_cvt_pk_fp8_f32 v8, v4, v5
	v_mul_f32_e32 v10, v40, v9
	v_mul_f32_e32 v11, v36, v6
	v_mul_f32_e32 v7, v41, v9
	v_mul_f32_e32 v6, v37, v6
	v_med3_f32 v10, v10, s51, v193
	v_med3_f32 v11, v11, s51, v193
	v_med3_f32 v7, v7, s51, v193
	v_med3_f32 v6, v6, s51, v193
	v_cvt_pk_fp8_f32 v12, v10, v11 op_sel:[0,0,1]
	v_cvt_pk_fp8_f32 v8, v7, v6 op_sel:[0,0,1]
	s_andn2_b64 vcc, exec, s[0:1]
	global_store_dword v[2:3], v12, off offset:384
	global_store_dword v[2:3], v8, off offset:448
	s_cbranch_vccnz .LBB0_885
	s_andn2_b64 vcc, exec, s[6:7]
	s_cbranch_vccnz .LBB0_884
	s_barrier
	s_branch .LBB0_884

; #define PG8_STAGE(bufoff, gbase, voff) do { _Pragma("unroll") for (int _i = 0; _i < 2; ++_i) \
;         __builtin_amdgcn_global_load_lds((const unsigned*)((const char*)(gbase) + (voff)[_i]), (PG8_LAS unsigned*)(lds + (bufoff) + ldsw + _i * 8192), 16, 0, 0); } while (0)
; #define PG8_LDA(dst, b, h) do { _Pragma("unroll") for (int m = 0; m < 4; ++m) _Pragma("unroll") for (int k = 0; k < 2; ++k) dst[m][k] = *(const PG8_LAS bf16x8*)(lds + PG8_SA(b, h) + aoff + m * 2048 + k * 1024); } while (0)
; #define PG8_LDB(dst, b, h) do { _Pragma("unroll") for (int n = 0; n < 2; ++n) _Pragma("unroll") for (int k = 0; k < 2; ++k) dst[n][k] = *(const PG8_LAS bf16x8*)(lds + PG8_SB(b, h) + boff + n * 2048 + k * 1024); } while (0)
; #define PG8_MMA(ai, bj, At, Bt) do { __builtin_amdgcn_s_setprio(1); _Pragma("unroll") for (int m = 0; m < 4; ++m) _Pragma("unroll") for (int n = 0; n < 2; ++n) _Pragma("unroll") for (int k = 0; k < 2; ++k) \
;         acc[ai][bj][m][n] = __builtin_amdgcn_mfma_f32_16x16x32_bf16(Bt[n][k], At[m][k], acc[ai][bj][m][n], 0, 0, 0); __builtin_amdgcn_s_setprio(0); } while (0)
; template <class Epi, class Sched, bool ALIGN_EPI = false, bool SP2 = false, bool ABLK = false, bool BBLK = false>
; __device__ __forceinline__ void gemm_phase_f8(PG8_LAS unsigned char* lds, const Gemm g, const Sched& S, const Epi& E) {
;     ...
;             PG8_LDB(B0, 0, 0); PG8_LDB(B1, 0, 1); PG8_SCHED; PG8_LDA(At, 0, 0); PG8_STAGE(PG8_SA(1, 1), a1 + hstep, voffA);
;             PG8_WAIT_V(8); PG8_WAIT_L(0); PG8_BAR; PG8_MMA(0, 0, At, B0); PG8_MMA(0, 1, At, B1); PG8_BAR; PG8_SCHED;
;             PG8_LDA(At, 0, 1); PG8_STAGE(PG8_SB(0, 0), b2, voffB); PG8_STAGE(PG8_SB(0, 1), b2 + hstep, voffB); PG8_STAGE(PG8_SA(0, 0), a2, voffA);
;             PG8_WAIT_V(8); PG8_WAIT_L(0); PG8_BAR; PG8_MMA(1, 0, At, B0); PG8_MMA(1, 1, At, B1); PG8_BAR; PG8_SCHED;
;             PG8_LDB(B0, 1, 0); PG8_LDB(B1, 1, 1); PG8_SCHED; PG8_LDA(At, 1, 0); PG8_STAGE(PG8_SA(0, 1), a2 + hstep, voffA);
;             PG8_WAIT_V(8); PG8_WAIT_L(0); PG8_BAR; PG8_MMA(0, 0, At, B0); PG8_MMA(0, 1, At, B1); PG8_BAR; PG8_SCHED;
;             PG8_LDA(At, 1, 1); PG8_STAGE(PG8_SB(1, 0), b3, voffB); PG8_STAGE(PG8_SB(1, 1), b3 + hstep, voffB); PG8_STAGE(PG8_SA(1, 0), a3, voffA);
;             PG8_WAIT_V(8); PG8_WAIT_L(0); PG8_BAR; PG8_MMA(1, 0, At, B0); PG8_MMA(1, 1, At, B1); PG8_BAR; PG8_SCHED;
.LBB0_913:
	ds_read_b128 v[18:21], v189
	ds_read_b128 v[22:25], v189 offset:1024
	ds_read_b128 v[26:29], v189 offset:2048
	ds_read_b128 v[30:33], v189 offset:3072
	ds_read_b128 v[2:5], v190
	ds_read_b128 v[6:9], v190 offset:1024
	ds_read_b128 v[10:13], v190 offset:2048
	ds_read_b128 v[14:17], v190 offset:3072
	s_add_u32 s24, s22, 0xfff80080
	s_addc_u32 s25, s23, -1
	s_cmp_eq_u32 s49, 28
	s_cselect_b32 s27, s13, s25
	s_cselect_b32 s26, s45, s24
	s_cselect_b32 s25, s11, s48
	s_cselect_b32 s24, s46, s47
	v_lshl_add_u64 v[210:211], s[22:23], 0, v[174:175]
	s_add_i32 m0, s34, 0xc000
	ds_read_b128 v[180:183], v191
	ds_read_b128 v[184:187], v191 offset:1024
	ds_read_b128 v[194:197], v191 offset:2048
	ds_read_b128 v[198:201], v191 offset:3072
	ds_read_b128 v[202:205], v191 offset:4096
	ds_read_b128 v[206:209], v191 offset:5120
	ds_read_b128 v[218:221], v191 offset:6144
	ds_read_b128 v[222:225], v191 offset:7168
	global_load_lds_dwordx4 v[210:211], off
	v_lshl_add_u64 v[210:211], s[22:23], 0, v[172:173]
	s_add_i32 m0, s34, 0xe000
	s_nop 0
	global_load_lds_dwordx4 v[210:211], off
	s_waitcnt vmcnt(8)
	s_waitcnt lgkmcnt(0)
	s_barrier
	s_setprio 1
	s_waitcnt lgkmcnt(0)
	v_mfma_f32_16x16x128_f8f6f4 v[158:161], v[18:25], v[180:187], v[158:161]
	v_mfma_f32_16x16x128_f8f6f4 v[142:145], v[26:33], v[180:187], v[142:145]
	v_mfma_f32_16x16x128_f8f6f4 v[154:157], v[18:25], v[194:201], v[154:157]
	v_mfma_f32_16x16x128_f8f6f4 v[138:141], v[26:33], v[194:201], v[138:141]
	v_mfma_f32_16x16x128_f8f6f4 v[150:153], v[18:25], v[202:209], v[150:153]
	v_mfma_f32_16x16x128_f8f6f4 v[134:137], v[26:33], v[202:209], v[134:137]
	v_mfma_f32_16x16x128_f8f6f4 v[146:149], v[18:25], v[218:225], v[146:149]
	v_mfma_f32_16x16x128_f8f6f4 v[130:133], v[26:33], v[218:225], v[130:133]
	s_setprio 0
	s_setprio 1
	v_mfma_f32_16x16x128_f8f6f4 v[126:129], v[2:9], v[180:187], v[126:129]
	v_mfma_f32_16x16x128_f8f6f4 v[110:113], v[10:17], v[180:187], v[110:113]
	v_mfma_f32_16x16x128_f8f6f4 v[122:125], v[2:9], v[194:201], v[122:125]
	v_mfma_f32_16x16x128_f8f6f4 v[106:109], v[10:17], v[194:201], v[106:109]
	v_mfma_f32_16x16x128_f8f6f4 v[118:121], v[2:9], v[202:209], v[118:121]
	v_mfma_f32_16x16x128_f8f6f4 v[102:105], v[10:17], v[202:209], v[102:105]
	v_mfma_f32_16x16x128_f8f6f4 v[114:117], v[2:9], v[218:225], v[114:117]
	v_mfma_f32_16x16x128_f8f6f4 v[98:101], v[10:17], v[218:225], v[98:101]
	s_setprio 0
	s_barrier
	s_add_i32 s50, s41, s31
	v_lshl_add_u64 v[180:181], s[24:25], 0, v[166:167]
	s_mov_b32 m0, s50
	ds_read_b128 v[194:197], v191 offset:16384
	ds_read_b128 v[198:201], v191 offset:17408
	ds_read_b128 v[202:205], v191 offset:18432
	ds_read_b128 v[206:209], v191 offset:19456
	ds_read_b128 v[218:221], v191 offset:20480
	ds_read_b128 v[222:225], v191 offset:21504
	ds_read_b128 v[226:229], v191 offset:22528
	ds_read_b128 v[230:233], v191 offset:23552
	global_load_lds_dwordx4 v[180:181], off
	s_add_i32 m0, s50, 0x2000
	s_add_u32 s50, s24, 0x80000
	v_lshl_add_u64 v[182:183], s[24:25], 0, v[162:163]
	s_addc_u32 s51, s25, 0
	s_add_i32 s52, s42, s31
	global_load_lds_dwordx4 v[182:183], off
	v_lshl_add_u64 v[184:185], s[50:51], 0, v[166:167]
	s_mov_b32 m0, s52
	v_lshl_add_u64 v[186:187], s[26:27], 0, v[164:165]
	global_load_lds_dwordx4 v[184:185], off
	v_lshl_add_u64 v[184:185], s[50:51], 0, v[162:163]
	s_add_i32 m0, s52, 0x2000
	s_nop 0
	global_load_lds_dwordx4 v[184:185], off
	v_lshl_add_u64 v[184:185], s[26:27], 0, v[168:169]
	s_mov_b32 m0, s34
	s_nop 0
	global_load_lds_dwordx4 v[184:185], off
	s_mov_b32 m0, s35
	s_nop 0
	global_load_lds_dwordx4 v[186:187], off
	s_waitcnt vmcnt(8)
	s_waitcnt lgkmcnt(0)
	s_barrier
	s_setprio 1
	s_waitcnt lgkmcnt(0)
	v_mfma_f32_16x16x128_f8f6f4 v[94:97], v[18:25], v[194:201], v[94:97]
	v_mfma_f32_16x16x128_f8f6f4 v[78:81], v[26:33], v[194:201], v[78:81]
	v_mfma_f32_16x16x128_f8f6f4 v[90:93], v[18:25], v[202:209], v[90:93]
	v_mfma_f32_16x16x128_f8f6f4 v[74:77], v[26:33], v[202:209], v[74:77]
	v_mfma_f32_16x16x128_f8f6f4 v[86:89], v[18:25], v[218:225], v[86:89]
	v_mfma_f32_16x16x128_f8f6f4 v[70:73], v[26:33], v[218:225], v[70:73]
	v_mfma_f32_16x16x128_f8f6f4 v[82:85], v[18:25], v[226:233], v[82:85]
	v_mfma_f32_16x16x128_f8f6f4 v[66:69], v[26:33], v[226:233], v[66:69]
	s_setprio 0
	s_setprio 1
	v_mfma_f32_16x16x128_f8f6f4 v[62:65], v[2:9], v[194:201], v[62:65]
	v_mfma_f32_16x16x128_f8f6f4 v[46:49], v[10:17], v[194:201], v[46:49]
	v_mfma_f32_16x16x128_f8f6f4 v[58:61], v[2:9], v[202:209], v[58:61]
	v_mfma_f32_16x16x128_f8f6f4 v[42:45], v[10:17], v[202:209], v[42:45]
	v_mfma_f32_16x16x128_f8f6f4 v[54:57], v[2:9], v[218:225], v[54:57]
	v_mfma_f32_16x16x128_f8f6f4 v[38:41], v[10:17], v[218:225], v[38:41]
	v_mfma_f32_16x16x128_f8f6f4 v[50:53], v[2:9], v[226:233], v[50:53]
	v_mfma_f32_16x16x128_f8f6f4 v[34:37], v[10:17], v[226:233], v[34:37]
	s_setprio 0
	s_barrier
	s_add_i32 s50, 0, 0x18000
	s_add_i32 s51, 0, 0x1c000
	v_add_u32_e32 v14, s50, v188
	v_add_u32_e32 v30, s51, v188
	ds_read_b128 v[2:5], v14
	ds_read_b128 v[6:9], v14 offset:1024
	ds_read_b128 v[10:13], v14 offset:2048
	ds_read_b128 v[14:17], v14 offset:3072
	ds_read_b128 v[18:21], v30
	ds_read_b128 v[22:25], v30 offset:1024
	ds_read_b128 v[26:29], v30 offset:2048
	ds_read_b128 v[30:33], v30 offset:3072
	s_add_u32 s26, s26, 0x80000
	s_addc_u32 s27, s27, 0
	s_mov_b32 m0, s36
	v_lshl_add_u64 v[210:211], s[26:27], 0, v[168:169]
	ds_read_b128 v[194:197], v191 offset:32768
	ds_read_b128 v[198:201], v191 offset:33792
	ds_read_b128 v[202:205], v191 offset:34816
	ds_read_b128 v[206:209], v191 offset:35840
	ds_read_b128 v[218:221], v191 offset:36864
	ds_read_b128 v[222:225], v191 offset:37888
	ds_read_b128 v[226:229], v191 offset:38912
	ds_read_b128 v[230:233], v191 offset:39936
	global_load_lds_dwordx4 v[210:211], off
	v_lshl_add_u64 v[210:211], s[26:27], 0, v[164:165]
	s_mov_b32 m0, s37
	s_nop 0
	global_load_lds_dwordx4 v[210:211], off
	s_waitcnt vmcnt(8)
	s_waitcnt lgkmcnt(0)
	s_barrier
; #define PG8_STAGE(bufoff, gbase, voff) do { _Pragma("unroll") for (int _i = 0; _i < 2; ++_i) \
;         __builtin_amdgcn_global_load_lds((const unsigned*)((const char*)(gbase) + (voff)[_i]), (PG8_LAS unsigned*)(lds + (bufoff) + ldsw + _i * 8192), 16, 0, 0); } while (0)
; #define PG8_LDA(dst, b, h) do { _Pragma("unroll") for (int m = 0; m < 4; ++m) _Pragma("unroll") for (int k = 0; k < 2; ++k) dst[m][k] = *(const PG8_LAS bf16x8*)(lds + PG8_SA(b, h) + aoff + m * 2048 + k * 1024); } while (0)
; #define PG8_MMA(ai, bj, At, Bt) do { __builtin_amdgcn_s_setprio(1); _Pragma("unroll") for (int m = 0; m < 4; ++m) _Pragma("unroll") for (int n = 0; n < 2; ++n) _Pragma("unroll") for (int k = 0; k < 2; ++k) \
;         acc[ai][bj][m][n] = __builtin_amdgcn_mfma_f32_16x16x32_bf16(Bt[n][k], At[m][k], acc[ai][bj][m][n], 0, 0, 0); __builtin_amdgcn_s_setprio(0); } while (0)
; #define PG8_WAIT_V(n) asm volatile("s_waitcnt vmcnt(" #n ")" ::: "memory")
; #define PG8_WAIT_L(n) asm volatile("s_waitcnt lgkmcnt(" #n ")" ::: "memory")
; #define PG8_BAR __builtin_amdgcn_s_barrier()
; #define PG8_SCHED __builtin_amdgcn_sched_barrier(0)
; #define PG8_STAGE(bufoff, gbase, voff) do { _Pragma("unroll") for (int _i = 0; _i < 2; ++_i) \
;         __builtin_amdgcn_global_load_lds((const unsigned*)((const char*)(gbase) + (voff)[_i]), (PG8_LAS unsigned*)(lds + (bufoff) + ldsw + _i * 8192), 16, 0, 0); } while (0)
;     __device__ __forceinline__ void operator()(const f32x4 (&acc)[2][2][4][2], const Unit& u, int wr, int wc, int fr, int fq) const {
;     ...
;         for (int ai = 0; ai < 2; ++ai) { float rs4[4];
; #pragma unroll
;             for (int m = 0; m < 4; ++m) rs4[m] = rsqrtf(ss[u.pm * 256 + ai * HALF + wr * 64 + m * 16 + fr] * (1.0f / 4096.0f) + RMS_EPS) * (sc * 16.f);
; template <class Epi, class Sched, bool ALIGN_EPI = false, bool SP2 = false, bool ABLK = false, bool BBLK = false>
; __device__ __forceinline__ void gemm_phase_f8(PG8_LAS unsigned char* lds, const Gemm g, const Sched& S, const Epi& E) {
;     ...
;             PG8_WAIT_V(8); PG8_WAIT_L(0); PG8_BAR; PG8_MMA(0, 0, At, B0); PG8_MMA(0, 1, At, B1); PG8_BAR; PG8_SCHED;
;             PG8_LDA(At, 1, 1); PG8_STAGE(PG8_SB(1, 0), b3, voffB); PG8_STAGE(PG8_SB(1, 1), b3 + hstep, voffB); PG8_STAGE(PG8_SA(1, 0), a3, voffA);
;             PG8_WAIT_V(8); PG8_WAIT_L(0); PG8_BAR; PG8_MMA(1, 0, At, B0); PG8_MMA(1, 1, At, B1); PG8_BAR; PG8_SCHED;
	s_setprio 1
	s_waitcnt lgkmcnt(0)
	v_mfma_f32_16x16x128_f8f6f4 v[158:161], v[2:9], v[194:201], v[158:161]
	v_mfma_f32_16x16x128_f8f6f4 v[142:145], v[10:17], v[194:201], v[142:145]
	v_mfma_f32_16x16x128_f8f6f4 v[154:157], v[2:9], v[202:209], v[154:157]
	v_mfma_f32_16x16x128_f8f6f4 v[138:141], v[10:17], v[202:209], v[138:141]
	v_mfma_f32_16x16x128_f8f6f4 v[150:153], v[2:9], v[218:225], v[150:153]
	v_mfma_f32_16x16x128_f8f6f4 v[134:137], v[10:17], v[218:225], v[134:137]
	v_mfma_f32_16x16x128_f8f6f4 v[146:149], v[2:9], v[226:233], v[146:149]
	v_mfma_f32_16x16x128_f8f6f4 v[130:133], v[10:17], v[226:233], v[130:133]
	s_setprio 0
	s_setprio 1
	v_mfma_f32_16x16x128_f8f6f4 v[126:129], v[18:25], v[194:201], v[126:129]
	v_mfma_f32_16x16x128_f8f6f4 v[110:113], v[26:33], v[194:201], v[110:113]
	v_mfma_f32_16x16x128_f8f6f4 v[122:125], v[18:25], v[202:209], v[122:125]
	v_mfma_f32_16x16x128_f8f6f4 v[106:109], v[26:33], v[202:209], v[106:109]
	v_mfma_f32_16x16x128_f8f6f4 v[118:121], v[18:25], v[218:225], v[118:121]
	v_mfma_f32_16x16x128_f8f6f4 v[102:105], v[26:33], v[218:225], v[102:105]
	v_mfma_f32_16x16x128_f8f6f4 v[114:117], v[18:25], v[226:233], v[114:117]
	v_mfma_f32_16x16x128_f8f6f4 v[98:101], v[26:33], v[226:233], v[98:101]
	s_setprio 0
	s_barrier
	s_add_i32 s26, s50, s31
	v_lshl_add_u64 v[180:181], v[180:181], 0, s[4:5]
	s_mov_b32 m0, s26
	ds_read_b128 v[194:197], v191 offset:49152
	ds_read_b128 v[198:201], v191 offset:50176
	ds_read_b128 v[202:205], v191 offset:51200
	ds_read_b128 v[206:209], v191 offset:52224
	ds_read_b128 v[218:221], v191 offset:53248
	ds_read_b128 v[222:225], v191 offset:54272
	ds_read_b128 v[226:229], v191 offset:55296
	ds_read_b128 v[230:233], v191 offset:56320
	global_load_lds_dwordx4 v[180:181], off
	s_add_i32 m0, s26, 0x2000
	s_add_u32 s24, s24, 0x80800
	v_lshl_add_u64 v[180:181], v[182:183], 0, s[4:5]
	s_addc_u32 s25, s25, 0
	s_add_i32 s26, s51, s31
	global_load_lds_dwordx4 v[180:181], off
	v_lshl_add_u64 v[180:181], s[24:25], 0, v[166:167]
	s_mov_b32 m0, s26
	s_nop 0
	global_load_lds_dwordx4 v[180:181], off
	v_lshl_add_u64 v[180:181], s[24:25], 0, v[162:163]
	s_add_i32 m0, s26, 0x2000
	s_nop 0
	global_load_lds_dwordx4 v[180:181], off
	v_lshl_add_u64 v[180:181], v[184:185], 0, s[6:7]
	s_mov_b32 m0, s39
	s_nop 0
	global_load_lds_dwordx4 v[180:181], off
	v_lshl_add_u64 v[180:181], v[186:187], 0, s[6:7]
	s_mov_b32 m0, s40
	s_nop 0
	global_load_lds_dwordx4 v[180:181], off
	s_waitcnt vmcnt(8)
	s_waitcnt lgkmcnt(0)
	s_barrier
	s_setprio 1
	s_waitcnt lgkmcnt(0)
	v_mfma_f32_16x16x128_f8f6f4 v[94:97], v[2:9], v[194:201], v[94:97]
	v_mfma_f32_16x16x128_f8f6f4 v[78:81], v[10:17], v[194:201], v[78:81]
	v_mfma_f32_16x16x128_f8f6f4 v[90:93], v[2:9], v[202:209], v[90:93]
	v_mfma_f32_16x16x128_f8f6f4 v[74:77], v[10:17], v[202:209], v[74:77]
	v_mfma_f32_16x16x128_f8f6f4 v[86:89], v[2:9], v[218:225], v[86:89]
	v_mfma_f32_16x16x128_f8f6f4 v[70:73], v[10:17], v[218:225], v[70:73]
	v_mfma_f32_16x16x128_f8f6f4 v[82:85], v[2:9], v[226:233], v[82:85]
	v_mfma_f32_16x16x128_f8f6f4 v[66:69], v[10:17], v[226:233], v[66:69]
	s_setprio 0
	s_setprio 1
	v_mfma_f32_16x16x128_f8f6f4 v[62:65], v[18:25], v[194:201], v[62:65]
	v_mfma_f32_16x16x128_f8f6f4 v[46:49], v[26:33], v[194:201], v[46:49]
	v_mfma_f32_16x16x128_f8f6f4 v[58:61], v[18:25], v[202:209], v[58:61]
	v_mfma_f32_16x16x128_f8f6f4 v[42:45], v[26:33], v[202:209], v[42:45]
	v_mfma_f32_16x16x128_f8f6f4 v[54:57], v[18:25], v[218:225], v[54:57]
	v_mfma_f32_16x16x128_f8f6f4 v[38:41], v[26:33], v[218:225], v[38:41]
	v_mfma_f32_16x16x128_f8f6f4 v[50:53], v[18:25], v[226:233], v[50:53]
	v_mfma_f32_16x16x128_f8f6f4 v[34:37], v[26:33], v[226:233], v[34:37]
	s_setprio 0
	s_barrier
	s_add_i32 s49, s49, 2
	s_add_u32 s47, s47, 0x1000
	s_addc_u32 s48, s48, 0
	s_add_u32 s22, s22, 0x100
	s_addc_u32 s23, s23, 0
	s_cmp_lt_u32 s49, 30
	s_cbranch_scc1 .LBB0_913
	v_lshl_add_u32 v242, s18, 8, v1
	v_ashrrev_i32_e32 v243, 31, v242
	v_lshl_add_u64 v[244:245], v[242:243], 2, s[20:21]
	global_load_dword v234, v[244:245], off
	global_load_dword v235, v[244:245], off offset:64
	global_load_dword v236, v[244:245], off offset:128
	global_load_dword v237, v[244:245], off offset:192
	global_load_dword v238, v[244:245], off offset:512
	global_load_dword v239, v[244:245], off offset:576
	global_load_dword v240, v[244:245], off offset:640
	global_load_dword v241, v[244:245], off offset:704
	s_andn2_b64 vcc, exec, s[8:9]
	s_cbranch_vccnz .LBB0_916
	s_barrier
;     __device__ __forceinline__ void operator()(const f32x4 (&acc)[2][2][4][2], const Unit& u, int wr, int wc, int fr, int fq) const {
;     ...
;         for (int ai = 0; ai < 2; ++ai) { float rs4[4];
; #pragma unroll
;             for (int m = 0; m < 4; ++m) rs4[m] = rsqrtf(ss[u.pm * 256 + ai * HALF + wr * 64 + m * 16 + fr] * (1.0f / 4096.0f) + RMS_EPS) * (sc * 16.f);
;             const int T = (u.pm & 15) * 4 + ai * 2 + wr;
; #pragma unroll
;             for (int bj = 0; bj < 2; ++bj) { const int head = u.pn * 2 + bj;
;                 unsigned char* base = VT + (((size_t)b * 16 + head) * 64 + T) * 8192 + (wc * 32 + 8 * fq) * 64 + 32 * (fr >> 3) + 4 * (fr & 7);
; #pragma unroll
;                 for (int n = 0; n < 2; ++n)
; #pragma unroll
;                     for (int jj = 0; jj < 4; ++jj)
;                         *(unsigned*)(base + (4 * n + jj) * 64) = pk4_fp8(acc[ai][bj][0][n][jj] * rs4[0], acc[ai][bj][1][n][jj] * rs4[1], acc[ai][bj][2][n][jj] * rs4[2], acc[ai][bj][3][n][jj] * rs4[3]); } }
.LBB0_916:
	v_lshl_add_u32 v6, s18, 8, v1
	v_ashrrev_i32_e32 v7, 31, v6
	s_nop 15
	s_nop 15
	v_lshl_add_u64 v[2:3], v[6:7], 2, s[20:21]
	v_mov_b32_e32 v15, 0
	s_lshl_b32 s11, s18, 2
	s_lshl_b32 s22, s19, 1
	s_ashr_i32 s24, s18, 4
	s_and_b32 s11, s11, 60
	s_ashr_i32 s23, s22, 31
	s_add_i32 s18, s11, s30
	s_ashr_i32 s25, s24, 31
	s_lshl_b64 s[26:27], s[22:23], 19
	s_ashr_i32 s19, s18, 31
	s_lshl_b64 s[24:25], s[24:25], 23
	s_lshl_b64 s[18:19], s[18:19], 13
	v_mov_b32_e32 v17, 0
	s_or_b32 s22, s22, 1
	s_ashr_i32 s23, s22, 31
	s_lshl_b64 s[22:23], s[22:23], 19
	s_waitcnt vmcnt(0)
	v_fmamk_f32 v4, v234, 0x39800000, v192
	v_cmp_gt_f32_e32 vcc, s43, v4
	v_mul_f32_e32 v5, 0x4b800000, v4
	s_nop 0
	v_cndmask_b32_e32 v4, v4, v5, vcc
	v_rsq_f32_e32 v4, v4
	s_nop 0
	v_mul_f32_e32 v5, 0x45800000, v4
	v_cndmask_b32_e32 v4, v4, v5, vcc
	v_mul_f32_e32 v7, 0x3e800000, v4
	v_mul_f32_e32 v8, v158, v7
	v_med3_f32 v8, v8, s44, v193
	v_fmamk_f32 v4, v235, 0x39800000, v192
	v_cmp_gt_f32_e32 vcc, s43, v4
	v_mul_f32_e32 v5, 0x4b800000, v4
	s_nop 0
	v_cndmask_b32_e32 v4, v4, v5, vcc
	v_rsq_f32_e32 v4, v4
	s_nop 0
	v_mul_f32_e32 v5, 0x45800000, v4
	v_cndmask_b32_e32 v4, v4, v5, vcc
	v_mul_f32_e32 v10, 0x3e800000, v4
	v_mul_f32_e32 v9, v154, v10
	v_med3_f32 v9, v9, s44, v193
	v_cvt_pk_fp8_f32 v15, v8, v9
	v_mul_f32_e32 v8, v159, v7
	v_mul_f32_e32 v9, v155, v10
	v_med3_f32 v8, v8, s44, v193
	v_med3_f32 v9, v9, s44, v193
	v_fmamk_f32 v4, v236, 0x39800000, v192
	v_cmp_gt_f32_e32 vcc, s43, v4
	v_mul_f32_e32 v5, 0x4b800000, v4
	v_fmamk_f32 v2, v237, 0x39800000, v192
	v_cndmask_b32_e32 v4, v4, v5, vcc
	v_rsq_f32_e32 v4, v4
	v_mul_f32_e32 v3, 0x4b800000, v2
	v_mul_f32_e32 v5, 0x45800000, v4
	v_cndmask_b32_e32 v4, v4, v5, vcc
	v_cmp_gt_f32_e32 vcc, s43, v2
	v_mul_f32_e32 v11, 0x3e800000, v4
	v_mul_f32_e32 v13, v150, v11
	v_cndmask_b32_e32 v2, v2, v3, vcc
	v_rsq_f32_e32 v2, v2
	v_med3_f32 v13, v13, s44, v193
	v_mul_f32_e32 v3, 0x45800000, v2
	v_cndmask_b32_e32 v2, v2, v3, vcc
	v_mul_f32_e32 v12, 0x3e800000, v2
	v_mul_f32_e32 v14, v146, v12
	v_med3_f32 v14, v14, s44, v193
	v_cvt_pk_fp8_f32 v15, v13, v14 op_sel:[0,0,1]
	v_lshl_add_u64 v[2:3], v[170:171], 0, s[26:27]
	v_lshl_add_u64 v[4:5], v[2:3], 0, s[24:25]
	v_lshl_add_u64 v[2:3], v[4:5], 0, s[18:19]
	global_store_dword v[2:3], v15, off
	v_mov_b32_e32 v15, 0
	v_cvt_pk_fp8_f32 v15, v8, v9
	v_mul_f32_e32 v13, v151, v11
	v_mul_f32_e32 v14, v147, v12
	v_med3_f32 v13, v13, s44, v193
	v_med3_f32 v14, v14, s44, v193
	v_cvt_pk_fp8_f32 v15, v13, v14 op_sel:[0,0,1]
	v_mul_f32_e32 v8, v160, v7
	v_mul_f32_e32 v9, v156, v10
	v_med3_f32 v8, v8, s44, v193
	global_store_dword v[2:3], v15, off offset:64
	v_med3_f32 v9, v9, s44, v193
	v_mov_b32_e32 v15, 0
	v_cvt_pk_fp8_f32 v15, v8, v9
	v_mul_f32_e32 v13, v152, v11
	v_mul_f32_e32 v14, v148, v12
	v_med3_f32 v13, v13, s44, v193
	v_med3_f32 v14, v14, s44, v193
	v_cvt_pk_fp8_f32 v15, v13, v14 op_sel:[0,0,1]
	v_mul_f32_e32 v8, v161, v7
	v_mul_f32_e32 v9, v157, v10
	v_med3_f32 v8, v8, s44, v193
	global_store_dword v[2:3], v15, off offset:128
	v_med3_f32 v9, v9, s44, v193
	v_mov_b32_e32 v15, 0
	v_cvt_pk_fp8_f32 v15, v8, v9
	v_mul_f32_e32 v13, v153, v11
	v_mul_f32_e32 v14, v149, v12
	v_med3_f32 v13, v13, s44, v193
	v_med3_f32 v14, v14, s44, v193
	v_cvt_pk_fp8_f32 v15, v13, v14 op_sel:[0,0,1]
	v_mul_f32_e32 v8, v142, v7
	v_mul_f32_e32 v9, v138, v10
	v_med3_f32 v8, v8, s44, v193
	global_store_dword v[2:3], v15, off offset:192
	v_med3_f32 v9, v9, s44, v193
	v_mov_b32_e32 v15, 0
	v_cvt_pk_fp8_f32 v15, v8, v9
	v_mul_f32_e32 v13, v134, v11
	v_mul_f32_e32 v14, v130, v12
	v_med3_f32 v13, v13, s44, v193
	v_med3_f32 v14, v14, s44, v193
	v_cvt_pk_fp8_f32 v15, v13, v14 op_sel:[0,0,1]
	v_mul_f32_e32 v8, v143, v7
	v_mul_f32_e32 v9, v139, v10
	v_med3_f32 v8, v8, s44, v193
	global_store_dword v[2:3], v15, off offset:256
	v_med3_f32 v9, v9, s44, v193
	v_mov_b32_e32 v15, 0
	v_cvt_pk_fp8_f32 v15, v8, v9
	v_mul_f32_e32 v13, v135, v11
	v_mul_f32_e32 v14, v131, v12
	v_med3_f32 v13, v13, s44, v193
	v_med3_f32 v14, v14, s44, v193
	v_cvt_pk_fp8_f32 v15, v13, v14 op_sel:[0,0,1]
	v_mul_f32_e32 v8, v144, v7
	v_mul_f32_e32 v9, v140, v10
	v_med3_f32 v8, v8, s44, v193
	global_store_dword v[2:3], v15, off offset:320
	v_med3_f32 v9, v9, s44, v193
	v_mov_b32_e32 v15, 0
	v_cvt_pk_fp8_f32 v15, v8, v9
	v_mul_f32_e32 v13, v136, v11
	v_mul_f32_e32 v14, v132, v12
	v_med3_f32 v13, v13, s44, v193
	v_med3_f32 v14, v14, s44, v193
	v_cvt_pk_fp8_f32 v15, v13, v14 op_sel:[0,0,1]
	v_mul_f32_e32 v8, v145, v7
	v_mul_f32_e32 v9, v141, v10
	v_med3_f32 v8, v8, s44, v193
	global_store_dword v[2:3], v15, off offset:384
	v_med3_f32 v9, v9, s44, v193
	v_mov_b32_e32 v15, 0
	v_cvt_pk_fp8_f32 v15, v8, v9
	v_mul_f32_e32 v13, v137, v11
	v_mul_f32_e32 v14, v133, v12
	v_med3_f32 v13, v13, s44, v193
	v_med3_f32 v14, v14, s44, v193
	v_cvt_pk_fp8_f32 v15, v13, v14 op_sel:[0,0,1]
	v_mul_f32_e32 v13, v126, v7
	v_mul_f32_e32 v14, v122, v10
	v_med3_f32 v13, v13, s44, v193
	v_med3_f32 v14, v14, s44, v193
	v_cvt_pk_fp8_f32 v17, v13, v14
	global_store_dword v[2:3], v15, off offset:448
	v_mul_f32_e32 v15, v118, v11
	v_mul_f32_e32 v16, v114, v12
	v_med3_f32 v15, v15, s44, v193
	v_med3_f32 v16, v16, s44, v193
	v_cvt_pk_fp8_f32 v17, v15, v16 op_sel:[0,0,1]
	v_lshl_add_u64 v[2:3], v[170:171], 0, s[22:23]
	v_lshl_add_u64 v[2:3], v[2:3], 0, s[24:25]
	v_lshl_add_u64 v[8:9], v[2:3], 0, s[18:19]
	v_mul_f32_e32 v13, v127, v7
	v_mul_f32_e32 v14, v123, v10
	global_store_dword v[8:9], v17, off
	v_med3_f32 v13, v13, s44, v193
	v_med3_f32 v14, v14, s44, v193
	v_mov_b32_e32 v17, 0
	v_cvt_pk_fp8_f32 v17, v13, v14
	v_mul_f32_e32 v15, v119, v11
	v_mul_f32_e32 v16, v115, v12
;     __device__ __forceinline__ void operator()(const f32x4 (&acc)[2][2][4][2], const Unit& u, int wr, int wc, int fr, int fq) const {
;     ...
;         for (int ai = 0; ai < 2; ++ai) { float rs4[4];
; #pragma unroll
;             for (int m = 0; m < 4; ++m) rs4[m] = rsqrtf(ss[u.pm * 256 + ai * HALF + wr * 64 + m * 16 + fr] * (1.0f / 4096.0f) + RMS_EPS) * (sc * 16.f);
;             const int T = (u.pm & 15) * 4 + ai * 2 + wr;
; #pragma unroll
;             for (int bj = 0; bj < 2; ++bj) { const int head = u.pn * 2 + bj;
;                 unsigned char* base = VT + (((size_t)b * 16 + head) * 64 + T) * 8192 + (wc * 32 + 8 * fq) * 64 + 32 * (fr >> 3) + 4 * (fr & 7);
; #pragma unroll
;                 for (int n = 0; n < 2; ++n)
; #pragma unroll
;                     for (int jj = 0; jj < 4; ++jj)
;                         *(unsigned*)(base + (4 * n + jj) * 64) = pk4_fp8(acc[ai][bj][0][n][jj] * rs4[0], acc[ai][bj][1][n][jj] * rs4[1], acc[ai][bj][2][n][jj] * rs4[2], acc[ai][bj][3][n][jj] * rs4[3]); } }
	v_med3_f32 v15, v15, s44, v193
	v_med3_f32 v16, v16, s44, v193
	v_cvt_pk_fp8_f32 v17, v15, v16 op_sel:[0,0,1]
	v_mul_f32_e32 v13, v128, v7
	v_mul_f32_e32 v14, v124, v10
	v_med3_f32 v13, v13, s44, v193
	global_store_dword v[8:9], v17, off offset:64
	v_med3_f32 v14, v14, s44, v193
	v_mov_b32_e32 v17, 0
	v_cvt_pk_fp8_f32 v17, v13, v14
	v_mul_f32_e32 v15, v120, v11
	v_mul_f32_e32 v16, v116, v12
	v_med3_f32 v15, v15, s44, v193
	v_med3_f32 v16, v16, s44, v193
	v_cvt_pk_fp8_f32 v17, v15, v16 op_sel:[0,0,1]
	v_mul_f32_e32 v13, v129, v7
	v_mul_f32_e32 v14, v125, v10
	v_med3_f32 v13, v13, s44, v193
	global_store_dword v[8:9], v17, off offset:128
	v_med3_f32 v14, v14, s44, v193
	v_mov_b32_e32 v17, 0
	v_cvt_pk_fp8_f32 v17, v13, v14
	v_mul_f32_e32 v15, v121, v11
	v_mul_f32_e32 v16, v117, v12
	v_med3_f32 v15, v15, s44, v193
	v_med3_f32 v16, v16, s44, v193
	v_cvt_pk_fp8_f32 v17, v15, v16 op_sel:[0,0,1]
	v_mul_f32_e32 v13, v110, v7
	v_mul_f32_e32 v14, v106, v10
	v_med3_f32 v13, v13, s44, v193
	global_store_dword v[8:9], v17, off offset:192
	v_med3_f32 v14, v14, s44, v193
	v_mov_b32_e32 v17, 0
	v_cvt_pk_fp8_f32 v17, v13, v14
	v_mul_f32_e32 v15, v102, v11
	v_mul_f32_e32 v16, v98, v12
	v_med3_f32 v15, v15, s44, v193
	v_med3_f32 v16, v16, s44, v193
	v_cvt_pk_fp8_f32 v17, v15, v16 op_sel:[0,0,1]
	v_mul_f32_e32 v13, v111, v7
	v_mul_f32_e32 v14, v107, v10
	v_med3_f32 v13, v13, s44, v193
	global_store_dword v[8:9], v17, off offset:256
	v_med3_f32 v14, v14, s44, v193
	v_mov_b32_e32 v17, 0
	v_cvt_pk_fp8_f32 v17, v13, v14
	v_mul_f32_e32 v15, v103, v11
	v_mul_f32_e32 v16, v99, v12
	v_med3_f32 v15, v15, s44, v193
	v_med3_f32 v16, v16, s44, v193
	v_cvt_pk_fp8_f32 v17, v15, v16 op_sel:[0,0,1]
	v_mul_f32_e32 v13, v112, v7
	v_mul_f32_e32 v14, v108, v10
	v_med3_f32 v13, v13, s44, v193
	global_store_dword v[8:9], v17, off offset:320
	v_med3_f32 v14, v14, s44, v193
	v_mov_b32_e32 v17, 0
	v_mul_f32_e32 v7, v113, v7
	v_mul_f32_e32 v10, v109, v10
	v_cvt_pk_fp8_f32 v17, v13, v14
	v_med3_f32 v7, v7, s44, v193
	v_med3_f32 v10, v10, s44, v193
	v_mov_b32_e32 v13, 0
	v_cvt_pk_fp8_f32 v13, v7, v10
	v_mul_f32_e32 v15, v104, v11
	v_mul_f32_e32 v16, v100, v12
	v_mul_f32_e32 v11, v105, v11
	v_mul_f32_e32 v12, v101, v12
	v_med3_f32 v15, v15, s44, v193
	v_med3_f32 v16, v16, s44, v193
	v_med3_f32 v11, v11, s44, v193
	v_med3_f32 v12, v12, s44, v193
	v_cvt_pk_fp8_f32 v17, v15, v16 op_sel:[0,0,1]
	v_cvt_pk_fp8_f32 v13, v11, v12 op_sel:[0,0,1]
	v_add_u32_e32 v10, 0xa0, v6
	v_ashrrev_i32_e32 v11, 31, v10
	global_store_dword v[8:9], v17, off offset:384
	global_store_dword v[8:9], v13, off offset:448
	v_add_u32_e32 v8, 0x80, v6
	v_ashrrev_i32_e32 v9, 31, v8
	v_lshl_add_u64 v[8:9], v[8:9], 2, s[20:21]
	v_lshl_add_u64 v[10:11], v[10:11], 2, s[20:21]
	v_mov_b32_e32 v14, 0
	s_add_u32 s18, s18, 0x4000
	s_addc_u32 s19, s19, 0
	v_lshl_add_u64 v[4:5], v[4:5], 0, s[18:19]
	v_lshl_add_u64 v[2:3], v[2:3], 0, s[18:19]
	s_mov_b64 s[18:19], -1
	v_fmamk_f32 v7, v238, 0x39800000, v192
	v_cmp_gt_f32_e32 vcc, s43, v7
	v_mul_f32_e32 v8, 0x4b800000, v7
	s_nop 0
	v_cndmask_b32_e32 v7, v7, v8, vcc
	v_rsq_f32_e32 v7, v7
	s_nop 0
	v_mul_f32_e32 v8, 0x45800000, v7
	v_cndmask_b32_e32 v7, v7, v8, vcc
	v_add_u32_e32 v8, 0x90, v6
	v_ashrrev_i32_e32 v9, 31, v8
	v_lshl_add_u64 v[8:9], v[8:9], 2, s[20:21]
	v_mul_f32_e32 v7, 0x3e800000, v7
	v_fmamk_f32 v8, v239, 0x39800000, v192
	v_cmp_gt_f32_e32 vcc, s43, v8
	v_mul_f32_e32 v9, 0x4b800000, v8
	s_nop 0
	v_cndmask_b32_e32 v8, v8, v9, vcc
	v_rsq_f32_e32 v8, v8
	s_nop 0
	v_mul_f32_e32 v9, 0x45800000, v8
	v_cndmask_b32_e32 v8, v8, v9, vcc
	v_mul_f32_e32 v8, 0x3e800000, v8
	v_fmamk_f32 v9, v240, 0x39800000, v192
	v_cmp_gt_f32_e32 vcc, s43, v9
	v_mul_f32_e32 v10, 0x4b800000, v9
	s_nop 0
	v_cndmask_b32_e32 v9, v9, v10, vcc
	v_rsq_f32_e32 v9, v9
	s_nop 0
	v_mul_f32_e32 v10, 0x45800000, v9
	v_cndmask_b32_e32 v9, v9, v10, vcc
	v_add_u32_e32 v10, 0xb0, v6
	v_ashrrev_i32_e32 v11, 31, v10
	v_lshl_add_u64 v[10:11], v[10:11], 2, s[20:21]
	v_mul_f32_e32 v11, v90, v8
	v_med3_f32 v11, v11, s44, v193
	v_mul_f32_e32 v9, 0x3e800000, v9
	v_mul_f32_e32 v12, v86, v9
	v_med3_f32 v12, v12, s44, v193
	v_fmamk_f32 v6, v241, 0x39800000, v192
	v_cmp_gt_f32_e32 vcc, s43, v6
	v_mul_f32_e32 v10, 0x4b800000, v6
	s_nop 0
	v_cndmask_b32_e32 v6, v6, v10, vcc
	v_rsq_f32_e32 v6, v6
	s_nop 0
	v_mul_f32_e32 v10, 0x45800000, v6
	v_cndmask_b32_e32 v6, v6, v10, vcc
	v_mul_f32_e32 v10, v94, v7
	v_med3_f32 v10, v10, s44, v193
	v_cvt_pk_fp8_f32 v14, v10, v11
	v_mul_f32_e32 v6, 0x3e800000, v6
	v_mul_f32_e32 v13, v82, v6
	v_med3_f32 v13, v13, s44, v193
	v_cvt_pk_fp8_f32 v14, v12, v13 op_sel:[0,0,1]
	v_mul_f32_e32 v10, v95, v7
	v_mul_f32_e32 v11, v91, v8
	v_med3_f32 v10, v10, s44, v193
	global_store_dword v[4:5], v14, off
	v_med3_f32 v11, v11, s44, v193
	v_mov_b32_e32 v14, 0
	v_cvt_pk_fp8_f32 v14, v10, v11
	v_mul_f32_e32 v12, v87, v9
	v_mul_f32_e32 v13, v83, v6
	v_med3_f32 v12, v12, s44, v193
	v_med3_f32 v13, v13, s44, v193
	v_cvt_pk_fp8_f32 v14, v12, v13 op_sel:[0,0,1]
	v_mul_f32_e32 v10, v96, v7
	v_mul_f32_e32 v11, v92, v8
	v_med3_f32 v10, v10, s44, v193
	global_store_dword v[4:5], v14, off offset:64
	v_med3_f32 v11, v11, s44, v193
	v_mov_b32_e32 v14, 0
	v_cvt_pk_fp8_f32 v14, v10, v11
	v_mul_f32_e32 v12, v88, v9
	v_mul_f32_e32 v13, v84, v6
;     __device__ __forceinline__ void operator()(const f32x4 (&acc)[2][2][4][2], const Unit& u, int wr, int wc, int fr, int fq) const {
;     ...
;             for (int bj = 0; bj < 2; ++bj) { const int head = u.pn * 2 + bj;
;                 unsigned char* base = VT + (((size_t)b * 16 + head) * 64 + T) * 8192 + (wc * 32 + 8 * fq) * 64 + 32 * (fr >> 3) + 4 * (fr & 7);
; #pragma unroll
;                 for (int n = 0; n < 2; ++n)
; #pragma unroll
;                     for (int jj = 0; jj < 4; ++jj)
;                         *(unsigned*)(base + (4 * n + jj) * 64) = pk4_fp8(acc[ai][bj][0][n][jj] * rs4[0], acc[ai][bj][1][n][jj] * rs4[1], acc[ai][bj][2][n][jj] * rs4[2], acc[ai][bj][3][n][jj] * rs4[3]); } }
	v_med3_f32 v12, v12, s44, v193
	v_med3_f32 v13, v13, s44, v193
	v_cvt_pk_fp8_f32 v14, v12, v13 op_sel:[0,0,1]
	v_mul_f32_e32 v10, v97, v7
	v_mul_f32_e32 v11, v93, v8
	v_med3_f32 v10, v10, s44, v193
	global_store_dword v[4:5], v14, off offset:128
	v_med3_f32 v11, v11, s44, v193
	v_mov_b32_e32 v14, 0
	v_cvt_pk_fp8_f32 v14, v10, v11
	v_mul_f32_e32 v12, v89, v9
	v_mul_f32_e32 v13, v85, v6
	v_med3_f32 v12, v12, s44, v193
	v_med3_f32 v13, v13, s44, v193
	v_cvt_pk_fp8_f32 v14, v12, v13 op_sel:[0,0,1]
	v_mul_f32_e32 v10, v78, v7
	v_mul_f32_e32 v11, v74, v8
	v_med3_f32 v10, v10, s44, v193
	global_store_dword v[4:5], v14, off offset:192
	v_med3_f32 v11, v11, s44, v193
	v_mov_b32_e32 v14, 0
	v_cvt_pk_fp8_f32 v14, v10, v11
	v_mul_f32_e32 v12, v70, v9
	v_mul_f32_e32 v13, v66, v6
	v_med3_f32 v12, v12, s44, v193
	v_med3_f32 v13, v13, s44, v193
	v_cvt_pk_fp8_f32 v14, v12, v13 op_sel:[0,0,1]
	v_mul_f32_e32 v10, v79, v7
	v_mul_f32_e32 v11, v75, v8
	v_med3_f32 v10, v10, s44, v193
	global_store_dword v[4:5], v14, off offset:256
	v_med3_f32 v11, v11, s44, v193
	v_mov_b32_e32 v14, 0
	v_cvt_pk_fp8_f32 v14, v10, v11
	v_mul_f32_e32 v12, v71, v9
	v_mul_f32_e32 v13, v67, v6
	v_med3_f32 v12, v12, s44, v193
	v_med3_f32 v13, v13, s44, v193
	v_cvt_pk_fp8_f32 v14, v12, v13 op_sel:[0,0,1]
	v_mul_f32_e32 v10, v80, v7
	v_mul_f32_e32 v11, v76, v8
	v_med3_f32 v10, v10, s44, v193
	global_store_dword v[4:5], v14, off offset:320
	v_med3_f32 v11, v11, s44, v193
	v_mov_b32_e32 v14, 0
	v_cvt_pk_fp8_f32 v14, v10, v11
	v_mul_f32_e32 v12, v72, v9
	v_mul_f32_e32 v13, v68, v6
	v_med3_f32 v12, v12, s44, v193
	v_med3_f32 v13, v13, s44, v193
	v_cvt_pk_fp8_f32 v14, v12, v13 op_sel:[0,0,1]
	v_mul_f32_e32 v10, v81, v7
	v_mul_f32_e32 v11, v77, v8
	v_med3_f32 v10, v10, s44, v193
	global_store_dword v[4:5], v14, off offset:384
	v_med3_f32 v11, v11, s44, v193
	v_mov_b32_e32 v14, 0
	v_cvt_pk_fp8_f32 v14, v10, v11
	v_mul_f32_e32 v12, v73, v9
	v_mul_f32_e32 v13, v69, v6
	v_med3_f32 v12, v12, s44, v193
	v_med3_f32 v13, v13, s44, v193
	v_cvt_pk_fp8_f32 v14, v12, v13 op_sel:[0,0,1]
	v_mov_b32_e32 v12, 0
	v_mul_f32_e32 v10, v54, v9
	v_mul_f32_e32 v11, v50, v6
	global_store_dword v[4:5], v14, off offset:448
	v_mul_f32_e32 v4, v62, v7
	v_mul_f32_e32 v5, v58, v8
	v_med3_f32 v4, v4, s44, v193
	v_med3_f32 v5, v5, s44, v193
	v_cvt_pk_fp8_f32 v12, v4, v5
	v_med3_f32 v10, v10, s44, v193
	v_med3_f32 v11, v11, s44, v193
	v_mul_f32_e32 v4, v63, v7
	v_cvt_pk_fp8_f32 v12, v10, v11 op_sel:[0,0,1]
	v_mul_f32_e32 v5, v59, v8
	v_med3_f32 v4, v4, s44, v193
	v_med3_f32 v5, v5, s44, v193
	global_store_dword v[2:3], v12, off
	v_mov_b32_e32 v12, 0
	v_cvt_pk_fp8_f32 v12, v4, v5
	v_mul_f32_e32 v10, v55, v9
	v_mul_f32_e32 v11, v51, v6
	v_med3_f32 v10, v10, s44, v193
	v_med3_f32 v11, v11, s44, v193
	v_cvt_pk_fp8_f32 v12, v10, v11 op_sel:[0,0,1]
	v_mul_f32_e32 v4, v64, v7
	v_mul_f32_e32 v5, v60, v8
	v_med3_f32 v4, v4, s44, v193
	global_store_dword v[2:3], v12, off offset:64
	v_med3_f32 v5, v5, s44, v193
	v_mov_b32_e32 v12, 0
	v_cvt_pk_fp8_f32 v12, v4, v5
	v_mul_f32_e32 v10, v56, v9
	v_mul_f32_e32 v11, v52, v6
	v_med3_f32 v10, v10, s44, v193
	v_med3_f32 v11, v11, s44, v193
	v_cvt_pk_fp8_f32 v12, v10, v11 op_sel:[0,0,1]
	v_mul_f32_e32 v4, v65, v7
	v_mul_f32_e32 v5, v61, v8
	v_med3_f32 v4, v4, s44, v193
	global_store_dword v[2:3], v12, off offset:128
	v_med3_f32 v5, v5, s44, v193
	v_mov_b32_e32 v12, 0
	v_cvt_pk_fp8_f32 v12, v4, v5
	v_mul_f32_e32 v10, v57, v9
	v_mul_f32_e32 v11, v53, v6
	v_med3_f32 v10, v10, s44, v193
	v_med3_f32 v11, v11, s44, v193
	v_cvt_pk_fp8_f32 v12, v10, v11 op_sel:[0,0,1]
	v_mul_f32_e32 v4, v46, v7
	v_mul_f32_e32 v5, v42, v8
	v_med3_f32 v4, v4, s44, v193
	global_store_dword v[2:3], v12, off offset:192
	v_med3_f32 v5, v5, s44, v193
	v_mov_b32_e32 v12, 0
	v_cvt_pk_fp8_f32 v12, v4, v5
	v_mul_f32_e32 v10, v38, v9
	v_mul_f32_e32 v11, v34, v6
	v_med3_f32 v10, v10, s44, v193
	v_med3_f32 v11, v11, s44, v193
	v_cvt_pk_fp8_f32 v12, v10, v11 op_sel:[0,0,1]
	v_mul_f32_e32 v4, v47, v7
	v_mul_f32_e32 v5, v43, v8
	v_med3_f32 v4, v4, s44, v193
	global_store_dword v[2:3], v12, off offset:256
	v_med3_f32 v5, v5, s44, v193
	v_mov_b32_e32 v12, 0
	v_cvt_pk_fp8_f32 v12, v4, v5
	v_mul_f32_e32 v10, v39, v9
	v_mul_f32_e32 v11, v35, v6
	v_med3_f32 v10, v10, s44, v193
	v_med3_f32 v11, v11, s44, v193
	v_cvt_pk_fp8_f32 v12, v10, v11 op_sel:[0,0,1]
	v_mul_f32_e32 v4, v48, v7
	v_mul_f32_e32 v5, v44, v8
	v_med3_f32 v4, v4, s44, v193
	global_store_dword v[2:3], v12, off offset:320
	v_med3_f32 v5, v5, s44, v193
	v_mov_b32_e32 v12, 0
	v_cvt_pk_fp8_f32 v12, v4, v5
	v_mul_f32_e32 v4, v49, v7
	v_mul_f32_e32 v5, v45, v8
	v_med3_f32 v4, v4, s44, v193
	v_med3_f32 v5, v5, s44, v193
	v_mov_b32_e32 v8, 0
	v_cvt_pk_fp8_f32 v8, v4, v5
	v_mul_f32_e32 v10, v40, v9
	v_mul_f32_e32 v11, v36, v6
	v_mul_f32_e32 v7, v41, v9
	v_mul_f32_e32 v6, v37, v6
	v_med3_f32 v10, v10, s44, v193
	v_med3_f32 v11, v11, s44, v193
	v_med3_f32 v7, v7, s44, v193
	v_med3_f32 v6, v6, s44, v193
	v_cvt_pk_fp8_f32 v12, v10, v11 op_sel:[0,0,1]
	v_cvt_pk_fp8_f32 v8, v7, v6 op_sel:[0,0,1]
	s_and_b64 vcc, exec, s[0:1]
	global_store_dword v[2:3], v12, off offset:384
	global_store_dword v[2:3], v8, off offset:448
	s_cbranch_vccz .LBB0_905
	s_andn2_b64 vcc, exec, s[2:3]
	s_cbranch_vccnz .LBB0_904
	s_barrier
	s_branch .LBB0_904

; #define GAS __attribute__((address_space(1)))
; #define LAS __attribute__((address_space(3)))
; #define LDS_WAIT() asm volatile("s_waitcnt lgkmcnt(0)" ::: "memory")
;     ...
;     for (int i = 0; i < 16; ++i) { const int kk = 4 * i + kq;
;         f32x4 v = __builtin_nontemporal_load((const GAS f32x4*)(W + (size_t)(k0 + kk) * ldw + n0 + 4 * c4));
;         v = v * (gk ? gk[k0 + kk] * scale : scale);
;         LAS float* d = scr + kk * 65 + 4 * c4; d[0] = v[0]; d[1] = v[1]; d[2] = v[2]; d[3] = v[3]; }
;     LDS_WAIT(); asm volatile("" ::: "memory");
.LBB0_1003:
	s_mov_b32 s100, 0x10000
	s_mov_b32 s101, 0
	global_load_dwordx4 v[64:67], v[8:9], off nt
	v_lshl_add_u64 v[8:9], v[8:9], 0, s[100:101]
	global_load_dwordx4 v[68:71], v[8:9], off nt
	v_lshl_add_u64 v[8:9], v[8:9], 0, s[100:101]
	global_load_dwordx4 v[72:75], v[8:9], off nt
	v_lshl_add_u64 v[8:9], v[8:9], 0, s[100:101]
	global_load_dwordx4 v[76:79], v[8:9], off nt
	v_lshl_add_u64 v[8:9], v[8:9], 0, s[100:101]
	global_load_dwordx4 v[80:83], v[8:9], off nt
	v_lshl_add_u64 v[8:9], v[8:9], 0, s[100:101]
	global_load_dwordx4 v[84:87], v[8:9], off nt
	v_lshl_add_u64 v[8:9], v[8:9], 0, s[100:101]
	global_load_dwordx4 v[88:91], v[8:9], off nt
	v_lshl_add_u64 v[8:9], v[8:9], 0, s[100:101]
	global_load_dwordx4 v[92:95], v[8:9], off nt
	v_lshl_add_u64 v[8:9], v[8:9], 0, s[100:101]
	global_load_dwordx4 v[96:99], v[8:9], off nt
	v_lshl_add_u64 v[8:9], v[8:9], 0, s[100:101]
	global_load_dwordx4 v[100:103], v[8:9], off nt
	v_lshl_add_u64 v[8:9], v[8:9], 0, s[100:101]
	global_load_dwordx4 v[104:107], v[8:9], off nt
	v_lshl_add_u64 v[8:9], v[8:9], 0, s[100:101]
	global_load_dwordx4 v[108:111], v[8:9], off nt
	v_lshl_add_u64 v[8:9], v[8:9], 0, s[100:101]
	global_load_dwordx4 v[112:115], v[8:9], off nt
	v_lshl_add_u64 v[8:9], v[8:9], 0, s[100:101]
	global_load_dwordx4 v[116:119], v[8:9], off nt
	v_lshl_add_u64 v[8:9], v[8:9], 0, s[100:101]
	global_load_dwordx4 v[120:123], v[8:9], off nt
	v_lshl_add_u64 v[8:9], v[8:9], 0, s[100:101]
	global_load_dwordx4 v[124:127], v[8:9], off nt
	s_waitcnt vmcnt(15)
	v_pk_mul_f32 v[64:65], v[64:65], s[92:93] op_sel_hi:[1,0]
	v_pk_mul_f32 v[66:67], v[66:67], s[92:93] op_sel_hi:[1,0]
	ds_write2_b32 v11, v64, v65 offset1:1
	ds_write2_b32 v11, v66, v67 offset0:2 offset1:3
	s_waitcnt vmcnt(14)
	v_pk_mul_f32 v[68:69], v[68:69], s[92:93] op_sel_hi:[1,0]
	v_pk_mul_f32 v[70:71], v[70:71], s[92:93] op_sel_hi:[1,0]
	v_add_u32_e32 v2, 0x410, v11
	ds_write2_b32 v2, v68, v69 offset1:1
	ds_write2_b32 v2, v70, v71 offset0:2 offset1:3
	s_waitcnt vmcnt(13)
	v_pk_mul_f32 v[72:73], v[72:73], s[92:93] op_sel_hi:[1,0]
	v_pk_mul_f32 v[74:75], v[74:75], s[92:93] op_sel_hi:[1,0]
	v_add_u32_e32 v2, 0x820, v11
	ds_write2_b32 v2, v72, v73 offset1:1
	ds_write2_b32 v2, v74, v75 offset0:2 offset1:3
	s_waitcnt vmcnt(12)
	v_pk_mul_f32 v[76:77], v[76:77], s[92:93] op_sel_hi:[1,0]
	v_pk_mul_f32 v[78:79], v[78:79], s[92:93] op_sel_hi:[1,0]
	v_add_u32_e32 v2, 0xc30, v11
	ds_write2_b32 v2, v76, v77 offset1:1
	ds_write2_b32 v2, v78, v79 offset0:2 offset1:3
	s_waitcnt vmcnt(11)
	v_pk_mul_f32 v[80:81], v[80:81], s[92:93] op_sel_hi:[1,0]
	v_pk_mul_f32 v[82:83], v[82:83], s[92:93] op_sel_hi:[1,0]
	v_add_u32_e32 v2, 0x1040, v11
	ds_write2_b32 v2, v80, v81 offset1:1
	ds_write2_b32 v2, v82, v83 offset0:2 offset1:3
	s_waitcnt vmcnt(10)
	v_pk_mul_f32 v[84:85], v[84:85], s[92:93] op_sel_hi:[1,0]
	v_pk_mul_f32 v[86:87], v[86:87], s[92:93] op_sel_hi:[1,0]
	v_add_u32_e32 v2, 0x1450, v11
	ds_write2_b32 v2, v84, v85 offset1:1
	ds_write2_b32 v2, v86, v87 offset0:2 offset1:3
	s_waitcnt vmcnt(9)
	v_pk_mul_f32 v[88:89], v[88:89], s[92:93] op_sel_hi:[1,0]
	v_pk_mul_f32 v[90:91], v[90:91], s[92:93] op_sel_hi:[1,0]
	v_add_u32_e32 v2, 0x1860, v11
	ds_write2_b32 v2, v88, v89 offset1:1
	ds_write2_b32 v2, v90, v91 offset0:2 offset1:3
	s_waitcnt vmcnt(8)
	v_pk_mul_f32 v[92:93], v[92:93], s[92:93] op_sel_hi:[1,0]
	v_pk_mul_f32 v[94:95], v[94:95], s[92:93] op_sel_hi:[1,0]
	v_add_u32_e32 v2, 0x1c70, v11
	ds_write2_b32 v2, v92, v93 offset1:1
	ds_write2_b32 v2, v94, v95 offset0:2 offset1:3
	s_waitcnt vmcnt(7)
	v_pk_mul_f32 v[96:97], v[96:97], s[92:93] op_sel_hi:[1,0]
	v_pk_mul_f32 v[98:99], v[98:99], s[92:93] op_sel_hi:[1,0]
	v_add_u32_e32 v2, 0x2080, v11
	ds_write2_b32 v2, v96, v97 offset1:1
	ds_write2_b32 v2, v98, v99 offset0:2 offset1:3
	s_waitcnt vmcnt(6)
	v_pk_mul_f32 v[100:101], v[100:101], s[92:93] op_sel_hi:[1,0]
	v_pk_mul_f32 v[102:103], v[102:103], s[92:93] op_sel_hi:[1,0]
	v_add_u32_e32 v2, 0x2490, v11
	ds_write2_b32 v2, v100, v101 offset1:1
	ds_write2_b32 v2, v102, v103 offset0:2 offset1:3
	s_waitcnt vmcnt(5)
	v_pk_mul_f32 v[104:105], v[104:105], s[92:93] op_sel_hi:[1,0]
	v_pk_mul_f32 v[106:107], v[106:107], s[92:93] op_sel_hi:[1,0]
	v_add_u32_e32 v2, 0x28a0, v11
	ds_write2_b32 v2, v104, v105 offset1:1
	ds_write2_b32 v2, v106, v107 offset0:2 offset1:3
	s_waitcnt vmcnt(4)
	v_pk_mul_f32 v[108:109], v[108:109], s[92:93] op_sel_hi:[1,0]
	v_pk_mul_f32 v[110:111], v[110:111], s[92:93] op_sel_hi:[1,0]
	v_add_u32_e32 v2, 0x2cb0, v11
	ds_write2_b32 v2, v108, v109 offset1:1
	ds_write2_b32 v2, v110, v111 offset0:2 offset1:3
	s_waitcnt vmcnt(3)
	v_pk_mul_f32 v[112:113], v[112:113], s[92:93] op_sel_hi:[1,0]
	v_pk_mul_f32 v[114:115], v[114:115], s[92:93] op_sel_hi:[1,0]
	v_add_u32_e32 v2, 0x30c0, v11
	ds_write2_b32 v2, v112, v113 offset1:1
	ds_write2_b32 v2, v114, v115 offset0:2 offset1:3
	s_waitcnt vmcnt(2)
	v_pk_mul_f32 v[116:117], v[116:117], s[92:93] op_sel_hi:[1,0]
	v_pk_mul_f32 v[118:119], v[118:119], s[92:93] op_sel_hi:[1,0]
	v_add_u32_e32 v2, 0x34d0, v11
	ds_write2_b32 v2, v116, v117 offset1:1
	ds_write2_b32 v2, v118, v119 offset0:2 offset1:3
	s_waitcnt vmcnt(1)
	v_pk_mul_f32 v[120:121], v[120:121], s[92:93] op_sel_hi:[1,0]
	v_pk_mul_f32 v[122:123], v[122:123], s[92:93] op_sel_hi:[1,0]
	v_add_u32_e32 v2, 0x38e0, v11
	ds_write2_b32 v2, v120, v121 offset1:1
	ds_write2_b32 v2, v122, v123 offset0:2 offset1:3
	s_waitcnt vmcnt(0)
	v_pk_mul_f32 v[124:125], v[124:125], s[92:93] op_sel_hi:[1,0]
	v_pk_mul_f32 v[126:127], v[126:127], s[92:93] op_sel_hi:[1,0]
	v_add_u32_e32 v2, 0x3cf0, v11
	ds_write2_b32 v2, v124, v125 offset1:1
	ds_write2_b32 v2, v126, v127 offset0:2 offset1:3
	v_and_b32_e32 v2, 48, v10
	s_waitcnt lgkmcnt(0)
; #define GAS __attribute__((address_space(1)))
; #define LAS __attribute__((address_space(3)))
; #define LDS_WAIT() asm volatile("s_waitcnt lgkmcnt(0)" ::: "memory")
;     ...
;     LDS_WAIT(); asm volatile("" ::: "memory");
;     const int c = lane & 3;
; #pragma unroll
;     for (int j = 0; j < 4; ++j) { const int n = (lane >> 2) + 16 * j; const LAS float* s = scr + (16 * c) * 65 + n;
;         v4u o; o.x = pg8::pk4_fp8(s[0 * 65], s[1 * 65], s[2 * 65], s[3 * 65]); o.y = pg8::pk4_fp8(s[4 * 65], s[5 * 65], s[6 * 65], s[7 * 65]);
;         o.z = pg8::pk4_fp8(s[8 * 65], s[9 * 65], s[10 * 65], s[11 * 65]); o.w = pg8::pk4_fp8(s[12 * 65], s[13 * 65], s[14 * 65], s[15 * 65]);
;         *(GAS v4u*)(WT + ((size_t)((n0 + n) >> 4) * (K >> 5) + ((k0 + 16 * c) >> 5)) * 512 + ((n0 + n) & 15) * 32 + ((16 * c) & 31)) = o; }
;     LDS_WAIT(); asm volatile("" ::: "memory");
	v_mul_u32_u24_e32 v8, 0x104, v2
	v_and_b32_e32 v9, -4, v23
	v_add3_u32 v48, s82, v8, v9
	v_and_b32_e32 v6, 16, v10
	ds_read2_b32 v[10:11], v48 offset1:16
	v_ashrrev_i32_e32 v22, 2, v23
	v_lshlrev_b32_e32 v4, 5, v22
	v_readlane_b32 s18, v253, 56
	v_and_b32_e32 v4, 0x1e0, v4
	v_mov_b32_e32 v5, v3
	v_readlane_b32 s19, v253, 57
	ds_read2_b32 v[12:13], v48 offset0:65 offset1:81
	ds_read2_b32 v[14:15], v48 offset0:130 offset1:146
	ds_read2_b32 v[16:17], v48 offset0:195 offset1:211
	v_lshl_add_u64 v[4:5], s[18:19], 0, v[4:5]
	v_mov_b32_e32 v7, v3
	v_lshl_add_u64 v[4:5], v[4:5], 0, v[6:7]
	s_waitcnt lgkmcnt(3)
	v_max_f32_e32 v6, v10, v10
	v_med3_f32 v7, v6, s95, v199
	s_waitcnt lgkmcnt(2)
	v_max_f32_e32 v6, v12, v12
	v_med3_f32 v8, v6, s95, v199
	s_waitcnt lgkmcnt(1)
	v_max_f32_e32 v6, v14, v14
	v_add_u32_e32 v49, 0x400, v48
	v_med3_f32 v9, v6, s95, v199
	v_mov_b32_e32 v6, v3
	ds_read2_b32 v[18:19], v49 offset0:4 offset1:20
	v_cvt_pk_fp8_f32 v6, v7, v8
	s_waitcnt lgkmcnt(1)
	v_max_f32_e32 v10, v16, v16
	ds_read2_b32 v[20:21], v49 offset0:69 offset1:85
	ds_read2_b32 v[24:25], v49 offset0:134 offset1:150
	ds_read2_b32 v[26:27], v49 offset0:199 offset1:215
	v_med3_f32 v7, v10, s95, v199
	v_cvt_pk_fp8_f32 v6, v9, v7 op_sel:[0,0,1]
	s_waitcnt lgkmcnt(3)
	v_max_f32_e32 v7, v18, v18
	v_med3_f32 v8, v7, s95, v199
	s_waitcnt lgkmcnt(2)
	v_max_f32_e32 v7, v20, v20
	v_med3_f32 v9, v7, s95, v199
	s_waitcnt lgkmcnt(1)
	v_max_f32_e32 v7, v24, v24
	v_add_u32_e32 v50, 0x800, v48
	v_med3_f32 v10, v7, s95, v199
	v_mov_b32_e32 v7, v3
	ds_read2_b32 v[28:29], v50 offset0:8 offset1:24
	v_cvt_pk_fp8_f32 v7, v8, v9
	s_waitcnt lgkmcnt(1)
	v_max_f32_e32 v12, v26, v26
	ds_read2_b32 v[30:31], v50 offset0:73 offset1:89
	ds_read2_b32 v[32:33], v50 offset0:138 offset1:154
	ds_read2_b32 v[34:35], v50 offset0:203 offset1:219
	v_med3_f32 v8, v12, s95, v199
	v_cvt_pk_fp8_f32 v7, v10, v8 op_sel:[0,0,1]
	s_waitcnt lgkmcnt(3)
	v_max_f32_e32 v8, v28, v28
	v_med3_f32 v9, v8, s95, v199
	s_waitcnt lgkmcnt(2)
	v_max_f32_e32 v8, v30, v30
	v_med3_f32 v10, v8, s95, v199
	s_waitcnt lgkmcnt(1)
	v_max_f32_e32 v8, v32, v32
	v_add_u32_e32 v51, 0xc00, v48
	v_med3_f32 v12, v8, s95, v199
	v_mov_b32_e32 v8, v3
	ds_read2_b32 v[36:37], v51 offset0:12 offset1:28
	v_cvt_pk_fp8_f32 v8, v9, v10
	s_waitcnt lgkmcnt(1)
	v_max_f32_e32 v14, v34, v34
	ds_read2_b32 v[38:39], v51 offset0:77 offset1:93
	ds_read2_b32 v[40:41], v51 offset0:142 offset1:158
	ds_read2_b32 v[42:43], v51 offset0:207 offset1:223
	v_med3_f32 v9, v14, s95, v199
	v_cvt_pk_fp8_f32 v8, v12, v9 op_sel:[0,0,1]
	s_waitcnt lgkmcnt(3)
	v_max_f32_e32 v9, v36, v36
	v_med3_f32 v10, v9, s95, v199
	s_waitcnt lgkmcnt(2)
	v_max_f32_e32 v9, v38, v38
	v_med3_f32 v12, v9, s95, v199
	v_mov_b32_e32 v9, v3
	v_cvt_pk_fp8_f32 v9, v10, v12
	s_waitcnt lgkmcnt(1)
	v_max_f32_e32 v14, v40, v40
	s_waitcnt lgkmcnt(0)
	v_max_f32_e32 v12, v42, v42
	v_add_u32_e32 v22, s4, v22
	s_andn2_b32 s5, s5, 63
	v_med3_f32 v10, v14, s95, v199
	v_med3_f32 v12, v12, s95, v199
	v_ashrrev_i32_e32 v44, 4, v22
	v_or_b32_e32 v2, s5, v2
	v_cvt_pk_fp8_f32 v9, v10, v12 op_sel:[0,0,1]
	v_ashrrev_i32_e32 v45, 31, v44
	v_lshrrev_b32_e32 v2, 5, v2
	v_lshlrev_b64 v[44:45], 13, v[44:45]
	v_lshlrev_b64 v[46:47], 9, v[2:3]
	v_lshl_add_u64 v[44:45], v[4:5], 0, v[44:45]
	v_lshl_add_u64 v[44:45], v[44:45], 0, v[46:47]
	global_store_dwordx4 v[44:45], v[6:9], off
	v_max_f32_e32 v2, v11, v11
	v_med3_f32 v2, v2, s95, v199
	v_max_f32_e32 v6, v13, v13
	v_med3_f32 v7, v6, s95, v199
	v_mov_b32_e32 v6, v3
	v_cvt_pk_fp8_f32 v6, v2, v7
	v_max_f32_e32 v8, v15, v15
	v_max_f32_e32 v7, v17, v17
	v_med3_f32 v2, v8, s95, v199
	v_med3_f32 v7, v7, s95, v199
	v_cvt_pk_fp8_f32 v6, v2, v7 op_sel:[0,0,1]
	v_max_f32_e32 v2, v19, v19
	v_max_f32_e32 v7, v21, v21
	v_med3_f32 v2, v2, s95, v199
	v_med3_f32 v8, v7, s95, v199
	v_mov_b32_e32 v7, v3
	v_cvt_pk_fp8_f32 v7, v2, v8
	v_max_f32_e32 v9, v25, v25
	v_max_f32_e32 v8, v27, v27
	v_med3_f32 v2, v9, s95, v199
	v_med3_f32 v8, v8, s95, v199
	v_cvt_pk_fp8_f32 v7, v2, v8 op_sel:[0,0,1]
	v_max_f32_e32 v2, v29, v29
	v_max_f32_e32 v8, v31, v31
	v_med3_f32 v2, v2, s95, v199
	v_med3_f32 v9, v8, s95, v199
	v_mov_b32_e32 v8, v3
	v_cvt_pk_fp8_f32 v8, v2, v9
	v_max_f32_e32 v10, v33, v33
	v_max_f32_e32 v9, v35, v35
	v_med3_f32 v2, v10, s95, v199
	v_med3_f32 v9, v9, s95, v199
	v_cvt_pk_fp8_f32 v8, v2, v9 op_sel:[0,0,1]
	v_max_f32_e32 v2, v37, v37
	v_max_f32_e32 v9, v39, v39
	v_med3_f32 v2, v2, s95, v199
	v_med3_f32 v10, v9, s95, v199
	v_mov_b32_e32 v9, v3
	v_cvt_pk_fp8_f32 v9, v2, v10
	v_max_f32_e32 v11, v41, v41
	v_max_f32_e32 v10, v43, v43
	v_med3_f32 v2, v11, s95, v199
	v_med3_f32 v10, v10, s95, v199
	v_cvt_pk_fp8_f32 v9, v2, v10 op_sel:[0,0,1]
	v_add_u32_e32 v2, 16, v22
	v_ashrrev_i32_e32 v10, 4, v2
	v_ashrrev_i32_e32 v11, 31, v10
	v_lshlrev_b64 v[10:11], 13, v[10:11]
	v_lshl_add_u64 v[10:11], v[4:5], 0, v[10:11]
	v_lshl_add_u64 v[10:11], v[10:11], 0, v[46:47]
	ds_read2_b32 v[12:13], v48 offset0:32 offset1:48
	global_store_dwordx4 v[10:11], v[6:9], off
	ds_read2_b32 v[10:11], v48 offset0:97 offset1:113
	ds_read2_b32 v[14:15], v48 offset0:162 offset1:178
	ds_read2_b32 v[16:17], v48 offset0:227 offset1:243
	ds_read2_b32 v[18:19], v49 offset0:36 offset1:52
	ds_read2_b32 v[20:21], v49 offset0:101 offset1:117
	ds_read2_b32 v[24:25], v49 offset0:166 offset1:182
	ds_read2_b32 v[26:27], v49 offset0:231 offset1:247
	s_waitcnt lgkmcnt(6)
; #define GAS __attribute__((address_space(1)))
; #define LAS __attribute__((address_space(3)))
; #define LDS_WAIT() asm volatile("s_waitcnt lgkmcnt(0)" ::: "memory")
;     ...
;     const int c = lane & 3;
; #pragma unroll
;     for (int j = 0; j < 4; ++j) { const int n = (lane >> 2) + 16 * j; const LAS float* s = scr + (16 * c) * 65 + n;
;         v4u o; o.x = pg8::pk4_fp8(s[0 * 65], s[1 * 65], s[2 * 65], s[3 * 65]); o.y = pg8::pk4_fp8(s[4 * 65], s[5 * 65], s[6 * 65], s[7 * 65]);
;         o.z = pg8::pk4_fp8(s[8 * 65], s[9 * 65], s[10 * 65], s[11 * 65]); o.w = pg8::pk4_fp8(s[12 * 65], s[13 * 65], s[14 * 65], s[15 * 65]);
;         *(GAS v4u*)(WT + ((size_t)((n0 + n) >> 4) * (K >> 5) + ((k0 + 16 * c) >> 5)) * 512 + ((n0 + n) & 15) * 32 + ((16 * c) & 31)) = o; }
;     LDS_WAIT(); asm volatile("" ::: "memory");
	v_max_f32_e32 v6, v10, v10
	v_max_f32_e32 v2, v12, v12
	v_med3_f32 v7, v6, s95, v199
	s_waitcnt lgkmcnt(5)
	v_max_f32_e32 v6, v14, v14
	v_med3_f32 v2, v2, s95, v199
	v_med3_f32 v8, v6, s95, v199
	v_mov_b32_e32 v6, v3
	v_cvt_pk_fp8_f32 v6, v2, v7
	s_waitcnt lgkmcnt(4)
	v_max_f32_e32 v2, v16, v16
	v_med3_f32 v2, v2, s95, v199
	s_waitcnt lgkmcnt(2)
	v_max_f32_e32 v7, v20, v20
	v_cvt_pk_fp8_f32 v6, v8, v2 op_sel:[0,0,1]
	v_max_f32_e32 v2, v18, v18
	v_med3_f32 v8, v7, s95, v199
	s_waitcnt lgkmcnt(1)
	v_max_f32_e32 v7, v24, v24
	v_med3_f32 v2, v2, s95, v199
	v_med3_f32 v9, v7, s95, v199
	v_mov_b32_e32 v7, v3
	ds_read2_b32 v[28:29], v50 offset0:40 offset1:56
	v_cvt_pk_fp8_f32 v7, v2, v8
	ds_read2_b32 v[30:31], v50 offset0:105 offset1:121
	ds_read2_b32 v[32:33], v50 offset0:170 offset1:186
	ds_read2_b32 v[34:35], v50 offset0:235 offset1:251
	s_waitcnt lgkmcnt(4)
	v_max_f32_e32 v2, v26, v26
	v_med3_f32 v2, v2, s95, v199
	s_waitcnt lgkmcnt(2)
	v_max_f32_e32 v8, v30, v30
	v_cvt_pk_fp8_f32 v7, v9, v2 op_sel:[0,0,1]
	v_max_f32_e32 v2, v28, v28
	v_med3_f32 v9, v8, s95, v199
	s_waitcnt lgkmcnt(1)
	v_max_f32_e32 v8, v32, v32
	v_med3_f32 v2, v2, s95, v199
	v_med3_f32 v10, v8, s95, v199
	v_mov_b32_e32 v8, v3
	ds_read2_b32 v[36:37], v51 offset0:44 offset1:60
	v_cvt_pk_fp8_f32 v8, v2, v9
	ds_read2_b32 v[38:39], v51 offset0:109 offset1:125
	ds_read2_b32 v[40:41], v51 offset0:174 offset1:190
	ds_read2_b32 v[42:43], v51 offset0:239 offset1:255
	s_waitcnt lgkmcnt(4)
	v_max_f32_e32 v2, v34, v34
	v_med3_f32 v2, v2, s95, v199
	v_cvt_pk_fp8_f32 v8, v10, v2 op_sel:[0,0,1]
	s_waitcnt lgkmcnt(3)
	v_max_f32_e32 v2, v36, v36
	s_waitcnt lgkmcnt(2)
	v_max_f32_e32 v9, v38, v38
	v_med3_f32 v2, v2, s95, v199
	v_med3_f32 v10, v9, s95, v199
	v_mov_b32_e32 v9, v3
	v_cvt_pk_fp8_f32 v9, v2, v10
	s_waitcnt lgkmcnt(1)
	v_max_f32_e32 v12, v40, v40
	s_waitcnt lgkmcnt(0)
	v_max_f32_e32 v10, v42, v42
	v_med3_f32 v2, v12, s95, v199
	v_med3_f32 v10, v10, s95, v199
	v_cvt_pk_fp8_f32 v9, v2, v10 op_sel:[0,0,1]
	v_add_u32_e32 v2, 32, v22
	v_ashrrev_i32_e32 v44, 4, v2
	v_ashrrev_i32_e32 v45, 31, v44
	v_lshlrev_b64 v[44:45], 13, v[44:45]
	v_lshl_add_u64 v[44:45], v[4:5], 0, v[44:45]
	v_lshl_add_u64 v[44:45], v[44:45], 0, v[46:47]
	global_store_dwordx4 v[44:45], v[6:9], off
	v_max_f32_e32 v2, v13, v13
	v_med3_f32 v2, v2, s95, v199
	v_max_f32_e32 v6, v11, v11
	v_med3_f32 v7, v6, s95, v199
	v_mov_b32_e32 v6, v3
	v_cvt_pk_fp8_f32 v6, v2, v7
	v_max_f32_e32 v8, v15, v15
	v_max_f32_e32 v7, v17, v17
	v_med3_f32 v2, v8, s95, v199
	v_med3_f32 v7, v7, s95, v199
	v_cvt_pk_fp8_f32 v6, v2, v7 op_sel:[0,0,1]
	v_max_f32_e32 v2, v19, v19
	v_max_f32_e32 v7, v21, v21
	v_med3_f32 v2, v2, s95, v199
	v_med3_f32 v8, v7, s95, v199
	v_mov_b32_e32 v7, v3
	v_cvt_pk_fp8_f32 v7, v2, v8
	v_max_f32_e32 v9, v25, v25
	v_max_f32_e32 v8, v27, v27
	v_med3_f32 v2, v9, s95, v199
	v_med3_f32 v8, v8, s95, v199
	v_cvt_pk_fp8_f32 v7, v2, v8 op_sel:[0,0,1]
	v_max_f32_e32 v2, v29, v29
	v_max_f32_e32 v8, v31, v31
	v_med3_f32 v2, v2, s95, v199
	v_med3_f32 v9, v8, s95, v199
	v_mov_b32_e32 v8, v3
	v_cvt_pk_fp8_f32 v8, v2, v9
	v_max_f32_e32 v10, v33, v33
	v_max_f32_e32 v9, v35, v35
	v_med3_f32 v2, v10, s95, v199
	v_med3_f32 v9, v9, s95, v199
	v_cvt_pk_fp8_f32 v8, v2, v9 op_sel:[0,0,1]
	v_max_f32_e32 v2, v37, v37
	v_max_f32_e32 v9, v39, v39
	v_med3_f32 v2, v2, s95, v199
	v_med3_f32 v10, v9, s95, v199
	v_mov_b32_e32 v9, v3
	v_cvt_pk_fp8_f32 v9, v2, v10
	v_max_f32_e32 v11, v41, v41
	v_max_f32_e32 v10, v43, v43
	v_med3_f32 v2, v11, s95, v199
	v_med3_f32 v10, v10, s95, v199
	v_cvt_pk_fp8_f32 v9, v2, v10 op_sel:[0,0,1]
	v_add_u32_e32 v2, 48, v22
	v_ashrrev_i32_e32 v10, 4, v2
	v_ashrrev_i32_e32 v11, 31, v10
	v_lshlrev_b64 v[10:11], 13, v[10:11]
	v_lshl_add_u64 v[4:5], v[4:5], 0, v[10:11]
	v_lshl_add_u64 v[4:5], v[4:5], 0, v[46:47]
	global_store_dwordx4 v[4:5], v[6:9], off
	s_waitcnt lgkmcnt(0)

; #define GAS __attribute__((address_space(1)))
; #define LAS __attribute__((address_space(3)))
; #define LDS_WAIT() asm volatile("s_waitcnt lgkmcnt(0)" ::: "memory")
;     ...
;     for (int i = 0; i < 16; ++i) { const int kk = 4 * i + kq;
;         f32x4 v = __builtin_nontemporal_load((const GAS f32x4*)(W + (size_t)(k0 + kk) * ldw + n0 + 4 * c4));
;         v = v * (gk ? gk[k0 + kk] * scale : scale);
;         LAS float* d = scr + kk * 65 + 4 * c4; d[0] = v[0]; d[1] = v[1]; d[2] = v[2]; d[3] = v[3]; }
;     LDS_WAIT(); asm volatile("" ::: "memory");
.LBB0_1008:
	s_mov_b32 s100, 0x4000
	s_mov_b32 s101, 0
	global_load_dwordx4 v[64:67], v[8:9], off nt
	v_lshl_add_u64 v[8:9], v[8:9], 0, s[100:101]
	global_load_dwordx4 v[68:71], v[8:9], off nt
	v_lshl_add_u64 v[8:9], v[8:9], 0, s[100:101]
	global_load_dwordx4 v[72:75], v[8:9], off nt
	v_lshl_add_u64 v[8:9], v[8:9], 0, s[100:101]
	global_load_dwordx4 v[76:79], v[8:9], off nt
	v_lshl_add_u64 v[8:9], v[8:9], 0, s[100:101]
	global_load_dwordx4 v[80:83], v[8:9], off nt
	v_lshl_add_u64 v[8:9], v[8:9], 0, s[100:101]
	global_load_dwordx4 v[84:87], v[8:9], off nt
	v_lshl_add_u64 v[8:9], v[8:9], 0, s[100:101]
	global_load_dwordx4 v[88:91], v[8:9], off nt
	v_lshl_add_u64 v[8:9], v[8:9], 0, s[100:101]
	global_load_dwordx4 v[92:95], v[8:9], off nt
	v_lshl_add_u64 v[8:9], v[8:9], 0, s[100:101]
	global_load_dwordx4 v[96:99], v[8:9], off nt
	v_lshl_add_u64 v[8:9], v[8:9], 0, s[100:101]
	global_load_dwordx4 v[100:103], v[8:9], off nt
	v_lshl_add_u64 v[8:9], v[8:9], 0, s[100:101]
	global_load_dwordx4 v[104:107], v[8:9], off nt
	v_lshl_add_u64 v[8:9], v[8:9], 0, s[100:101]
	global_load_dwordx4 v[108:111], v[8:9], off nt
	v_lshl_add_u64 v[8:9], v[8:9], 0, s[100:101]
	global_load_dwordx4 v[112:115], v[8:9], off nt
	v_lshl_add_u64 v[8:9], v[8:9], 0, s[100:101]
	global_load_dwordx4 v[116:119], v[8:9], off nt
	v_lshl_add_u64 v[8:9], v[8:9], 0, s[100:101]
	global_load_dwordx4 v[120:123], v[8:9], off nt
	v_lshl_add_u64 v[8:9], v[8:9], 0, s[100:101]
	global_load_dwordx4 v[124:127], v[8:9], off nt
	s_waitcnt vmcnt(15)
	v_pk_mul_f32 v[64:65], v[64:65], s[92:93] op_sel_hi:[1,0]
	v_pk_mul_f32 v[66:67], v[66:67], s[92:93] op_sel_hi:[1,0]
	ds_write2_b32 v11, v64, v65 offset1:1
	ds_write2_b32 v11, v66, v67 offset0:2 offset1:3
	s_waitcnt vmcnt(14)
	v_pk_mul_f32 v[68:69], v[68:69], s[92:93] op_sel_hi:[1,0]
	v_pk_mul_f32 v[70:71], v[70:71], s[92:93] op_sel_hi:[1,0]
	v_add_u32_e32 v2, 0x410, v11
	ds_write2_b32 v2, v68, v69 offset1:1
	ds_write2_b32 v2, v70, v71 offset0:2 offset1:3
	s_waitcnt vmcnt(13)
	v_pk_mul_f32 v[72:73], v[72:73], s[92:93] op_sel_hi:[1,0]
	v_pk_mul_f32 v[74:75], v[74:75], s[92:93] op_sel_hi:[1,0]
	v_add_u32_e32 v2, 0x820, v11
	ds_write2_b32 v2, v72, v73 offset1:1
	ds_write2_b32 v2, v74, v75 offset0:2 offset1:3
	s_waitcnt vmcnt(12)
	v_pk_mul_f32 v[76:77], v[76:77], s[92:93] op_sel_hi:[1,0]
	v_pk_mul_f32 v[78:79], v[78:79], s[92:93] op_sel_hi:[1,0]
	v_add_u32_e32 v2, 0xc30, v11
	ds_write2_b32 v2, v76, v77 offset1:1
	ds_write2_b32 v2, v78, v79 offset0:2 offset1:3
	s_waitcnt vmcnt(11)
	v_pk_mul_f32 v[80:81], v[80:81], s[92:93] op_sel_hi:[1,0]
	v_pk_mul_f32 v[82:83], v[82:83], s[92:93] op_sel_hi:[1,0]
	v_add_u32_e32 v2, 0x1040, v11
	ds_write2_b32 v2, v80, v81 offset1:1
	ds_write2_b32 v2, v82, v83 offset0:2 offset1:3
	s_waitcnt vmcnt(10)
	v_pk_mul_f32 v[84:85], v[84:85], s[92:93] op_sel_hi:[1,0]
	v_pk_mul_f32 v[86:87], v[86:87], s[92:93] op_sel_hi:[1,0]
	v_add_u32_e32 v2, 0x1450, v11
	ds_write2_b32 v2, v84, v85 offset1:1
	ds_write2_b32 v2, v86, v87 offset0:2 offset1:3
	s_waitcnt vmcnt(9)
	v_pk_mul_f32 v[88:89], v[88:89], s[92:93] op_sel_hi:[1,0]
	v_pk_mul_f32 v[90:91], v[90:91], s[92:93] op_sel_hi:[1,0]
	v_add_u32_e32 v2, 0x1860, v11
	ds_write2_b32 v2, v88, v89 offset1:1
	ds_write2_b32 v2, v90, v91 offset0:2 offset1:3
	s_waitcnt vmcnt(8)
	v_pk_mul_f32 v[92:93], v[92:93], s[92:93] op_sel_hi:[1,0]
	v_pk_mul_f32 v[94:95], v[94:95], s[92:93] op_sel_hi:[1,0]
	v_add_u32_e32 v2, 0x1c70, v11
	ds_write2_b32 v2, v92, v93 offset1:1
	ds_write2_b32 v2, v94, v95 offset0:2 offset1:3
	s_waitcnt vmcnt(7)
	v_pk_mul_f32 v[96:97], v[96:97], s[92:93] op_sel_hi:[1,0]
	v_pk_mul_f32 v[98:99], v[98:99], s[92:93] op_sel_hi:[1,0]
	v_add_u32_e32 v2, 0x2080, v11
	ds_write2_b32 v2, v96, v97 offset1:1
	ds_write2_b32 v2, v98, v99 offset0:2 offset1:3
	s_waitcnt vmcnt(6)
	v_pk_mul_f32 v[100:101], v[100:101], s[92:93] op_sel_hi:[1,0]
	v_pk_mul_f32 v[102:103], v[102:103], s[92:93] op_sel_hi:[1,0]
	v_add_u32_e32 v2, 0x2490, v11
	ds_write2_b32 v2, v100, v101 offset1:1
	ds_write2_b32 v2, v102, v103 offset0:2 offset1:3
	s_waitcnt vmcnt(5)
	v_pk_mul_f32 v[104:105], v[104:105], s[92:93] op_sel_hi:[1,0]
	v_pk_mul_f32 v[106:107], v[106:107], s[92:93] op_sel_hi:[1,0]
	v_add_u32_e32 v2, 0x28a0, v11
	ds_write2_b32 v2, v104, v105 offset1:1
	ds_write2_b32 v2, v106, v107 offset0:2 offset1:3
	s_waitcnt vmcnt(4)
	v_pk_mul_f32 v[108:109], v[108:109], s[92:93] op_sel_hi:[1,0]
	v_pk_mul_f32 v[110:111], v[110:111], s[92:93] op_sel_hi:[1,0]
	v_add_u32_e32 v2, 0x2cb0, v11
	ds_write2_b32 v2, v108, v109 offset1:1
	ds_write2_b32 v2, v110, v111 offset0:2 offset1:3
	s_waitcnt vmcnt(3)
	v_pk_mul_f32 v[112:113], v[112:113], s[92:93] op_sel_hi:[1,0]
	v_pk_mul_f32 v[114:115], v[114:115], s[92:93] op_sel_hi:[1,0]
	v_add_u32_e32 v2, 0x30c0, v11
	ds_write2_b32 v2, v112, v113 offset1:1
	ds_write2_b32 v2, v114, v115 offset0:2 offset1:3
	s_waitcnt vmcnt(2)
	v_pk_mul_f32 v[116:117], v[116:117], s[92:93] op_sel_hi:[1,0]
	v_pk_mul_f32 v[118:119], v[118:119], s[92:93] op_sel_hi:[1,0]
	v_add_u32_e32 v2, 0x34d0, v11
	ds_write2_b32 v2, v116, v117 offset1:1
	ds_write2_b32 v2, v118, v119 offset0:2 offset1:3
	s_waitcnt vmcnt(1)
	v_pk_mul_f32 v[120:121], v[120:121], s[92:93] op_sel_hi:[1,0]
	v_pk_mul_f32 v[122:123], v[122:123], s[92:93] op_sel_hi:[1,0]
	v_add_u32_e32 v2, 0x38e0, v11
	ds_write2_b32 v2, v120, v121 offset1:1
	ds_write2_b32 v2, v122, v123 offset0:2 offset1:3
	s_waitcnt vmcnt(0)
	v_pk_mul_f32 v[124:125], v[124:125], s[92:93] op_sel_hi:[1,0]
	v_pk_mul_f32 v[126:127], v[126:127], s[92:93] op_sel_hi:[1,0]
	v_add_u32_e32 v2, 0x3cf0, v11
	ds_write2_b32 v2, v124, v125 offset1:1
	ds_write2_b32 v2, v126, v127 offset0:2 offset1:3
	v_and_b32_e32 v2, 48, v10
	s_waitcnt lgkmcnt(0)
; #define GAS __attribute__((address_space(1)))
; #define LAS __attribute__((address_space(3)))
; #define LDS_WAIT() asm volatile("s_waitcnt lgkmcnt(0)" ::: "memory")
;     ...
;     LDS_WAIT(); asm volatile("" ::: "memory");
;     const int c = lane & 3;
; #pragma unroll
;     for (int j = 0; j < 4; ++j) { const int n = (lane >> 2) + 16 * j; const LAS float* s = scr + (16 * c) * 65 + n;
;         v4u o; o.x = pg8::pk4_fp8(s[0 * 65], s[1 * 65], s[2 * 65], s[3 * 65]); o.y = pg8::pk4_fp8(s[4 * 65], s[5 * 65], s[6 * 65], s[7 * 65]);
;         o.z = pg8::pk4_fp8(s[8 * 65], s[9 * 65], s[10 * 65], s[11 * 65]); o.w = pg8::pk4_fp8(s[12 * 65], s[13 * 65], s[14 * 65], s[15 * 65]);
;         *(GAS v4u*)(WT + ((size_t)((n0 + n) >> 4) * (K >> 5) + ((k0 + 16 * c) >> 5)) * 512 + ((n0 + n) & 15) * 32 + ((16 * c) & 31)) = o; }
;     LDS_WAIT(); asm volatile("" ::: "memory");
	v_mul_u32_u24_e32 v8, 0x104, v2
	v_and_b32_e32 v9, -4, v23
	v_add3_u32 v48, s82, v8, v9
	v_and_b32_e32 v6, 16, v10
	ds_read2_b32 v[10:11], v48 offset1:16
	v_ashrrev_i32_e32 v22, 2, v23
	v_lshlrev_b32_e32 v4, 5, v22
	v_readlane_b32 s18, v252, 6
	v_and_b32_e32 v4, 0x1e0, v4
	v_mov_b32_e32 v5, v3
	v_readlane_b32 s19, v252, 7
	ds_read2_b32 v[12:13], v48 offset0:65 offset1:81
	ds_read2_b32 v[14:15], v48 offset0:130 offset1:146
	ds_read2_b32 v[16:17], v48 offset0:195 offset1:211
	v_lshl_add_u64 v[4:5], s[18:19], 0, v[4:5]
	v_mov_b32_e32 v7, v3
	v_lshl_add_u64 v[4:5], v[4:5], 0, v[6:7]
	s_waitcnt lgkmcnt(3)
	v_max_f32_e32 v6, v10, v10
	v_med3_f32 v7, v6, s95, v199
	s_waitcnt lgkmcnt(2)
	v_max_f32_e32 v6, v12, v12
	v_med3_f32 v8, v6, s95, v199
	s_waitcnt lgkmcnt(1)
	v_max_f32_e32 v6, v14, v14
	v_add_u32_e32 v49, 0x400, v48
	v_med3_f32 v9, v6, s95, v199
	v_mov_b32_e32 v6, v3
	ds_read2_b32 v[18:19], v49 offset0:4 offset1:20
	v_cvt_pk_fp8_f32 v6, v7, v8
	s_waitcnt lgkmcnt(1)
	v_max_f32_e32 v10, v16, v16
	ds_read2_b32 v[20:21], v49 offset0:69 offset1:85
	ds_read2_b32 v[24:25], v49 offset0:134 offset1:150
	ds_read2_b32 v[26:27], v49 offset0:199 offset1:215
	v_med3_f32 v7, v10, s95, v199
	v_cvt_pk_fp8_f32 v6, v9, v7 op_sel:[0,0,1]
	s_waitcnt lgkmcnt(3)
	v_max_f32_e32 v7, v18, v18
	v_med3_f32 v8, v7, s95, v199
	s_waitcnt lgkmcnt(2)
	v_max_f32_e32 v7, v20, v20
	v_med3_f32 v9, v7, s95, v199
	s_waitcnt lgkmcnt(1)
	v_max_f32_e32 v7, v24, v24
	v_add_u32_e32 v50, 0x800, v48
	v_med3_f32 v10, v7, s95, v199
	v_mov_b32_e32 v7, v3
	ds_read2_b32 v[28:29], v50 offset0:8 offset1:24
	v_cvt_pk_fp8_f32 v7, v8, v9
	s_waitcnt lgkmcnt(1)
	v_max_f32_e32 v12, v26, v26
	ds_read2_b32 v[30:31], v50 offset0:73 offset1:89
	ds_read2_b32 v[32:33], v50 offset0:138 offset1:154
	ds_read2_b32 v[34:35], v50 offset0:203 offset1:219
	v_med3_f32 v8, v12, s95, v199
	v_cvt_pk_fp8_f32 v7, v10, v8 op_sel:[0,0,1]
	s_waitcnt lgkmcnt(3)
	v_max_f32_e32 v8, v28, v28
	v_med3_f32 v9, v8, s95, v199
	s_waitcnt lgkmcnt(2)
	v_max_f32_e32 v8, v30, v30
	v_med3_f32 v10, v8, s95, v199
	s_waitcnt lgkmcnt(1)
	v_max_f32_e32 v8, v32, v32
	v_add_u32_e32 v51, 0xc00, v48
	v_med3_f32 v12, v8, s95, v199
	v_mov_b32_e32 v8, v3
	ds_read2_b32 v[36:37], v51 offset0:12 offset1:28
	v_cvt_pk_fp8_f32 v8, v9, v10
	s_waitcnt lgkmcnt(1)
	v_max_f32_e32 v14, v34, v34
	ds_read2_b32 v[38:39], v51 offset0:77 offset1:93
	ds_read2_b32 v[40:41], v51 offset0:142 offset1:158
	ds_read2_b32 v[42:43], v51 offset0:207 offset1:223
	v_med3_f32 v9, v14, s95, v199
	v_cvt_pk_fp8_f32 v8, v12, v9 op_sel:[0,0,1]
	s_waitcnt lgkmcnt(3)
	v_max_f32_e32 v9, v36, v36
	v_med3_f32 v10, v9, s95, v199
	s_waitcnt lgkmcnt(2)
	v_max_f32_e32 v9, v38, v38
	v_med3_f32 v12, v9, s95, v199
	v_mov_b32_e32 v9, v3
	v_cvt_pk_fp8_f32 v9, v10, v12
	s_waitcnt lgkmcnt(1)
	v_max_f32_e32 v14, v40, v40
	s_waitcnt lgkmcnt(0)
	v_max_f32_e32 v12, v42, v42
	v_add_u32_e32 v22, s4, v22
	v_med3_f32 v10, v14, s95, v199
	v_med3_f32 v12, v12, s95, v199
	v_ashrrev_i32_e32 v44, 4, v22
	v_lshl_or_b32 v2, s9, 6, v2
	v_cvt_pk_fp8_f32 v9, v10, v12 op_sel:[0,0,1]
	v_ashrrev_i32_e32 v45, 31, v44
	v_lshrrev_b32_e32 v2, 5, v2
	v_lshlrev_b64 v[44:45], 16, v[44:45]
	v_lshlrev_b64 v[46:47], 9, v[2:3]
	v_lshl_add_u64 v[44:45], v[4:5], 0, v[44:45]
	v_lshl_add_u64 v[44:45], v[44:45], 0, v[46:47]
	global_store_dwordx4 v[44:45], v[6:9], off
	v_max_f32_e32 v2, v11, v11
	v_med3_f32 v2, v2, s95, v199
	v_max_f32_e32 v6, v13, v13
	v_med3_f32 v7, v6, s95, v199
	v_mov_b32_e32 v6, v3
	v_cvt_pk_fp8_f32 v6, v2, v7
	v_max_f32_e32 v8, v15, v15
	v_max_f32_e32 v7, v17, v17
	v_med3_f32 v2, v8, s95, v199
	v_med3_f32 v7, v7, s95, v199
	v_cvt_pk_fp8_f32 v6, v2, v7 op_sel:[0,0,1]
	v_max_f32_e32 v2, v19, v19
	v_max_f32_e32 v7, v21, v21
	v_med3_f32 v2, v2, s95, v199
	v_med3_f32 v8, v7, s95, v199
	v_mov_b32_e32 v7, v3
	v_cvt_pk_fp8_f32 v7, v2, v8
	v_max_f32_e32 v9, v25, v25
	v_max_f32_e32 v8, v27, v27
	v_med3_f32 v2, v9, s95, v199
	v_med3_f32 v8, v8, s95, v199
	v_cvt_pk_fp8_f32 v7, v2, v8 op_sel:[0,0,1]
	v_max_f32_e32 v2, v29, v29
	v_max_f32_e32 v8, v31, v31
	v_med3_f32 v2, v2, s95, v199
	v_med3_f32 v9, v8, s95, v199
	v_mov_b32_e32 v8, v3
	v_cvt_pk_fp8_f32 v8, v2, v9
	v_max_f32_e32 v10, v33, v33
	v_max_f32_e32 v9, v35, v35
	v_med3_f32 v2, v10, s95, v199
	v_med3_f32 v9, v9, s95, v199
	v_cvt_pk_fp8_f32 v8, v2, v9 op_sel:[0,0,1]
	v_max_f32_e32 v2, v37, v37
	v_max_f32_e32 v9, v39, v39
	v_med3_f32 v2, v2, s95, v199
	v_med3_f32 v10, v9, s95, v199
	v_mov_b32_e32 v9, v3
	v_cvt_pk_fp8_f32 v9, v2, v10
	v_max_f32_e32 v11, v41, v41
	v_max_f32_e32 v10, v43, v43
	v_med3_f32 v2, v11, s95, v199
	v_med3_f32 v10, v10, s95, v199
	v_cvt_pk_fp8_f32 v9, v2, v10 op_sel:[0,0,1]
	v_add_u32_e32 v2, 16, v22
	v_ashrrev_i32_e32 v10, 4, v2
	v_ashrrev_i32_e32 v11, 31, v10
	v_lshlrev_b64 v[10:11], 16, v[10:11]
	v_lshl_add_u64 v[10:11], v[4:5], 0, v[10:11]
	v_lshl_add_u64 v[10:11], v[10:11], 0, v[46:47]
	ds_read2_b32 v[12:13], v48 offset0:32 offset1:48
	global_store_dwordx4 v[10:11], v[6:9], off
	ds_read2_b32 v[10:11], v48 offset0:97 offset1:113
	ds_read2_b32 v[14:15], v48 offset0:162 offset1:178
	ds_read2_b32 v[16:17], v48 offset0:227 offset1:243
	ds_read2_b32 v[18:19], v49 offset0:36 offset1:52
	ds_read2_b32 v[20:21], v49 offset0:101 offset1:117
	ds_read2_b32 v[24:25], v49 offset0:166 offset1:182
	ds_read2_b32 v[26:27], v49 offset0:231 offset1:247
	s_waitcnt lgkmcnt(6)
; #define GAS __attribute__((address_space(1)))
; #define LAS __attribute__((address_space(3)))
; #define LDS_WAIT() asm volatile("s_waitcnt lgkmcnt(0)" ::: "memory")
;     ...
;     const int c = lane & 3;
; #pragma unroll
;     for (int j = 0; j < 4; ++j) { const int n = (lane >> 2) + 16 * j; const LAS float* s = scr + (16 * c) * 65 + n;
;         v4u o; o.x = pg8::pk4_fp8(s[0 * 65], s[1 * 65], s[2 * 65], s[3 * 65]); o.y = pg8::pk4_fp8(s[4 * 65], s[5 * 65], s[6 * 65], s[7 * 65]);
;         o.z = pg8::pk4_fp8(s[8 * 65], s[9 * 65], s[10 * 65], s[11 * 65]); o.w = pg8::pk4_fp8(s[12 * 65], s[13 * 65], s[14 * 65], s[15 * 65]);
;         *(GAS v4u*)(WT + ((size_t)((n0 + n) >> 4) * (K >> 5) + ((k0 + 16 * c) >> 5)) * 512 + ((n0 + n) & 15) * 32 + ((16 * c) & 31)) = o; }
;     LDS_WAIT(); asm volatile("" ::: "memory");
	v_max_f32_e32 v6, v10, v10
	v_max_f32_e32 v2, v12, v12
	v_med3_f32 v7, v6, s95, v199
	s_waitcnt lgkmcnt(5)
	v_max_f32_e32 v6, v14, v14
	v_med3_f32 v2, v2, s95, v199
	v_med3_f32 v8, v6, s95, v199
	v_mov_b32_e32 v6, v3
	v_cvt_pk_fp8_f32 v6, v2, v7
	s_waitcnt lgkmcnt(4)
	v_max_f32_e32 v2, v16, v16
	v_med3_f32 v2, v2, s95, v199
	s_waitcnt lgkmcnt(2)
	v_max_f32_e32 v7, v20, v20
	v_cvt_pk_fp8_f32 v6, v8, v2 op_sel:[0,0,1]
	v_max_f32_e32 v2, v18, v18
	v_med3_f32 v8, v7, s95, v199
	s_waitcnt lgkmcnt(1)
	v_max_f32_e32 v7, v24, v24
	v_med3_f32 v2, v2, s95, v199
	v_med3_f32 v9, v7, s95, v199
	v_mov_b32_e32 v7, v3
	ds_read2_b32 v[28:29], v50 offset0:40 offset1:56
	v_cvt_pk_fp8_f32 v7, v2, v8
	ds_read2_b32 v[30:31], v50 offset0:105 offset1:121
	ds_read2_b32 v[32:33], v50 offset0:170 offset1:186
	ds_read2_b32 v[34:35], v50 offset0:235 offset1:251
	s_waitcnt lgkmcnt(4)
	v_max_f32_e32 v2, v26, v26
	v_med3_f32 v2, v2, s95, v199
	s_waitcnt lgkmcnt(2)
	v_max_f32_e32 v8, v30, v30
	v_cvt_pk_fp8_f32 v7, v9, v2 op_sel:[0,0,1]
	v_max_f32_e32 v2, v28, v28
	v_med3_f32 v9, v8, s95, v199
	s_waitcnt lgkmcnt(1)
	v_max_f32_e32 v8, v32, v32
	v_med3_f32 v2, v2, s95, v199
	v_med3_f32 v10, v8, s95, v199
	v_mov_b32_e32 v8, v3
	ds_read2_b32 v[36:37], v51 offset0:44 offset1:60
	v_cvt_pk_fp8_f32 v8, v2, v9
	ds_read2_b32 v[38:39], v51 offset0:109 offset1:125
	ds_read2_b32 v[40:41], v51 offset0:174 offset1:190
	ds_read2_b32 v[42:43], v51 offset0:239 offset1:255
	s_waitcnt lgkmcnt(4)
	v_max_f32_e32 v2, v34, v34
	v_med3_f32 v2, v2, s95, v199
	v_cvt_pk_fp8_f32 v8, v10, v2 op_sel:[0,0,1]
	s_waitcnt lgkmcnt(3)
	v_max_f32_e32 v2, v36, v36
	s_waitcnt lgkmcnt(2)
	v_max_f32_e32 v9, v38, v38
	v_med3_f32 v2, v2, s95, v199
	v_med3_f32 v10, v9, s95, v199
	v_mov_b32_e32 v9, v3
	v_cvt_pk_fp8_f32 v9, v2, v10
	s_waitcnt lgkmcnt(1)
	v_max_f32_e32 v12, v40, v40
	s_waitcnt lgkmcnt(0)
	v_max_f32_e32 v10, v42, v42
	v_med3_f32 v2, v12, s95, v199
	v_med3_f32 v10, v10, s95, v199
	v_cvt_pk_fp8_f32 v9, v2, v10 op_sel:[0,0,1]
	v_add_u32_e32 v2, 32, v22
	v_ashrrev_i32_e32 v44, 4, v2
	v_ashrrev_i32_e32 v45, 31, v44
	v_lshlrev_b64 v[44:45], 16, v[44:45]
	v_lshl_add_u64 v[44:45], v[4:5], 0, v[44:45]
	v_lshl_add_u64 v[44:45], v[44:45], 0, v[46:47]
	global_store_dwordx4 v[44:45], v[6:9], off
	v_max_f32_e32 v2, v13, v13
	v_med3_f32 v2, v2, s95, v199
	v_max_f32_e32 v6, v11, v11
	v_med3_f32 v7, v6, s95, v199
	v_mov_b32_e32 v6, v3
	v_cvt_pk_fp8_f32 v6, v2, v7
	v_max_f32_e32 v8, v15, v15
	v_max_f32_e32 v7, v17, v17
	v_med3_f32 v2, v8, s95, v199
	v_med3_f32 v7, v7, s95, v199
	v_cvt_pk_fp8_f32 v6, v2, v7 op_sel:[0,0,1]
	v_max_f32_e32 v2, v19, v19
	v_max_f32_e32 v7, v21, v21
	v_med3_f32 v2, v2, s95, v199
	v_med3_f32 v8, v7, s95, v199
	v_mov_b32_e32 v7, v3
	v_cvt_pk_fp8_f32 v7, v2, v8
	v_max_f32_e32 v9, v25, v25
	v_max_f32_e32 v8, v27, v27
	v_med3_f32 v2, v9, s95, v199
	v_med3_f32 v8, v8, s95, v199
	v_cvt_pk_fp8_f32 v7, v2, v8 op_sel:[0,0,1]
	v_max_f32_e32 v2, v29, v29
	v_max_f32_e32 v8, v31, v31
	v_med3_f32 v2, v2, s95, v199
	v_med3_f32 v9, v8, s95, v199
	v_mov_b32_e32 v8, v3
	v_cvt_pk_fp8_f32 v8, v2, v9
	v_max_f32_e32 v10, v33, v33
	v_max_f32_e32 v9, v35, v35
	v_med3_f32 v2, v10, s95, v199
	v_med3_f32 v9, v9, s95, v199
	v_cvt_pk_fp8_f32 v8, v2, v9 op_sel:[0,0,1]
	v_max_f32_e32 v2, v37, v37
	v_max_f32_e32 v9, v39, v39
	v_med3_f32 v2, v2, s95, v199
	v_med3_f32 v10, v9, s95, v199
	v_mov_b32_e32 v9, v3
	v_cvt_pk_fp8_f32 v9, v2, v10
	v_max_f32_e32 v11, v41, v41
	v_max_f32_e32 v10, v43, v43
	v_med3_f32 v2, v11, s95, v199
	v_med3_f32 v10, v10, s95, v199
	v_cvt_pk_fp8_f32 v9, v2, v10 op_sel:[0,0,1]
	v_add_u32_e32 v2, 48, v22
	v_ashrrev_i32_e32 v10, 4, v2
	v_ashrrev_i32_e32 v11, 31, v10
	v_lshlrev_b64 v[10:11], 16, v[10:11]
	v_lshl_add_u64 v[4:5], v[4:5], 0, v[10:11]
	v_lshl_add_u64 v[4:5], v[4:5], 0, v[46:47]
	global_store_dwordx4 v[4:5], v[6:9], off
	s_waitcnt lgkmcnt(0)

; #define GAS __attribute__((address_space(1)))
;     ...
;     for (int i = 0; i < 16; ++i) { const int kk = 4 * i + kq;
;         f32x4 v = __builtin_nontemporal_load((const GAS f32x4*)(W + (size_t)(k0 + kk) * ldw + n0 + 4 * c4));
;         v = v * (gk ? gk[k0 + kk] * scale : scale);
.LBB0_1014:
	s_mov_b32 s100, 0x2000
	s_mov_b32 s101, 0
	s_andn2_b64 vcc, exec, s[0:1]
	s_cbranch_vccnz .Lconv_nogain_cq
	global_load_dword v164, v[10:11], off offset:-32
	global_load_dword v166, v[10:11], off offset:-16
	global_load_dword v168, v[10:11], off
	global_load_dword v170, v[10:11], off offset:16
	global_load_dword v172, v[10:11], off offset:32
	global_load_dword v174, v[10:11], off offset:48
	global_load_dword v176, v[10:11], off offset:64
	global_load_dword v178, v[10:11], off offset:80
	global_load_dword v180, v[10:11], off offset:96
	global_load_dword v182, v[10:11], off offset:112
	global_load_dword v184, v[10:11], off offset:128
	global_load_dword v186, v[10:11], off offset:144
	global_load_dword v188, v[10:11], off offset:160
	global_load_dword v190, v[10:11], off offset:176
	global_load_dword v192, v[10:11], off offset:192
	global_load_dword v194, v[10:11], off offset:208
	s_branch .Lconv_gdone_cq

; #define GAS __attribute__((address_space(1)))
; #define LAS __attribute__((address_space(3)))
; #define LDS_WAIT() asm volatile("s_waitcnt lgkmcnt(0)" ::: "memory")
;     ...
;     for (int i = 0; i < 16; ++i) { const int kk = 4 * i + kq;
;         f32x4 v = __builtin_nontemporal_load((const GAS f32x4*)(W + (size_t)(k0 + kk) * ldw + n0 + 4 * c4));
;         v = v * (gk ? gk[k0 + kk] * scale : scale);
;         LAS float* d = scr + kk * 65 + 4 * c4; d[0] = v[0]; d[1] = v[1]; d[2] = v[2]; d[3] = v[3]; }
;     LDS_WAIT(); asm volatile("" ::: "memory");
.Lconv_gdone_cq:
	global_load_dwordx4 v[64:67], v[12:13], off nt
	v_lshl_add_u64 v[12:13], v[12:13], 0, s[100:101]
	global_load_dwordx4 v[68:71], v[12:13], off nt
	v_lshl_add_u64 v[12:13], v[12:13], 0, s[100:101]
	global_load_dwordx4 v[72:75], v[12:13], off nt
	v_lshl_add_u64 v[12:13], v[12:13], 0, s[100:101]
	global_load_dwordx4 v[76:79], v[12:13], off nt
	v_lshl_add_u64 v[12:13], v[12:13], 0, s[100:101]
	global_load_dwordx4 v[80:83], v[12:13], off nt
	v_lshl_add_u64 v[12:13], v[12:13], 0, s[100:101]
	global_load_dwordx4 v[84:87], v[12:13], off nt
	v_lshl_add_u64 v[12:13], v[12:13], 0, s[100:101]
	global_load_dwordx4 v[88:91], v[12:13], off nt
	v_lshl_add_u64 v[12:13], v[12:13], 0, s[100:101]
	global_load_dwordx4 v[92:95], v[12:13], off nt
	v_lshl_add_u64 v[12:13], v[12:13], 0, s[100:101]
	global_load_dwordx4 v[96:99], v[12:13], off nt
	v_lshl_add_u64 v[12:13], v[12:13], 0, s[100:101]
	global_load_dwordx4 v[100:103], v[12:13], off nt
	v_lshl_add_u64 v[12:13], v[12:13], 0, s[100:101]
	global_load_dwordx4 v[104:107], v[12:13], off nt
	v_lshl_add_u64 v[12:13], v[12:13], 0, s[100:101]
	global_load_dwordx4 v[108:111], v[12:13], off nt
	v_lshl_add_u64 v[12:13], v[12:13], 0, s[100:101]
	global_load_dwordx4 v[112:115], v[12:13], off nt
	v_lshl_add_u64 v[12:13], v[12:13], 0, s[100:101]
	global_load_dwordx4 v[116:119], v[12:13], off nt
	v_lshl_add_u64 v[12:13], v[12:13], 0, s[100:101]
	global_load_dwordx4 v[120:123], v[12:13], off nt
	v_lshl_add_u64 v[12:13], v[12:13], 0, s[100:101]
	global_load_dwordx4 v[124:127], v[12:13], off nt
	s_waitcnt vmcnt(15)
	v_mul_f32_e32 v164, 0x42800000, v164
	v_pk_mul_f32 v[64:65], v[64:65], v[164:165] op_sel_hi:[1,0]
	v_pk_mul_f32 v[66:67], v[66:67], v[164:165] op_sel_hi:[1,0]
	ds_write2_b32 v16, v64, v65 offset1:1
	ds_write2_b32 v16, v66, v67 offset0:2 offset1:3
	s_waitcnt vmcnt(14)
	v_mul_f32_e32 v166, 0x42800000, v166
	v_pk_mul_f32 v[68:69], v[68:69], v[166:167] op_sel_hi:[1,0]
	v_pk_mul_f32 v[70:71], v[70:71], v[166:167] op_sel_hi:[1,0]
	v_add_u32_e32 v2, 0x410, v16
	ds_write2_b32 v2, v68, v69 offset1:1
	ds_write2_b32 v2, v70, v71 offset0:2 offset1:3
	s_waitcnt vmcnt(13)
	v_mul_f32_e32 v168, 0x42800000, v168
	v_pk_mul_f32 v[72:73], v[72:73], v[168:169] op_sel_hi:[1,0]
	v_pk_mul_f32 v[74:75], v[74:75], v[168:169] op_sel_hi:[1,0]
	v_add_u32_e32 v2, 0x820, v16
	ds_write2_b32 v2, v72, v73 offset1:1
	ds_write2_b32 v2, v74, v75 offset0:2 offset1:3
	s_waitcnt vmcnt(12)
	v_mul_f32_e32 v170, 0x42800000, v170
	v_pk_mul_f32 v[76:77], v[76:77], v[170:171] op_sel_hi:[1,0]
	v_pk_mul_f32 v[78:79], v[78:79], v[170:171] op_sel_hi:[1,0]
	v_add_u32_e32 v2, 0xc30, v16
	ds_write2_b32 v2, v76, v77 offset1:1
	ds_write2_b32 v2, v78, v79 offset0:2 offset1:3
	s_waitcnt vmcnt(11)
	v_mul_f32_e32 v172, 0x42800000, v172
	v_pk_mul_f32 v[80:81], v[80:81], v[172:173] op_sel_hi:[1,0]
	v_pk_mul_f32 v[82:83], v[82:83], v[172:173] op_sel_hi:[1,0]
	v_add_u32_e32 v2, 0x1040, v16
	ds_write2_b32 v2, v80, v81 offset1:1
	ds_write2_b32 v2, v82, v83 offset0:2 offset1:3
	s_waitcnt vmcnt(10)
	v_mul_f32_e32 v174, 0x42800000, v174
	v_pk_mul_f32 v[84:85], v[84:85], v[174:175] op_sel_hi:[1,0]
	v_pk_mul_f32 v[86:87], v[86:87], v[174:175] op_sel_hi:[1,0]
	v_add_u32_e32 v2, 0x1450, v16
	ds_write2_b32 v2, v84, v85 offset1:1
	ds_write2_b32 v2, v86, v87 offset0:2 offset1:3
	s_waitcnt vmcnt(9)
	v_mul_f32_e32 v176, 0x42800000, v176
	v_pk_mul_f32 v[88:89], v[88:89], v[176:177] op_sel_hi:[1,0]
	v_pk_mul_f32 v[90:91], v[90:91], v[176:177] op_sel_hi:[1,0]
	v_add_u32_e32 v2, 0x1860, v16
	ds_write2_b32 v2, v88, v89 offset1:1
	ds_write2_b32 v2, v90, v91 offset0:2 offset1:3
	s_waitcnt vmcnt(8)
	v_mul_f32_e32 v178, 0x42800000, v178
	v_pk_mul_f32 v[92:93], v[92:93], v[178:179] op_sel_hi:[1,0]
	v_pk_mul_f32 v[94:95], v[94:95], v[178:179] op_sel_hi:[1,0]
	v_add_u32_e32 v2, 0x1c70, v16
	ds_write2_b32 v2, v92, v93 offset1:1
	ds_write2_b32 v2, v94, v95 offset0:2 offset1:3
	s_waitcnt vmcnt(7)
	v_mul_f32_e32 v180, 0x42800000, v180
	v_pk_mul_f32 v[96:97], v[96:97], v[180:181] op_sel_hi:[1,0]
	v_pk_mul_f32 v[98:99], v[98:99], v[180:181] op_sel_hi:[1,0]
	v_add_u32_e32 v2, 0x2080, v16
	ds_write2_b32 v2, v96, v97 offset1:1
	ds_write2_b32 v2, v98, v99 offset0:2 offset1:3
	s_waitcnt vmcnt(6)
	v_mul_f32_e32 v182, 0x42800000, v182
	v_pk_mul_f32 v[100:101], v[100:101], v[182:183] op_sel_hi:[1,0]
	v_pk_mul_f32 v[102:103], v[102:103], v[182:183] op_sel_hi:[1,0]
	v_add_u32_e32 v2, 0x2490, v16
	ds_write2_b32 v2, v100, v101 offset1:1
	ds_write2_b32 v2, v102, v103 offset0:2 offset1:3
	s_waitcnt vmcnt(5)
	v_mul_f32_e32 v184, 0x42800000, v184
	v_pk_mul_f32 v[104:105], v[104:105], v[184:185] op_sel_hi:[1,0]
	v_pk_mul_f32 v[106:107], v[106:107], v[184:185] op_sel_hi:[1,0]
	v_add_u32_e32 v2, 0x28a0, v16
	ds_write2_b32 v2, v104, v105 offset1:1
	ds_write2_b32 v2, v106, v107 offset0:2 offset1:3
	s_waitcnt vmcnt(4)
	v_mul_f32_e32 v186, 0x42800000, v186
	v_pk_mul_f32 v[108:109], v[108:109], v[186:187] op_sel_hi:[1,0]
	v_pk_mul_f32 v[110:111], v[110:111], v[186:187] op_sel_hi:[1,0]
	v_add_u32_e32 v2, 0x2cb0, v16
	ds_write2_b32 v2, v108, v109 offset1:1
	ds_write2_b32 v2, v110, v111 offset0:2 offset1:3
	s_waitcnt vmcnt(3)
	v_mul_f32_e32 v188, 0x42800000, v188
	v_pk_mul_f32 v[112:113], v[112:113], v[188:189] op_sel_hi:[1,0]
	v_pk_mul_f32 v[114:115], v[114:115], v[188:189] op_sel_hi:[1,0]
	v_add_u32_e32 v2, 0x30c0, v16
	ds_write2_b32 v2, v112, v113 offset1:1
	ds_write2_b32 v2, v114, v115 offset0:2 offset1:3
	s_waitcnt vmcnt(2)
	v_mul_f32_e32 v190, 0x42800000, v190
	v_pk_mul_f32 v[116:117], v[116:117], v[190:191] op_sel_hi:[1,0]
	v_pk_mul_f32 v[118:119], v[118:119], v[190:191] op_sel_hi:[1,0]
	v_add_u32_e32 v2, 0x34d0, v16
	ds_write2_b32 v2, v116, v117 offset1:1
	ds_write2_b32 v2, v118, v119 offset0:2 offset1:3
	s_waitcnt vmcnt(1)
	v_mul_f32_e32 v192, 0x42800000, v192
	v_pk_mul_f32 v[120:121], v[120:121], v[192:193] op_sel_hi:[1,0]
	v_pk_mul_f32 v[122:123], v[122:123], v[192:193] op_sel_hi:[1,0]
	v_add_u32_e32 v2, 0x38e0, v16
	ds_write2_b32 v2, v120, v121 offset1:1
	ds_write2_b32 v2, v122, v123 offset0:2 offset1:3
	s_waitcnt vmcnt(0)
	v_mul_f32_e32 v194, 0x42800000, v194
	v_pk_mul_f32 v[124:125], v[124:125], v[194:195] op_sel_hi:[1,0]
	v_pk_mul_f32 v[126:127], v[126:127], v[194:195] op_sel_hi:[1,0]
	v_add_u32_e32 v2, 0x3cf0, v16
	ds_write2_b32 v2, v124, v125 offset1:1
	ds_write2_b32 v2, v126, v127 offset0:2 offset1:3
